# speedup vs baseline: 1.0605x; 1.0343x over previous
_Z15qkv_proj_kernelPKDF16_S0_PKfS2_S2_PDF16_S3_S3_:
	s_lshr_b32 s4, s2, 2
	s_and_b32 s3, s2, 7
	s_and_b32 s22, s4, 8
	s_or_b32 s4, s22, s3
	v_readfirstlane_b32 s18, v0
	s_ashr_i32 s3, s2, 6
	s_lshl_b32 s21, s4, 8
	s_bfe_u32 s20, s2, 0x20003
	v_and_b32_e32 v1, 63, v0
	s_cmpk_lt_u32 s18, 0x200
	s_mulk_i32 s20, 0xc0
	s_cbranch_scc1 .LBB1_30
	s_load_dwordx4 s[4:7], s[0:1], 0x0
	s_sub_i32 s10, 2, s3
	s_lshr_b32 s12, s18, 6
	s_add_i32 s12, s12, -8
	s_mul_i32 s13, s10, 0x600000
	s_mul_hi_i32 s14, s10, 0x600000
	s_mul_i32 s15, s10, 0x120000
	s_waitcnt lgkmcnt(0)
	s_add_u32 s4, s4, s13
	s_addc_u32 s5, s5, s14
	s_add_u32 s6, s6, s15
	s_addc_u32 s7, s7, 0
	v_lshrrev_b32_e32 v2, 2, v1
	v_lshrrev_b32_e32 v3, 4, v1
	v_xor_b32_e32 v3, v3, v1
	v_and_b32_e32 v3, 3, v3
	v_lshlrev_b32_e32 v3, 4, v3
	s_mul_i32 s16, s12, 7
	s_add_i32 s17, s16, 0
	s_lshl_b32 s19, s17, 4
	s_add_i32 s23, s19, s20
	s_add_i32 s19, s19, s21
	s_add_i32 s19, s19, -192
	s_cmp_ge_u32 s17, 12
	s_cselect_b32 s23, s19, s23
	s_cselect_b32 s24, s4, s6
	s_cselect_b32 s25, s5, s7
	v_add_u32_e32 v4, s23, v2
	v_mul_u32_u24_e32 v4, 0x600, v4
	v_add_u32_e32 v4, v4, v3
	v_mov_b32_e32 v5, 0
	v_lshl_add_u64 v[4:5], v[4:5], 0, s[24:25]
	s_add_i32 s17, s16, 1
	s_lshl_b32 s19, s17, 4
	s_add_i32 s23, s19, s20
	s_add_i32 s19, s19, s21
	s_add_i32 s19, s19, -192
	s_cmp_ge_u32 s17, 12
	s_cselect_b32 s23, s19, s23
	s_cselect_b32 s24, s4, s6
	s_cselect_b32 s25, s5, s7
	v_add_u32_e32 v6, s23, v2
	v_mul_u32_u24_e32 v6, 0x600, v6
	v_add_u32_e32 v6, v6, v3
	v_mov_b32_e32 v7, 0
	v_lshl_add_u64 v[6:7], v[6:7], 0, s[24:25]
	s_add_i32 s17, s16, 2
	s_lshl_b32 s19, s17, 4
	s_add_i32 s23, s19, s20
	s_add_i32 s19, s19, s21
	s_add_i32 s19, s19, -192
	s_cmp_ge_u32 s17, 12
	s_cselect_b32 s23, s19, s23
	s_cselect_b32 s24, s4, s6
	s_cselect_b32 s25, s5, s7
	v_add_u32_e32 v8, s23, v2
	v_mul_u32_u24_e32 v8, 0x600, v8
	v_add_u32_e32 v8, v8, v3
	v_mov_b32_e32 v9, 0
	v_lshl_add_u64 v[8:9], v[8:9], 0, s[24:25]
	s_add_i32 s17, s16, 3
	s_lshl_b32 s19, s17, 4
	s_add_i32 s23, s19, s20
	s_add_i32 s19, s19, s21
	s_add_i32 s19, s19, -192
	s_cmp_ge_u32 s17, 12
	s_cselect_b32 s23, s19, s23
	s_cselect_b32 s24, s4, s6
	s_cselect_b32 s25, s5, s7
	v_add_u32_e32 v10, s23, v2
	v_mul_u32_u24_e32 v10, 0x600, v10
	v_add_u32_e32 v10, v10, v3
	v_mov_b32_e32 v11, 0
	v_lshl_add_u64 v[10:11], v[10:11], 0, s[24:25]
	s_add_i32 s17, s16, 4
	s_lshl_b32 s19, s17, 4
	s_add_i32 s23, s19, s20
	s_add_i32 s19, s19, s21
	s_add_i32 s19, s19, -192
	s_cmp_ge_u32 s17, 12
	s_cselect_b32 s23, s19, s23
	s_cselect_b32 s24, s4, s6
	s_cselect_b32 s25, s5, s7
	v_add_u32_e32 v12, s23, v2
	v_mul_u32_u24_e32 v12, 0x600, v12
	v_add_u32_e32 v12, v12, v3
	v_mov_b32_e32 v13, 0
	v_lshl_add_u64 v[12:13], v[12:13], 0, s[24:25]
	s_add_i32 s17, s16, 5
	s_lshl_b32 s19, s17, 4
	s_add_i32 s23, s19, s20
	s_add_i32 s19, s19, s21
	s_add_i32 s19, s19, -192
	s_cmp_ge_u32 s17, 12
	s_cselect_b32 s23, s19, s23
	s_cselect_b32 s24, s4, s6
	s_cselect_b32 s25, s5, s7
	v_add_u32_e32 v14, s23, v2
	v_mul_u32_u24_e32 v14, 0x600, v14
	v_add_u32_e32 v14, v14, v3
	v_mov_b32_e32 v15, 0
	v_lshl_add_u64 v[14:15], v[14:15], 0, s[24:25]
	s_add_i32 s17, s16, 6
	s_lshl_b32 s19, s17, 4
	s_add_i32 s23, s19, s20
	s_add_i32 s19, s19, s21
	s_add_i32 s19, s19, -192
	s_cmp_ge_u32 s17, 12
	s_cselect_b32 s23, s19, s23
	s_cselect_b32 s24, s4, s6
	s_cselect_b32 s25, s5, s7
	v_add_u32_e32 v16, s23, v2
	v_mul_u32_u24_e32 v16, 0x600, v16
	v_add_u32_e32 v16, v16, v3
	v_mov_b32_e32 v17, 0
	v_lshl_add_u64 v[16:17], v[16:17], 0, s[24:25]
	s_mul_i32 s26, s12, 0x1c00
	s_add_i32 m0, s26, 2048
	s_nop 0
	global_load_lds_dwordx4 v[4:5], off
	s_add_i32 m0, s26, 3072
	s_nop 0
	global_load_lds_dwordx4 v[6:7], off
	s_add_i32 m0, s26, 4096
	s_nop 0
	global_load_lds_dwordx4 v[8:9], off
	s_add_i32 m0, s26, 5120
	s_nop 0
	global_load_lds_dwordx4 v[10:11], off
	s_add_i32 m0, s26, 6144
	s_nop 0
	global_load_lds_dwordx4 v[12:13], off
	s_add_i32 m0, s26, 7168
	s_nop 0
	global_load_lds_dwordx4 v[14:15], off
	s_add_i32 m0, s26, 8192
	s_nop 0
	global_load_lds_dwordx4 v[16:17], off
	s_add_i32 m0, s26, 30656
	s_nop 0
	global_load_lds_dwordx4 v[4:5], off offset:64
	s_add_i32 m0, s26, 31680
	s_nop 0
	global_load_lds_dwordx4 v[6:7], off offset:64
	s_add_i32 m0, s26, 32704
	s_nop 0
	global_load_lds_dwordx4 v[8:9], off offset:64
	s_add_i32 m0, s26, 33728
	s_nop 0
	global_load_lds_dwordx4 v[10:11], off offset:64
	s_add_i32 m0, s26, 34752
	s_nop 0
	global_load_lds_dwordx4 v[12:13], off offset:64
	s_add_i32 m0, s26, 35776
	s_nop 0
	global_load_lds_dwordx4 v[14:15], off offset:64
	s_add_i32 m0, s26, 36800
	s_nop 0
	global_load_lds_dwordx4 v[16:17], off offset:64
	s_add_i32 m0, s26, 59264
	s_nop 0
	global_load_lds_dwordx4 v[4:5], off offset:128
	s_add_i32 m0, s26, 60288
	s_nop 0
	global_load_lds_dwordx4 v[6:7], off offset:128
	s_add_i32 m0, s26, 61312
	s_nop 0
	global_load_lds_dwordx4 v[8:9], off offset:128
	s_add_i32 m0, s26, 62336
	s_nop 0
	global_load_lds_dwordx4 v[10:11], off offset:128
	s_add_i32 m0, s26, 63360
	s_nop 0
	global_load_lds_dwordx4 v[12:13], off offset:128
	s_add_i32 m0, s26, 64384
	s_nop 0
	global_load_lds_dwordx4 v[14:15], off offset:128
	s_add_i32 m0, s26, 65408
	s_nop 0
	global_load_lds_dwordx4 v[16:17], off offset:128
	s_add_i32 m0, s26, 87872
	s_nop 0
	global_load_lds_dwordx4 v[4:5], off offset:192
	s_add_i32 m0, s26, 88896
	s_nop 0
	global_load_lds_dwordx4 v[6:7], off offset:192
	s_add_i32 m0, s26, 89920
	s_nop 0
	global_load_lds_dwordx4 v[8:9], off offset:192
	s_add_i32 m0, s26, 90944
	s_nop 0
	global_load_lds_dwordx4 v[10:11], off offset:192
	s_add_i32 m0, s26, 91968
	s_nop 0
	global_load_lds_dwordx4 v[12:13], off offset:192
	s_add_i32 m0, s26, 92992
	s_nop 0
	global_load_lds_dwordx4 v[14:15], off offset:192
	s_add_i32 m0, s26, 94016
	s_nop 0
	global_load_lds_dwordx4 v[16:17], off offset:192
	s_waitcnt vmcnt(21)
	s_barrier
	s_add_i32 m0, s26, 116480
	s_nop 0
	global_load_lds_dwordx4 v[4:5], off offset:256
	s_add_i32 m0, s26, 117504
	s_nop 0
	global_load_lds_dwordx4 v[6:7], off offset:256
	s_add_i32 m0, s26, 118528
	s_nop 0
	global_load_lds_dwordx4 v[8:9], off offset:256
	s_add_i32 m0, s26, 119552
	s_nop 0
	global_load_lds_dwordx4 v[10:11], off offset:256
	s_add_i32 m0, s26, 120576
	s_nop 0
	global_load_lds_dwordx4 v[12:13], off offset:256
	s_add_i32 m0, s26, 121600
	s_nop 0
	global_load_lds_dwordx4 v[14:15], off offset:256
	s_add_i32 m0, s26, 122624
	s_nop 0
	global_load_lds_dwordx4 v[16:17], off offset:256
	s_waitcnt vmcnt(21)
	s_barrier
	s_add_i32 m0, s26, 1728
	s_nop 0
	global_load_lds_dwordx4 v[4:5], off offset:320
	s_add_i32 m0, s26, 2752
	s_nop 0
	global_load_lds_dwordx4 v[6:7], off offset:320
	s_add_i32 m0, s26, 3776
	s_nop 0
	global_load_lds_dwordx4 v[8:9], off offset:320
	s_add_i32 m0, s26, 4800
	s_nop 0
	global_load_lds_dwordx4 v[10:11], off offset:320
	s_add_i32 m0, s26, 5824
	s_nop 0
	global_load_lds_dwordx4 v[12:13], off offset:320
	s_add_i32 m0, s26, 6848
	s_nop 0
	global_load_lds_dwordx4 v[14:15], off offset:320
	s_add_i32 m0, s26, 7872
	s_nop 0
	global_load_lds_dwordx4 v[16:17], off offset:320
	s_waitcnt vmcnt(21)
	s_barrier
	s_add_i32 m0, s26, 30336
	s_nop 0
	global_load_lds_dwordx4 v[4:5], off offset:384
	s_add_i32 m0, s26, 31360
	s_nop 0
	global_load_lds_dwordx4 v[6:7], off offset:384
	s_add_i32 m0, s26, 32384
	s_nop 0
	global_load_lds_dwordx4 v[8:9], off offset:384
	s_add_i32 m0, s26, 33408
	s_nop 0
	global_load_lds_dwordx4 v[10:11], off offset:384
	s_add_i32 m0, s26, 34432
	s_nop 0
	global_load_lds_dwordx4 v[12:13], off offset:384
	s_add_i32 m0, s26, 35456
	s_nop 0
	global_load_lds_dwordx4 v[14:15], off offset:384
	s_add_i32 m0, s26, 36480
	s_nop 0
	global_load_lds_dwordx4 v[16:17], off offset:384
	s_waitcnt vmcnt(21)
	s_barrier
	s_add_i32 m0, s26, 58944
	s_nop 0
	global_load_lds_dwordx4 v[4:5], off offset:448
	s_add_i32 m0, s26, 59968
	s_nop 0
	global_load_lds_dwordx4 v[6:7], off offset:448
	s_add_i32 m0, s26, 60992
	s_nop 0
	global_load_lds_dwordx4 v[8:9], off offset:448
	s_add_i32 m0, s26, 62016
	s_nop 0
	global_load_lds_dwordx4 v[10:11], off offset:448
	s_add_i32 m0, s26, 63040
	s_nop 0
	global_load_lds_dwordx4 v[12:13], off offset:448
	s_add_i32 m0, s26, 64064
	s_nop 0
	global_load_lds_dwordx4 v[14:15], off offset:448
	s_add_i32 m0, s26, 65088
	s_nop 0
	global_load_lds_dwordx4 v[16:17], off offset:448
	s_waitcnt vmcnt(21)
	s_barrier
	s_add_i32 m0, s26, 87552
	s_nop 0
	global_load_lds_dwordx4 v[4:5], off offset:512
	s_add_i32 m0, s26, 88576
	s_nop 0
	global_load_lds_dwordx4 v[6:7], off offset:512
	s_add_i32 m0, s26, 89600
	s_nop 0
	global_load_lds_dwordx4 v[8:9], off offset:512
	s_add_i32 m0, s26, 90624
	s_nop 0
	global_load_lds_dwordx4 v[10:11], off offset:512
	s_add_i32 m0, s26, 91648
	s_nop 0
	global_load_lds_dwordx4 v[12:13], off offset:512
	s_add_i32 m0, s26, 92672
	s_nop 0
	global_load_lds_dwordx4 v[14:15], off offset:512
	s_add_i32 m0, s26, 93696
	s_nop 0
	global_load_lds_dwordx4 v[16:17], off offset:512
	s_waitcnt vmcnt(21)
	s_barrier
	s_add_i32 m0, s26, 116160
	s_nop 0
	global_load_lds_dwordx4 v[4:5], off offset:576
	s_add_i32 m0, s26, 117184
	s_nop 0
	global_load_lds_dwordx4 v[6:7], off offset:576
	s_add_i32 m0, s26, 118208
	s_nop 0
	global_load_lds_dwordx4 v[8:9], off offset:576
	s_add_i32 m0, s26, 119232
	s_nop 0
	global_load_lds_dwordx4 v[10:11], off offset:576
	s_add_i32 m0, s26, 120256
	s_nop 0
	global_load_lds_dwordx4 v[12:13], off offset:576
	s_add_i32 m0, s26, 121280
	s_nop 0
	global_load_lds_dwordx4 v[14:15], off offset:576
	s_add_i32 m0, s26, 122304
	s_nop 0
	global_load_lds_dwordx4 v[16:17], off offset:576
	s_waitcnt vmcnt(21)
	s_barrier
	s_add_i32 m0, s26, 1408
	s_nop 0
	global_load_lds_dwordx4 v[4:5], off offset:640
	s_add_i32 m0, s26, 2432
	s_nop 0
	global_load_lds_dwordx4 v[6:7], off offset:640
	s_add_i32 m0, s26, 3456
	s_nop 0
	global_load_lds_dwordx4 v[8:9], off offset:640
	s_add_i32 m0, s26, 4480
	s_nop 0
	global_load_lds_dwordx4 v[10:11], off offset:640
	s_add_i32 m0, s26, 5504
	s_nop 0
	global_load_lds_dwordx4 v[12:13], off offset:640
	s_add_i32 m0, s26, 6528
	s_nop 0
	global_load_lds_dwordx4 v[14:15], off offset:640
	s_add_i32 m0, s26, 7552
	s_nop 0
	global_load_lds_dwordx4 v[16:17], off offset:640
	s_waitcnt vmcnt(21)
	s_barrier
	s_add_i32 m0, s26, 30016
	s_nop 0
	global_load_lds_dwordx4 v[4:5], off offset:704
	s_add_i32 m0, s26, 31040
	s_nop 0
	global_load_lds_dwordx4 v[6:7], off offset:704
	s_add_i32 m0, s26, 32064
	s_nop 0
	global_load_lds_dwordx4 v[8:9], off offset:704
	s_add_i32 m0, s26, 33088
	s_nop 0
	global_load_lds_dwordx4 v[10:11], off offset:704
	s_add_i32 m0, s26, 34112
	s_nop 0
	global_load_lds_dwordx4 v[12:13], off offset:704
	s_add_i32 m0, s26, 35136
	s_nop 0
	global_load_lds_dwordx4 v[14:15], off offset:704
	s_add_i32 m0, s26, 36160
	s_nop 0
	global_load_lds_dwordx4 v[16:17], off offset:704
	s_waitcnt vmcnt(21)
	s_barrier
	s_add_i32 m0, s26, 58624
	s_nop 0
	global_load_lds_dwordx4 v[4:5], off offset:768
	s_add_i32 m0, s26, 59648
	s_nop 0
	global_load_lds_dwordx4 v[6:7], off offset:768
	s_add_i32 m0, s26, 60672
	s_nop 0
	global_load_lds_dwordx4 v[8:9], off offset:768
	s_add_i32 m0, s26, 61696
	s_nop 0
	global_load_lds_dwordx4 v[10:11], off offset:768
	s_add_i32 m0, s26, 62720
	s_nop 0
	global_load_lds_dwordx4 v[12:13], off offset:768
	s_add_i32 m0, s26, 63744
	s_nop 0
	global_load_lds_dwordx4 v[14:15], off offset:768
	s_add_i32 m0, s26, 64768
	s_nop 0
	global_load_lds_dwordx4 v[16:17], off offset:768
	s_waitcnt vmcnt(21)
	s_barrier
	s_add_i32 m0, s26, 87232
	s_nop 0
	global_load_lds_dwordx4 v[4:5], off offset:832
	s_add_i32 m0, s26, 88256
	s_nop 0
	global_load_lds_dwordx4 v[6:7], off offset:832
	s_add_i32 m0, s26, 89280
	s_nop 0
	global_load_lds_dwordx4 v[8:9], off offset:832
	s_add_i32 m0, s26, 90304
	s_nop 0
	global_load_lds_dwordx4 v[10:11], off offset:832
	s_add_i32 m0, s26, 91328
	s_nop 0
	global_load_lds_dwordx4 v[12:13], off offset:832
	s_add_i32 m0, s26, 92352
	s_nop 0
	global_load_lds_dwordx4 v[14:15], off offset:832
	s_add_i32 m0, s26, 93376
	s_nop 0
	global_load_lds_dwordx4 v[16:17], off offset:832
	s_waitcnt vmcnt(21)
	s_barrier
	s_add_i32 m0, s26, 115840
	s_nop 0
	global_load_lds_dwordx4 v[4:5], off offset:896
	s_add_i32 m0, s26, 116864
	s_nop 0
	global_load_lds_dwordx4 v[6:7], off offset:896
	s_add_i32 m0, s26, 117888
	s_nop 0
	global_load_lds_dwordx4 v[8:9], off offset:896
	s_add_i32 m0, s26, 118912
	s_nop 0
	global_load_lds_dwordx4 v[10:11], off offset:896
	s_add_i32 m0, s26, 119936
	s_nop 0
	global_load_lds_dwordx4 v[12:13], off offset:896
	s_add_i32 m0, s26, 120960
	s_nop 0
	global_load_lds_dwordx4 v[14:15], off offset:896
	s_add_i32 m0, s26, 121984
	s_nop 0
	global_load_lds_dwordx4 v[16:17], off offset:896
	s_waitcnt vmcnt(21)
	s_barrier
	s_add_i32 m0, s26, 1088
	s_nop 0
	global_load_lds_dwordx4 v[4:5], off offset:960
	s_add_i32 m0, s26, 2112
	s_nop 0
	global_load_lds_dwordx4 v[6:7], off offset:960
	s_add_i32 m0, s26, 3136
	s_nop 0
	global_load_lds_dwordx4 v[8:9], off offset:960
	s_add_i32 m0, s26, 4160
	s_nop 0
	global_load_lds_dwordx4 v[10:11], off offset:960
	s_add_i32 m0, s26, 5184
	s_nop 0
	global_load_lds_dwordx4 v[12:13], off offset:960
	s_add_i32 m0, s26, 6208
	s_nop 0
	global_load_lds_dwordx4 v[14:15], off offset:960
	s_add_i32 m0, s26, 7232
	s_nop 0
	global_load_lds_dwordx4 v[16:17], off offset:960
	s_waitcnt vmcnt(21)
	s_barrier
	s_add_i32 m0, s26, 29696
	s_nop 0
	global_load_lds_dwordx4 v[4:5], off offset:1024
	s_add_i32 m0, s26, 30720
	s_nop 0
	global_load_lds_dwordx4 v[6:7], off offset:1024
	s_add_i32 m0, s26, 31744
	s_nop 0
	global_load_lds_dwordx4 v[8:9], off offset:1024
	s_add_i32 m0, s26, 32768
	s_nop 0
	global_load_lds_dwordx4 v[10:11], off offset:1024
	s_add_i32 m0, s26, 33792
	s_nop 0
	global_load_lds_dwordx4 v[12:13], off offset:1024
	s_add_i32 m0, s26, 34816
	s_nop 0
	global_load_lds_dwordx4 v[14:15], off offset:1024
	s_add_i32 m0, s26, 35840
	s_nop 0
	global_load_lds_dwordx4 v[16:17], off offset:1024
	s_waitcnt vmcnt(21)
	s_barrier
	s_add_i32 m0, s26, 58304
	s_nop 0
	global_load_lds_dwordx4 v[4:5], off offset:1088
	s_add_i32 m0, s26, 59328
	s_nop 0
	global_load_lds_dwordx4 v[6:7], off offset:1088
	s_add_i32 m0, s26, 60352
	s_nop 0
	global_load_lds_dwordx4 v[8:9], off offset:1088
	s_add_i32 m0, s26, 61376
	s_nop 0
	global_load_lds_dwordx4 v[10:11], off offset:1088
	s_add_i32 m0, s26, 62400
	s_nop 0
	global_load_lds_dwordx4 v[12:13], off offset:1088
	s_add_i32 m0, s26, 63424
	s_nop 0
	global_load_lds_dwordx4 v[14:15], off offset:1088
	s_add_i32 m0, s26, 64448
	s_nop 0
	global_load_lds_dwordx4 v[16:17], off offset:1088
	s_waitcnt vmcnt(21)
	s_barrier
	s_add_i32 m0, s26, 86912
	s_nop 0
	global_load_lds_dwordx4 v[4:5], off offset:1152
	s_add_i32 m0, s26, 87936
	s_nop 0
	global_load_lds_dwordx4 v[6:7], off offset:1152
	s_add_i32 m0, s26, 88960
	s_nop 0
	global_load_lds_dwordx4 v[8:9], off offset:1152
	s_add_i32 m0, s26, 89984
	s_nop 0
	global_load_lds_dwordx4 v[10:11], off offset:1152
	s_add_i32 m0, s26, 91008
	s_nop 0
	global_load_lds_dwordx4 v[12:13], off offset:1152
	s_add_i32 m0, s26, 92032
	s_nop 0
	global_load_lds_dwordx4 v[14:15], off offset:1152
	s_add_i32 m0, s26, 93056
	s_nop 0
	global_load_lds_dwordx4 v[16:17], off offset:1152
	s_waitcnt vmcnt(21)
	s_barrier
	s_add_i32 m0, s26, 115520
	s_nop 0
	global_load_lds_dwordx4 v[4:5], off offset:1216
	s_add_i32 m0, s26, 116544
	s_nop 0
	global_load_lds_dwordx4 v[6:7], off offset:1216
	s_add_i32 m0, s26, 117568
	s_nop 0
	global_load_lds_dwordx4 v[8:9], off offset:1216
	s_add_i32 m0, s26, 118592
	s_nop 0
	global_load_lds_dwordx4 v[10:11], off offset:1216
	s_add_i32 m0, s26, 119616
	s_nop 0
	global_load_lds_dwordx4 v[12:13], off offset:1216
	s_add_i32 m0, s26, 120640
	s_nop 0
	global_load_lds_dwordx4 v[14:15], off offset:1216
	s_add_i32 m0, s26, 121664
	s_nop 0
	global_load_lds_dwordx4 v[16:17], off offset:1216
	s_waitcnt vmcnt(21)
	s_barrier
	s_add_i32 m0, s26, 768
	s_nop 0
	global_load_lds_dwordx4 v[4:5], off offset:1280
	s_add_i32 m0, s26, 1792
	s_nop 0
	global_load_lds_dwordx4 v[6:7], off offset:1280
	s_add_i32 m0, s26, 2816
	s_nop 0
	global_load_lds_dwordx4 v[8:9], off offset:1280
	s_add_i32 m0, s26, 3840
	s_nop 0
	global_load_lds_dwordx4 v[10:11], off offset:1280
	s_add_i32 m0, s26, 4864
	s_nop 0
	global_load_lds_dwordx4 v[12:13], off offset:1280
	s_add_i32 m0, s26, 5888
	s_nop 0
	global_load_lds_dwordx4 v[14:15], off offset:1280
	s_add_i32 m0, s26, 6912
	s_nop 0
	global_load_lds_dwordx4 v[16:17], off offset:1280
	s_waitcnt vmcnt(21)
	s_barrier
	s_add_i32 m0, s26, 29376
	s_nop 0
	global_load_lds_dwordx4 v[4:5], off offset:1344
	s_add_i32 m0, s26, 30400
	s_nop 0
	global_load_lds_dwordx4 v[6:7], off offset:1344
	s_add_i32 m0, s26, 31424
	s_nop 0
	global_load_lds_dwordx4 v[8:9], off offset:1344
	s_add_i32 m0, s26, 32448
	s_nop 0
	global_load_lds_dwordx4 v[10:11], off offset:1344
	s_add_i32 m0, s26, 33472
	s_nop 0
	global_load_lds_dwordx4 v[12:13], off offset:1344
	s_add_i32 m0, s26, 34496
	s_nop 0
	global_load_lds_dwordx4 v[14:15], off offset:1344
	s_add_i32 m0, s26, 35520
	s_nop 0
	global_load_lds_dwordx4 v[16:17], off offset:1344
	s_waitcnt vmcnt(21)
	s_barrier
	s_add_i32 m0, s26, 57984
	s_nop 0
	global_load_lds_dwordx4 v[4:5], off offset:1408
	s_add_i32 m0, s26, 59008
	s_nop 0
	global_load_lds_dwordx4 v[6:7], off offset:1408
	s_add_i32 m0, s26, 60032
	s_nop 0
	global_load_lds_dwordx4 v[8:9], off offset:1408
	s_add_i32 m0, s26, 61056
	s_nop 0
	global_load_lds_dwordx4 v[10:11], off offset:1408
	s_add_i32 m0, s26, 62080
	s_nop 0
	global_load_lds_dwordx4 v[12:13], off offset:1408
	s_add_i32 m0, s26, 63104
	s_nop 0
	global_load_lds_dwordx4 v[14:15], off offset:1408
	s_add_i32 m0, s26, 64128
	s_nop 0
	global_load_lds_dwordx4 v[16:17], off offset:1408
	s_waitcnt vmcnt(21)
	s_barrier
	s_add_i32 m0, s26, 86592
	s_nop 0
	global_load_lds_dwordx4 v[4:5], off offset:1472
	s_add_i32 m0, s26, 87616
	s_nop 0
	global_load_lds_dwordx4 v[6:7], off offset:1472
	s_add_i32 m0, s26, 88640
	s_nop 0
	global_load_lds_dwordx4 v[8:9], off offset:1472
	s_add_i32 m0, s26, 89664
	s_nop 0
	global_load_lds_dwordx4 v[10:11], off offset:1472
	s_add_i32 m0, s26, 90688
	s_nop 0
	global_load_lds_dwordx4 v[12:13], off offset:1472
	s_add_i32 m0, s26, 91712
	s_nop 0
	global_load_lds_dwordx4 v[14:15], off offset:1472
	s_add_i32 m0, s26, 92736
	s_nop 0
	global_load_lds_dwordx4 v[16:17], off offset:1472
	s_waitcnt vmcnt(21)
	s_barrier
	s_waitcnt vmcnt(14)
	s_barrier
	s_waitcnt vmcnt(7)
	s_barrier
	s_waitcnt vmcnt(0)
	s_barrier
.LBB1_30:
	s_load_dwordx8 s[8:15], s[0:1], 0x10
	s_load_dwordx2 s[16:17], s[0:1], 0x30
	s_bitcmp1_b32 s18, 6
	s_cselect_b32 s24, 0x60, 0
	s_lshr_b32 s4, s18, 1
	s_and_b32 s23, s4, 0x7fffffc0
	v_lshrrev_b32_e32 v98, 5, v1
	s_cmpk_lt_u32 s18, 0x200
	v_and_b32_e32 v1, 31, v0
	v_mov_b32_e32 v2, 0
	s_cselect_b64 s[4:5], -1, 0
	s_cmpk_gt_u32 s18, 0x1ff
	v_mov_b32_e32 v3, 0
	v_mov_b32_e32 v4, 0
	v_mov_b32_e32 v5, 0
	v_mov_b32_e32 v6, 0
	v_mov_b32_e32 v7, 0
	v_mov_b32_e32 v8, 0
	v_mov_b32_e32 v9, 0
	v_mov_b32_e32 v10, 0
	v_mov_b32_e32 v11, 0
	v_mov_b32_e32 v12, 0
	v_mov_b32_e32 v13, 0
	v_mov_b32_e32 v14, 0
	v_mov_b32_e32 v15, 0
	v_mov_b32_e32 v16, 0
	v_mov_b32_e32 v17, 0
	v_mov_b32_e32 v50, 0
	v_mov_b32_e32 v51, 0
	v_mov_b32_e32 v52, 0
	v_mov_b32_e32 v53, 0
	v_mov_b32_e32 v54, 0
	v_mov_b32_e32 v55, 0
	v_mov_b32_e32 v56, 0
	v_mov_b32_e32 v57, 0
	v_mov_b32_e32 v58, 0
	v_mov_b32_e32 v59, 0
	v_mov_b32_e32 v60, 0
	v_mov_b32_e32 v61, 0
	v_mov_b32_e32 v62, 0
	v_mov_b32_e32 v63, 0
	v_mov_b32_e32 v64, 0
	v_mov_b32_e32 v65, 0
	v_mov_b32_e32 v18, 0
	v_mov_b32_e32 v19, 0
	v_mov_b32_e32 v20, 0
	v_mov_b32_e32 v21, 0
	v_mov_b32_e32 v22, 0
	v_mov_b32_e32 v23, 0
	v_mov_b32_e32 v24, 0
	v_mov_b32_e32 v25, 0
	v_mov_b32_e32 v26, 0
	v_mov_b32_e32 v27, 0
	v_mov_b32_e32 v28, 0
	v_mov_b32_e32 v29, 0
	v_mov_b32_e32 v30, 0
	v_mov_b32_e32 v31, 0
	v_mov_b32_e32 v32, 0
	v_mov_b32_e32 v33, 0
	v_mov_b32_e32 v66, 0
	v_mov_b32_e32 v67, 0
	v_mov_b32_e32 v68, 0
	v_mov_b32_e32 v69, 0
	v_mov_b32_e32 v70, 0
	v_mov_b32_e32 v71, 0
	v_mov_b32_e32 v72, 0
	v_mov_b32_e32 v73, 0
	v_mov_b32_e32 v74, 0
	v_mov_b32_e32 v75, 0
	v_mov_b32_e32 v76, 0
	v_mov_b32_e32 v77, 0
	v_mov_b32_e32 v78, 0
	v_mov_b32_e32 v79, 0
	v_mov_b32_e32 v80, 0
	v_mov_b32_e32 v81, 0
	v_mov_b32_e32 v34, 0
	v_mov_b32_e32 v35, 0
	v_mov_b32_e32 v36, 0
	v_mov_b32_e32 v37, 0
	v_mov_b32_e32 v38, 0
	v_mov_b32_e32 v39, 0
	v_mov_b32_e32 v40, 0
	v_mov_b32_e32 v41, 0
	v_mov_b32_e32 v42, 0
	v_mov_b32_e32 v43, 0
	v_mov_b32_e32 v44, 0
	v_mov_b32_e32 v45, 0
	v_mov_b32_e32 v46, 0
	v_mov_b32_e32 v47, 0
	v_mov_b32_e32 v48, 0
	v_mov_b32_e32 v49, 0
	v_mov_b32_e32 v82, 0
	v_mov_b32_e32 v83, 0
	v_mov_b32_e32 v84, 0
	v_mov_b32_e32 v85, 0
	v_mov_b32_e32 v86, 0
	v_mov_b32_e32 v87, 0
	v_mov_b32_e32 v88, 0
	v_mov_b32_e32 v89, 0
	v_mov_b32_e32 v90, 0
	v_mov_b32_e32 v91, 0
	v_mov_b32_e32 v92, 0
	v_mov_b32_e32 v93, 0
	v_mov_b32_e32 v94, 0
	v_mov_b32_e32 v95, 0
	v_mov_b32_e32 v96, 0
	v_mov_b32_e32 v97, 0
	v_or_b32_e32 v99, s24, v1
	v_or_b32_e32 v100, s23, v1
	s_cbranch_scc1 .LBB1_35
	v_bfe_u32 v109, v0, 2, 2
	v_xor_b32_e32 v110, v109, v98
	v_xor_b32_e32 v111, 2, v110
	v_lshlrev_b32_e32 v110, 4, v110
	v_lshlrev_b32_e32 v111, 4, v111
	v_lshl_add_u32 v101, v99, 6, v110
	v_lshl_add_u32 v102, v99, 6, v111
	v_lshl_add_u32 v103, v100, 6, v110
	v_lshl_add_u32 v104, v100, 6, v111
	v_add_u32_e32 v101, 0x800, v101
	v_add_u32_e32 v102, 0x800, v102
	v_add_u32_e32 v103, 0x3800, v103
	v_add_u32_e32 v104, 0x3800, v104
	v_add_u32_e32 v105, 0xe000, v101
	v_add_u32_e32 v106, 0xe000, v102
	v_add_u32_e32 v107, 0xe000, v103
	v_add_u32_e32 v108, 0xe000, v104
	v_add_u32_e32 v152, 0x1c000, v101
	v_add_u32_e32 v153, 0x1c000, v102
	v_add_u32_e32 v154, 0x1c000, v103
	v_add_u32_e32 v155, 0x1c000, v104
	s_cmp_lt_u32 s2, 64
	s_cbranch_scc1 .Lqkv_cv
	s_barrier
	ds_read_b128 v[124:127], v103
	ds_read_b128 v[112:115], v101
	ds_read_b128 v[128:131], v103 offset:2048
	ds_read_b128 v[116:119], v101 offset:2048
	ds_read_b128 v[120:123], v101 offset:4096
	s_waitcnt lgkmcnt(0)
	v_mfma_f32_32x32x16_f16 v[82:97], v[112:115], v[124:127], v[82:97]
	ds_read_b128 v[144:147], v104
	v_mfma_f32_32x32x16_f16 v[34:49], v[112:115], v[128:131], v[34:49]
	ds_read_b128 v[132:135], v102
	v_mfma_f32_32x32x16_f16 v[66:81], v[116:119], v[124:127], v[66:81]
	ds_read_b128 v[148:151], v104 offset:2048
	v_mfma_f32_32x32x16_f16 v[18:33], v[116:119], v[128:131], v[18:33]
	ds_read_b128 v[136:139], v102 offset:2048
	v_mfma_f32_32x32x16_f16 v[50:65], v[120:123], v[124:127], v[50:65]
	ds_read_b128 v[140:143], v102 offset:4096
	v_mfma_f32_32x32x16_f16 v[2:17], v[120:123], v[128:131], v[2:17]
	s_waitcnt lgkmcnt(0)
	s_barrier
	v_mfma_f32_32x32x16_f16 v[82:97], v[132:135], v[144:147], v[82:97]
	ds_read_b128 v[124:127], v103 offset:28672
	v_mfma_f32_32x32x16_f16 v[34:49], v[132:135], v[148:151], v[34:49]
	ds_read_b128 v[112:115], v101 offset:28672
	v_mfma_f32_32x32x16_f16 v[66:81], v[136:139], v[144:147], v[66:81]
	ds_read_b128 v[128:131], v103 offset:30720
	v_mfma_f32_32x32x16_f16 v[18:33], v[136:139], v[148:151], v[18:33]
	ds_read_b128 v[116:119], v101 offset:30720
	v_mfma_f32_32x32x16_f16 v[50:65], v[140:143], v[144:147], v[50:65]
	ds_read_b128 v[120:123], v101 offset:32768
	v_mfma_f32_32x32x16_f16 v[2:17], v[140:143], v[148:151], v[2:17]
	s_waitcnt lgkmcnt(0)
	v_mfma_f32_32x32x16_f16 v[82:97], v[112:115], v[124:127], v[82:97]
	ds_read_b128 v[144:147], v104 offset:28672
	v_mfma_f32_32x32x16_f16 v[34:49], v[112:115], v[128:131], v[34:49]
	ds_read_b128 v[132:135], v102 offset:28672
	v_mfma_f32_32x32x16_f16 v[66:81], v[116:119], v[124:127], v[66:81]
	ds_read_b128 v[148:151], v104 offset:30720
	v_mfma_f32_32x32x16_f16 v[18:33], v[116:119], v[128:131], v[18:33]
	ds_read_b128 v[136:139], v102 offset:30720
	v_mfma_f32_32x32x16_f16 v[50:65], v[120:123], v[124:127], v[50:65]
	ds_read_b128 v[140:143], v102 offset:32768
	v_mfma_f32_32x32x16_f16 v[2:17], v[120:123], v[128:131], v[2:17]
	s_waitcnt lgkmcnt(0)
	s_barrier
	v_mfma_f32_32x32x16_f16 v[82:97], v[132:135], v[144:147], v[82:97]
	ds_read_b128 v[124:127], v107
	v_mfma_f32_32x32x16_f16 v[34:49], v[132:135], v[148:151], v[34:49]
	ds_read_b128 v[112:115], v105
	v_mfma_f32_32x32x16_f16 v[66:81], v[136:139], v[144:147], v[66:81]
	ds_read_b128 v[128:131], v107 offset:2048
	v_mfma_f32_32x32x16_f16 v[18:33], v[136:139], v[148:151], v[18:33]
	ds_read_b128 v[116:119], v105 offset:2048
	v_mfma_f32_32x32x16_f16 v[50:65], v[140:143], v[144:147], v[50:65]
	ds_read_b128 v[120:123], v105 offset:4096
	v_mfma_f32_32x32x16_f16 v[2:17], v[140:143], v[148:151], v[2:17]
	s_waitcnt lgkmcnt(0)
	v_mfma_f32_32x32x16_f16 v[82:97], v[112:115], v[124:127], v[82:97]
	ds_read_b128 v[144:147], v108
	v_mfma_f32_32x32x16_f16 v[34:49], v[112:115], v[128:131], v[34:49]
	ds_read_b128 v[132:135], v106
	v_mfma_f32_32x32x16_f16 v[66:81], v[116:119], v[124:127], v[66:81]
	ds_read_b128 v[148:151], v108 offset:2048
	v_mfma_f32_32x32x16_f16 v[18:33], v[116:119], v[128:131], v[18:33]
	ds_read_b128 v[136:139], v106 offset:2048
	v_mfma_f32_32x32x16_f16 v[50:65], v[120:123], v[124:127], v[50:65]
	ds_read_b128 v[140:143], v106 offset:4096
	v_mfma_f32_32x32x16_f16 v[2:17], v[120:123], v[128:131], v[2:17]
	s_waitcnt lgkmcnt(0)
	s_barrier
	v_mfma_f32_32x32x16_f16 v[82:97], v[132:135], v[144:147], v[82:97]
	ds_read_b128 v[124:127], v107 offset:28672
	v_mfma_f32_32x32x16_f16 v[34:49], v[132:135], v[148:151], v[34:49]
	ds_read_b128 v[112:115], v105 offset:28672
	v_mfma_f32_32x32x16_f16 v[66:81], v[136:139], v[144:147], v[66:81]
	ds_read_b128 v[128:131], v107 offset:30720
	v_mfma_f32_32x32x16_f16 v[18:33], v[136:139], v[148:151], v[18:33]
	ds_read_b128 v[116:119], v105 offset:30720
	v_mfma_f32_32x32x16_f16 v[50:65], v[140:143], v[144:147], v[50:65]
	ds_read_b128 v[120:123], v105 offset:32768
	v_mfma_f32_32x32x16_f16 v[2:17], v[140:143], v[148:151], v[2:17]
	s_waitcnt lgkmcnt(0)
	v_mfma_f32_32x32x16_f16 v[82:97], v[112:115], v[124:127], v[82:97]
	ds_read_b128 v[144:147], v108 offset:28672
	v_mfma_f32_32x32x16_f16 v[34:49], v[112:115], v[128:131], v[34:49]
	ds_read_b128 v[132:135], v106 offset:28672
	v_mfma_f32_32x32x16_f16 v[66:81], v[116:119], v[124:127], v[66:81]
	ds_read_b128 v[148:151], v108 offset:30720
	v_mfma_f32_32x32x16_f16 v[18:33], v[116:119], v[128:131], v[18:33]
	ds_read_b128 v[136:139], v106 offset:30720
	v_mfma_f32_32x32x16_f16 v[50:65], v[120:123], v[124:127], v[50:65]
	ds_read_b128 v[140:143], v106 offset:32768
	v_mfma_f32_32x32x16_f16 v[2:17], v[120:123], v[128:131], v[2:17]
	s_waitcnt lgkmcnt(0)
	s_barrier
	v_mfma_f32_32x32x16_f16 v[82:97], v[132:135], v[144:147], v[82:97]
	ds_read_b128 v[124:127], v154
	v_mfma_f32_32x32x16_f16 v[34:49], v[132:135], v[148:151], v[34:49]
	ds_read_b128 v[112:115], v152
	v_mfma_f32_32x32x16_f16 v[66:81], v[136:139], v[144:147], v[66:81]
	ds_read_b128 v[128:131], v154 offset:2048
	v_mfma_f32_32x32x16_f16 v[18:33], v[136:139], v[148:151], v[18:33]
	ds_read_b128 v[116:119], v152 offset:2048
	v_mfma_f32_32x32x16_f16 v[50:65], v[140:143], v[144:147], v[50:65]
	ds_read_b128 v[120:123], v152 offset:4096
	v_mfma_f32_32x32x16_f16 v[2:17], v[140:143], v[148:151], v[2:17]
	s_waitcnt lgkmcnt(0)
	v_mfma_f32_32x32x16_f16 v[82:97], v[112:115], v[124:127], v[82:97]
	ds_read_b128 v[144:147], v155
	v_mfma_f32_32x32x16_f16 v[34:49], v[112:115], v[128:131], v[34:49]
	ds_read_b128 v[132:135], v153
	v_mfma_f32_32x32x16_f16 v[66:81], v[116:119], v[124:127], v[66:81]
	ds_read_b128 v[148:151], v155 offset:2048
	v_mfma_f32_32x32x16_f16 v[18:33], v[116:119], v[128:131], v[18:33]
	ds_read_b128 v[136:139], v153 offset:2048
	v_mfma_f32_32x32x16_f16 v[50:65], v[120:123], v[124:127], v[50:65]
	ds_read_b128 v[140:143], v153 offset:4096
	v_mfma_f32_32x32x16_f16 v[2:17], v[120:123], v[128:131], v[2:17]
	s_waitcnt lgkmcnt(0)
	s_barrier
	v_mfma_f32_32x32x16_f16 v[82:97], v[132:135], v[144:147], v[82:97]
	ds_read_b128 v[124:127], v103
	v_mfma_f32_32x32x16_f16 v[34:49], v[132:135], v[148:151], v[34:49]
	ds_read_b128 v[112:115], v101
	v_mfma_f32_32x32x16_f16 v[66:81], v[136:139], v[144:147], v[66:81]
	ds_read_b128 v[128:131], v103 offset:2048
	v_mfma_f32_32x32x16_f16 v[18:33], v[136:139], v[148:151], v[18:33]
	ds_read_b128 v[116:119], v101 offset:2048
	v_mfma_f32_32x32x16_f16 v[50:65], v[140:143], v[144:147], v[50:65]
	ds_read_b128 v[120:123], v101 offset:4096
	v_mfma_f32_32x32x16_f16 v[2:17], v[140:143], v[148:151], v[2:17]
	s_waitcnt lgkmcnt(0)
	v_mfma_f32_32x32x16_f16 v[82:97], v[112:115], v[124:127], v[82:97]
	ds_read_b128 v[144:147], v104
	v_mfma_f32_32x32x16_f16 v[34:49], v[112:115], v[128:131], v[34:49]
	ds_read_b128 v[132:135], v102
	v_mfma_f32_32x32x16_f16 v[66:81], v[116:119], v[124:127], v[66:81]
	ds_read_b128 v[148:151], v104 offset:2048
	v_mfma_f32_32x32x16_f16 v[18:33], v[116:119], v[128:131], v[18:33]
	ds_read_b128 v[136:139], v102 offset:2048
	v_mfma_f32_32x32x16_f16 v[50:65], v[120:123], v[124:127], v[50:65]
	ds_read_b128 v[140:143], v102 offset:4096
	v_mfma_f32_32x32x16_f16 v[2:17], v[120:123], v[128:131], v[2:17]
	s_waitcnt lgkmcnt(0)
	s_barrier
	v_mfma_f32_32x32x16_f16 v[82:97], v[132:135], v[144:147], v[82:97]
	ds_read_b128 v[124:127], v103 offset:28672
	v_mfma_f32_32x32x16_f16 v[34:49], v[132:135], v[148:151], v[34:49]
	ds_read_b128 v[112:115], v101 offset:28672
	v_mfma_f32_32x32x16_f16 v[66:81], v[136:139], v[144:147], v[66:81]
	ds_read_b128 v[128:131], v103 offset:30720
	v_mfma_f32_32x32x16_f16 v[18:33], v[136:139], v[148:151], v[18:33]
	ds_read_b128 v[116:119], v101 offset:30720
	v_mfma_f32_32x32x16_f16 v[50:65], v[140:143], v[144:147], v[50:65]
	ds_read_b128 v[120:123], v101 offset:32768
	v_mfma_f32_32x32x16_f16 v[2:17], v[140:143], v[148:151], v[2:17]
	s_waitcnt lgkmcnt(0)
	v_mfma_f32_32x32x16_f16 v[82:97], v[112:115], v[124:127], v[82:97]
	ds_read_b128 v[144:147], v104 offset:28672
	v_mfma_f32_32x32x16_f16 v[34:49], v[112:115], v[128:131], v[34:49]
	ds_read_b128 v[132:135], v102 offset:28672
	v_mfma_f32_32x32x16_f16 v[66:81], v[116:119], v[124:127], v[66:81]
	ds_read_b128 v[148:151], v104 offset:30720
	v_mfma_f32_32x32x16_f16 v[18:33], v[116:119], v[128:131], v[18:33]
	ds_read_b128 v[136:139], v102 offset:30720
	v_mfma_f32_32x32x16_f16 v[50:65], v[120:123], v[124:127], v[50:65]
	ds_read_b128 v[140:143], v102 offset:32768
	v_mfma_f32_32x32x16_f16 v[2:17], v[120:123], v[128:131], v[2:17]
	s_waitcnt lgkmcnt(0)
	s_barrier
	v_mfma_f32_32x32x16_f16 v[82:97], v[132:135], v[144:147], v[82:97]
	ds_read_b128 v[124:127], v107
	v_mfma_f32_32x32x16_f16 v[34:49], v[132:135], v[148:151], v[34:49]
	ds_read_b128 v[112:115], v105
	v_mfma_f32_32x32x16_f16 v[66:81], v[136:139], v[144:147], v[66:81]
	ds_read_b128 v[128:131], v107 offset:2048
	v_mfma_f32_32x32x16_f16 v[18:33], v[136:139], v[148:151], v[18:33]
	ds_read_b128 v[116:119], v105 offset:2048
	v_mfma_f32_32x32x16_f16 v[50:65], v[140:143], v[144:147], v[50:65]
	ds_read_b128 v[120:123], v105 offset:4096
	v_mfma_f32_32x32x16_f16 v[2:17], v[140:143], v[148:151], v[2:17]
	s_waitcnt lgkmcnt(0)
	v_mfma_f32_32x32x16_f16 v[82:97], v[112:115], v[124:127], v[82:97]
	ds_read_b128 v[144:147], v108
	v_mfma_f32_32x32x16_f16 v[34:49], v[112:115], v[128:131], v[34:49]
	ds_read_b128 v[132:135], v106
	v_mfma_f32_32x32x16_f16 v[66:81], v[116:119], v[124:127], v[66:81]
	ds_read_b128 v[148:151], v108 offset:2048
	v_mfma_f32_32x32x16_f16 v[18:33], v[116:119], v[128:131], v[18:33]
	ds_read_b128 v[136:139], v106 offset:2048
	v_mfma_f32_32x32x16_f16 v[50:65], v[120:123], v[124:127], v[50:65]
	ds_read_b128 v[140:143], v106 offset:4096
	v_mfma_f32_32x32x16_f16 v[2:17], v[120:123], v[128:131], v[2:17]
	s_waitcnt lgkmcnt(0)
	s_barrier
	v_mfma_f32_32x32x16_f16 v[82:97], v[132:135], v[144:147], v[82:97]
	ds_read_b128 v[124:127], v107 offset:28672
	v_mfma_f32_32x32x16_f16 v[34:49], v[132:135], v[148:151], v[34:49]
	ds_read_b128 v[112:115], v105 offset:28672
	v_mfma_f32_32x32x16_f16 v[66:81], v[136:139], v[144:147], v[66:81]
	ds_read_b128 v[128:131], v107 offset:30720
	v_mfma_f32_32x32x16_f16 v[18:33], v[136:139], v[148:151], v[18:33]
	ds_read_b128 v[116:119], v105 offset:30720
	v_mfma_f32_32x32x16_f16 v[50:65], v[140:143], v[144:147], v[50:65]
	ds_read_b128 v[120:123], v105 offset:32768
	v_mfma_f32_32x32x16_f16 v[2:17], v[140:143], v[148:151], v[2:17]
	s_waitcnt lgkmcnt(0)
	v_mfma_f32_32x32x16_f16 v[82:97], v[112:115], v[124:127], v[82:97]
	ds_read_b128 v[144:147], v108 offset:28672
	v_mfma_f32_32x32x16_f16 v[34:49], v[112:115], v[128:131], v[34:49]
	ds_read_b128 v[132:135], v106 offset:28672
	v_mfma_f32_32x32x16_f16 v[66:81], v[116:119], v[124:127], v[66:81]
	ds_read_b128 v[148:151], v108 offset:30720
	v_mfma_f32_32x32x16_f16 v[18:33], v[116:119], v[128:131], v[18:33]
	ds_read_b128 v[136:139], v106 offset:30720
	v_mfma_f32_32x32x16_f16 v[50:65], v[120:123], v[124:127], v[50:65]
	ds_read_b128 v[140:143], v106 offset:32768
	v_mfma_f32_32x32x16_f16 v[2:17], v[120:123], v[128:131], v[2:17]
	s_waitcnt lgkmcnt(0)
	s_barrier
	v_mfma_f32_32x32x16_f16 v[82:97], v[132:135], v[144:147], v[82:97]
	ds_read_b128 v[124:127], v154
	v_mfma_f32_32x32x16_f16 v[34:49], v[132:135], v[148:151], v[34:49]
	ds_read_b128 v[112:115], v152
	v_mfma_f32_32x32x16_f16 v[66:81], v[136:139], v[144:147], v[66:81]
	ds_read_b128 v[128:131], v154 offset:2048
	v_mfma_f32_32x32x16_f16 v[18:33], v[136:139], v[148:151], v[18:33]
	ds_read_b128 v[116:119], v152 offset:2048
	v_mfma_f32_32x32x16_f16 v[50:65], v[140:143], v[144:147], v[50:65]
	ds_read_b128 v[120:123], v152 offset:4096
	v_mfma_f32_32x32x16_f16 v[2:17], v[140:143], v[148:151], v[2:17]
	s_waitcnt lgkmcnt(0)
	v_mfma_f32_32x32x16_f16 v[82:97], v[112:115], v[124:127], v[82:97]
	ds_read_b128 v[144:147], v155
	v_mfma_f32_32x32x16_f16 v[34:49], v[112:115], v[128:131], v[34:49]
	ds_read_b128 v[132:135], v153
	v_mfma_f32_32x32x16_f16 v[66:81], v[116:119], v[124:127], v[66:81]
	ds_read_b128 v[148:151], v155 offset:2048
	v_mfma_f32_32x32x16_f16 v[18:33], v[116:119], v[128:131], v[18:33]
	ds_read_b128 v[136:139], v153 offset:2048
	v_mfma_f32_32x32x16_f16 v[50:65], v[120:123], v[124:127], v[50:65]
	ds_read_b128 v[140:143], v153 offset:4096
	v_mfma_f32_32x32x16_f16 v[2:17], v[120:123], v[128:131], v[2:17]
	s_waitcnt lgkmcnt(0)
	s_barrier
	v_mfma_f32_32x32x16_f16 v[82:97], v[132:135], v[144:147], v[82:97]
	ds_read_b128 v[124:127], v103
	v_mfma_f32_32x32x16_f16 v[34:49], v[132:135], v[148:151], v[34:49]
	ds_read_b128 v[112:115], v101
	v_mfma_f32_32x32x16_f16 v[66:81], v[136:139], v[144:147], v[66:81]
	ds_read_b128 v[128:131], v103 offset:2048
	v_mfma_f32_32x32x16_f16 v[18:33], v[136:139], v[148:151], v[18:33]
	ds_read_b128 v[116:119], v101 offset:2048
	v_mfma_f32_32x32x16_f16 v[50:65], v[140:143], v[144:147], v[50:65]
	ds_read_b128 v[120:123], v101 offset:4096
	v_mfma_f32_32x32x16_f16 v[2:17], v[140:143], v[148:151], v[2:17]
	s_waitcnt lgkmcnt(0)
	v_mfma_f32_32x32x16_f16 v[82:97], v[112:115], v[124:127], v[82:97]
	ds_read_b128 v[144:147], v104
	v_mfma_f32_32x32x16_f16 v[34:49], v[112:115], v[128:131], v[34:49]
	ds_read_b128 v[132:135], v102
	v_mfma_f32_32x32x16_f16 v[66:81], v[116:119], v[124:127], v[66:81]
	ds_read_b128 v[148:151], v104 offset:2048
	v_mfma_f32_32x32x16_f16 v[18:33], v[116:119], v[128:131], v[18:33]
	ds_read_b128 v[136:139], v102 offset:2048
	v_mfma_f32_32x32x16_f16 v[50:65], v[120:123], v[124:127], v[50:65]
	ds_read_b128 v[140:143], v102 offset:4096
	v_mfma_f32_32x32x16_f16 v[2:17], v[120:123], v[128:131], v[2:17]
	s_waitcnt lgkmcnt(0)
	s_barrier
	v_mfma_f32_32x32x16_f16 v[82:97], v[132:135], v[144:147], v[82:97]
	ds_read_b128 v[124:127], v103 offset:28672
	v_mfma_f32_32x32x16_f16 v[34:49], v[132:135], v[148:151], v[34:49]
	ds_read_b128 v[112:115], v101 offset:28672
	v_mfma_f32_32x32x16_f16 v[66:81], v[136:139], v[144:147], v[66:81]
	ds_read_b128 v[128:131], v103 offset:30720
	v_mfma_f32_32x32x16_f16 v[18:33], v[136:139], v[148:151], v[18:33]
	ds_read_b128 v[116:119], v101 offset:30720
	v_mfma_f32_32x32x16_f16 v[50:65], v[140:143], v[144:147], v[50:65]
	ds_read_b128 v[120:123], v101 offset:32768
	v_mfma_f32_32x32x16_f16 v[2:17], v[140:143], v[148:151], v[2:17]
	s_waitcnt lgkmcnt(0)
	v_mfma_f32_32x32x16_f16 v[82:97], v[112:115], v[124:127], v[82:97]
	ds_read_b128 v[144:147], v104 offset:28672
	v_mfma_f32_32x32x16_f16 v[34:49], v[112:115], v[128:131], v[34:49]
	ds_read_b128 v[132:135], v102 offset:28672
	v_mfma_f32_32x32x16_f16 v[66:81], v[116:119], v[124:127], v[66:81]
	ds_read_b128 v[148:151], v104 offset:30720
	v_mfma_f32_32x32x16_f16 v[18:33], v[116:119], v[128:131], v[18:33]
	ds_read_b128 v[136:139], v102 offset:30720
	v_mfma_f32_32x32x16_f16 v[50:65], v[120:123], v[124:127], v[50:65]
	ds_read_b128 v[140:143], v102 offset:32768
	v_mfma_f32_32x32x16_f16 v[2:17], v[120:123], v[128:131], v[2:17]
	s_waitcnt lgkmcnt(0)
	s_barrier
	v_mfma_f32_32x32x16_f16 v[82:97], v[132:135], v[144:147], v[82:97]
	ds_read_b128 v[124:127], v107
	v_mfma_f32_32x32x16_f16 v[34:49], v[132:135], v[148:151], v[34:49]
	ds_read_b128 v[112:115], v105
	v_mfma_f32_32x32x16_f16 v[66:81], v[136:139], v[144:147], v[66:81]
	ds_read_b128 v[128:131], v107 offset:2048
	v_mfma_f32_32x32x16_f16 v[18:33], v[136:139], v[148:151], v[18:33]
	ds_read_b128 v[116:119], v105 offset:2048
	v_mfma_f32_32x32x16_f16 v[50:65], v[140:143], v[144:147], v[50:65]
	ds_read_b128 v[120:123], v105 offset:4096
	v_mfma_f32_32x32x16_f16 v[2:17], v[140:143], v[148:151], v[2:17]
	s_waitcnt lgkmcnt(0)
	v_mfma_f32_32x32x16_f16 v[82:97], v[112:115], v[124:127], v[82:97]
	ds_read_b128 v[144:147], v108
	v_mfma_f32_32x32x16_f16 v[34:49], v[112:115], v[128:131], v[34:49]
	ds_read_b128 v[132:135], v106
	v_mfma_f32_32x32x16_f16 v[66:81], v[116:119], v[124:127], v[66:81]
	ds_read_b128 v[148:151], v108 offset:2048
	v_mfma_f32_32x32x16_f16 v[18:33], v[116:119], v[128:131], v[18:33]
	ds_read_b128 v[136:139], v106 offset:2048
	v_mfma_f32_32x32x16_f16 v[50:65], v[120:123], v[124:127], v[50:65]
	ds_read_b128 v[140:143], v106 offset:4096
	v_mfma_f32_32x32x16_f16 v[2:17], v[120:123], v[128:131], v[2:17]
	s_waitcnt lgkmcnt(0)
	s_barrier
	v_mfma_f32_32x32x16_f16 v[82:97], v[132:135], v[144:147], v[82:97]
	ds_read_b128 v[124:127], v107 offset:28672
	v_mfma_f32_32x32x16_f16 v[34:49], v[132:135], v[148:151], v[34:49]
	ds_read_b128 v[112:115], v105 offset:28672
	v_mfma_f32_32x32x16_f16 v[66:81], v[136:139], v[144:147], v[66:81]
	ds_read_b128 v[128:131], v107 offset:30720
	v_mfma_f32_32x32x16_f16 v[18:33], v[136:139], v[148:151], v[18:33]
	ds_read_b128 v[116:119], v105 offset:30720
	v_mfma_f32_32x32x16_f16 v[50:65], v[140:143], v[144:147], v[50:65]
	ds_read_b128 v[120:123], v105 offset:32768
	v_mfma_f32_32x32x16_f16 v[2:17], v[140:143], v[148:151], v[2:17]
	s_waitcnt lgkmcnt(0)
	v_mfma_f32_32x32x16_f16 v[82:97], v[112:115], v[124:127], v[82:97]
	ds_read_b128 v[144:147], v108 offset:28672
	v_mfma_f32_32x32x16_f16 v[34:49], v[112:115], v[128:131], v[34:49]
	ds_read_b128 v[132:135], v106 offset:28672
	v_mfma_f32_32x32x16_f16 v[66:81], v[116:119], v[124:127], v[66:81]
	ds_read_b128 v[148:151], v108 offset:30720
	v_mfma_f32_32x32x16_f16 v[18:33], v[116:119], v[128:131], v[18:33]
	ds_read_b128 v[136:139], v106 offset:30720
	v_mfma_f32_32x32x16_f16 v[50:65], v[120:123], v[124:127], v[50:65]
	ds_read_b128 v[140:143], v106 offset:32768
	v_mfma_f32_32x32x16_f16 v[2:17], v[120:123], v[128:131], v[2:17]
	s_waitcnt lgkmcnt(0)
	s_barrier
	v_mfma_f32_32x32x16_f16 v[82:97], v[132:135], v[144:147], v[82:97]
	ds_read_b128 v[124:127], v154
	v_mfma_f32_32x32x16_f16 v[34:49], v[132:135], v[148:151], v[34:49]
	ds_read_b128 v[112:115], v152
	v_mfma_f32_32x32x16_f16 v[66:81], v[136:139], v[144:147], v[66:81]
	ds_read_b128 v[128:131], v154 offset:2048
	v_mfma_f32_32x32x16_f16 v[18:33], v[136:139], v[148:151], v[18:33]
	ds_read_b128 v[116:119], v152 offset:2048
	v_mfma_f32_32x32x16_f16 v[50:65], v[140:143], v[144:147], v[50:65]
	ds_read_b128 v[120:123], v152 offset:4096
	v_mfma_f32_32x32x16_f16 v[2:17], v[140:143], v[148:151], v[2:17]
	s_waitcnt lgkmcnt(0)
	v_mfma_f32_32x32x16_f16 v[82:97], v[112:115], v[124:127], v[82:97]
	ds_read_b128 v[144:147], v155
	v_mfma_f32_32x32x16_f16 v[34:49], v[112:115], v[128:131], v[34:49]
	ds_read_b128 v[132:135], v153
	v_mfma_f32_32x32x16_f16 v[66:81], v[116:119], v[124:127], v[66:81]
	ds_read_b128 v[148:151], v155 offset:2048
	v_mfma_f32_32x32x16_f16 v[18:33], v[116:119], v[128:131], v[18:33]
	ds_read_b128 v[136:139], v153 offset:2048
	v_mfma_f32_32x32x16_f16 v[50:65], v[120:123], v[124:127], v[50:65]
	ds_read_b128 v[140:143], v153 offset:4096
	v_mfma_f32_32x32x16_f16 v[2:17], v[120:123], v[128:131], v[2:17]
	s_waitcnt lgkmcnt(0)
	s_barrier
	v_mfma_f32_32x32x16_f16 v[82:97], v[132:135], v[144:147], v[82:97]
	ds_read_b128 v[124:127], v103
	v_mfma_f32_32x32x16_f16 v[34:49], v[132:135], v[148:151], v[34:49]
	ds_read_b128 v[112:115], v101
	v_mfma_f32_32x32x16_f16 v[66:81], v[136:139], v[144:147], v[66:81]
	ds_read_b128 v[128:131], v103 offset:2048
	v_mfma_f32_32x32x16_f16 v[18:33], v[136:139], v[148:151], v[18:33]
	ds_read_b128 v[116:119], v101 offset:2048
	v_mfma_f32_32x32x16_f16 v[50:65], v[140:143], v[144:147], v[50:65]
	ds_read_b128 v[120:123], v101 offset:4096
	v_mfma_f32_32x32x16_f16 v[2:17], v[140:143], v[148:151], v[2:17]
	s_waitcnt lgkmcnt(0)
	v_mfma_f32_32x32x16_f16 v[82:97], v[112:115], v[124:127], v[82:97]
	ds_read_b128 v[144:147], v104
	v_mfma_f32_32x32x16_f16 v[34:49], v[112:115], v[128:131], v[34:49]
	ds_read_b128 v[132:135], v102
	v_mfma_f32_32x32x16_f16 v[66:81], v[116:119], v[124:127], v[66:81]
	ds_read_b128 v[148:151], v104 offset:2048
	v_mfma_f32_32x32x16_f16 v[18:33], v[116:119], v[128:131], v[18:33]
	ds_read_b128 v[136:139], v102 offset:2048
	v_mfma_f32_32x32x16_f16 v[50:65], v[120:123], v[124:127], v[50:65]
	ds_read_b128 v[140:143], v102 offset:4096
	v_mfma_f32_32x32x16_f16 v[2:17], v[120:123], v[128:131], v[2:17]
	s_waitcnt lgkmcnt(0)
	s_barrier
	v_mfma_f32_32x32x16_f16 v[82:97], v[132:135], v[144:147], v[82:97]
	ds_read_b128 v[124:127], v103 offset:28672
	v_mfma_f32_32x32x16_f16 v[34:49], v[132:135], v[148:151], v[34:49]
	ds_read_b128 v[112:115], v101 offset:28672
	v_mfma_f32_32x32x16_f16 v[66:81], v[136:139], v[144:147], v[66:81]
	ds_read_b128 v[128:131], v103 offset:30720
	v_mfma_f32_32x32x16_f16 v[18:33], v[136:139], v[148:151], v[18:33]
	ds_read_b128 v[116:119], v101 offset:30720
	v_mfma_f32_32x32x16_f16 v[50:65], v[140:143], v[144:147], v[50:65]
	ds_read_b128 v[120:123], v101 offset:32768
	v_mfma_f32_32x32x16_f16 v[2:17], v[140:143], v[148:151], v[2:17]
	s_waitcnt lgkmcnt(0)
	v_mfma_f32_32x32x16_f16 v[82:97], v[112:115], v[124:127], v[82:97]
	ds_read_b128 v[144:147], v104 offset:28672
	v_mfma_f32_32x32x16_f16 v[34:49], v[112:115], v[128:131], v[34:49]
	ds_read_b128 v[132:135], v102 offset:28672
	v_mfma_f32_32x32x16_f16 v[66:81], v[116:119], v[124:127], v[66:81]
	ds_read_b128 v[148:151], v104 offset:30720
	v_mfma_f32_32x32x16_f16 v[18:33], v[116:119], v[128:131], v[18:33]
	ds_read_b128 v[136:139], v102 offset:30720
	v_mfma_f32_32x32x16_f16 v[50:65], v[120:123], v[124:127], v[50:65]
	ds_read_b128 v[140:143], v102 offset:32768
	v_mfma_f32_32x32x16_f16 v[2:17], v[120:123], v[128:131], v[2:17]
	s_waitcnt lgkmcnt(0)
	s_barrier
	v_mfma_f32_32x32x16_f16 v[82:97], v[132:135], v[144:147], v[82:97]
	ds_read_b128 v[124:127], v107
	v_mfma_f32_32x32x16_f16 v[34:49], v[132:135], v[148:151], v[34:49]
	ds_read_b128 v[112:115], v105
	v_mfma_f32_32x32x16_f16 v[66:81], v[136:139], v[144:147], v[66:81]
	ds_read_b128 v[128:131], v107 offset:2048
	v_mfma_f32_32x32x16_f16 v[18:33], v[136:139], v[148:151], v[18:33]
	ds_read_b128 v[116:119], v105 offset:2048
	v_mfma_f32_32x32x16_f16 v[50:65], v[140:143], v[144:147], v[50:65]
	ds_read_b128 v[120:123], v105 offset:4096
	v_mfma_f32_32x32x16_f16 v[2:17], v[140:143], v[148:151], v[2:17]
	s_waitcnt lgkmcnt(0)
	v_mfma_f32_32x32x16_f16 v[82:97], v[112:115], v[124:127], v[82:97]
	ds_read_b128 v[144:147], v108
	v_mfma_f32_32x32x16_f16 v[34:49], v[112:115], v[128:131], v[34:49]
	ds_read_b128 v[132:135], v106
	v_mfma_f32_32x32x16_f16 v[66:81], v[116:119], v[124:127], v[66:81]
	ds_read_b128 v[148:151], v108 offset:2048
	v_mfma_f32_32x32x16_f16 v[18:33], v[116:119], v[128:131], v[18:33]
	ds_read_b128 v[136:139], v106 offset:2048
	v_mfma_f32_32x32x16_f16 v[50:65], v[120:123], v[124:127], v[50:65]
	ds_read_b128 v[140:143], v106 offset:4096
	v_mfma_f32_32x32x16_f16 v[2:17], v[120:123], v[128:131], v[2:17]
	s_waitcnt lgkmcnt(0)
	s_barrier
	v_mfma_f32_32x32x16_f16 v[82:97], v[132:135], v[144:147], v[82:97]
	ds_read_b128 v[124:127], v107 offset:28672
	v_mfma_f32_32x32x16_f16 v[34:49], v[132:135], v[148:151], v[34:49]
	ds_read_b128 v[112:115], v105 offset:28672
	v_mfma_f32_32x32x16_f16 v[66:81], v[136:139], v[144:147], v[66:81]
	ds_read_b128 v[128:131], v107 offset:30720
	v_mfma_f32_32x32x16_f16 v[18:33], v[136:139], v[148:151], v[18:33]
	ds_read_b128 v[116:119], v105 offset:30720
	v_mfma_f32_32x32x16_f16 v[50:65], v[140:143], v[144:147], v[50:65]
	ds_read_b128 v[120:123], v105 offset:32768
	v_mfma_f32_32x32x16_f16 v[2:17], v[140:143], v[148:151], v[2:17]
	s_waitcnt lgkmcnt(0)
	v_mfma_f32_32x32x16_f16 v[82:97], v[112:115], v[124:127], v[82:97]
	ds_read_b128 v[144:147], v108 offset:28672
	v_mfma_f32_32x32x16_f16 v[34:49], v[112:115], v[128:131], v[34:49]
	ds_read_b128 v[132:135], v106 offset:28672
	v_mfma_f32_32x32x16_f16 v[66:81], v[116:119], v[124:127], v[66:81]
	ds_read_b128 v[148:151], v108 offset:30720
	v_mfma_f32_32x32x16_f16 v[18:33], v[116:119], v[128:131], v[18:33]
	ds_read_b128 v[136:139], v106 offset:30720
	v_mfma_f32_32x32x16_f16 v[50:65], v[120:123], v[124:127], v[50:65]
	ds_read_b128 v[140:143], v106 offset:32768
	v_mfma_f32_32x32x16_f16 v[2:17], v[120:123], v[128:131], v[2:17]
	s_waitcnt lgkmcnt(0)
	s_barrier
	v_mfma_f32_32x32x16_f16 v[82:97], v[132:135], v[144:147], v[82:97]
	ds_read_b128 v[124:127], v154
	v_mfma_f32_32x32x16_f16 v[34:49], v[132:135], v[148:151], v[34:49]
	ds_read_b128 v[112:115], v152
	v_mfma_f32_32x32x16_f16 v[66:81], v[136:139], v[144:147], v[66:81]
	ds_read_b128 v[128:131], v154 offset:2048
	v_mfma_f32_32x32x16_f16 v[18:33], v[136:139], v[148:151], v[18:33]
	ds_read_b128 v[116:119], v152 offset:2048
	v_mfma_f32_32x32x16_f16 v[50:65], v[140:143], v[144:147], v[50:65]
	ds_read_b128 v[120:123], v152 offset:4096
	v_mfma_f32_32x32x16_f16 v[2:17], v[140:143], v[148:151], v[2:17]
	s_waitcnt lgkmcnt(0)
	v_mfma_f32_32x32x16_f16 v[82:97], v[112:115], v[124:127], v[82:97]
	ds_read_b128 v[144:147], v155
	v_mfma_f32_32x32x16_f16 v[34:49], v[112:115], v[128:131], v[34:49]
	ds_read_b128 v[132:135], v153
	v_mfma_f32_32x32x16_f16 v[66:81], v[116:119], v[124:127], v[66:81]
	ds_read_b128 v[148:151], v155 offset:2048
	v_mfma_f32_32x32x16_f16 v[18:33], v[116:119], v[128:131], v[18:33]
	ds_read_b128 v[136:139], v153 offset:2048
	v_mfma_f32_32x32x16_f16 v[50:65], v[120:123], v[124:127], v[50:65]
	ds_read_b128 v[140:143], v153 offset:4096
	v_mfma_f32_32x32x16_f16 v[2:17], v[120:123], v[128:131], v[2:17]
	s_waitcnt lgkmcnt(0)
	s_barrier
	v_mfma_f32_32x32x16_f16 v[82:97], v[132:135], v[144:147], v[82:97]
	ds_read_b128 v[124:127], v103
	v_mfma_f32_32x32x16_f16 v[34:49], v[132:135], v[148:151], v[34:49]
	ds_read_b128 v[112:115], v101
	v_mfma_f32_32x32x16_f16 v[66:81], v[136:139], v[144:147], v[66:81]
	ds_read_b128 v[128:131], v103 offset:2048
	v_mfma_f32_32x32x16_f16 v[18:33], v[136:139], v[148:151], v[18:33]
	ds_read_b128 v[116:119], v101 offset:2048
	v_mfma_f32_32x32x16_f16 v[50:65], v[140:143], v[144:147], v[50:65]
	ds_read_b128 v[120:123], v101 offset:4096
	v_mfma_f32_32x32x16_f16 v[2:17], v[140:143], v[148:151], v[2:17]
	s_waitcnt lgkmcnt(0)
	v_mfma_f32_32x32x16_f16 v[82:97], v[112:115], v[124:127], v[82:97]
	ds_read_b128 v[144:147], v104
	v_mfma_f32_32x32x16_f16 v[34:49], v[112:115], v[128:131], v[34:49]
	ds_read_b128 v[132:135], v102
	v_mfma_f32_32x32x16_f16 v[66:81], v[116:119], v[124:127], v[66:81]
	ds_read_b128 v[148:151], v104 offset:2048
	v_mfma_f32_32x32x16_f16 v[18:33], v[116:119], v[128:131], v[18:33]
	ds_read_b128 v[136:139], v102 offset:2048
	v_mfma_f32_32x32x16_f16 v[50:65], v[120:123], v[124:127], v[50:65]
	ds_read_b128 v[140:143], v102 offset:4096
	v_mfma_f32_32x32x16_f16 v[2:17], v[120:123], v[128:131], v[2:17]
	s_waitcnt lgkmcnt(0)
	s_barrier
	v_mfma_f32_32x32x16_f16 v[82:97], v[132:135], v[144:147], v[82:97]
	ds_read_b128 v[124:127], v103 offset:28672
	v_mfma_f32_32x32x16_f16 v[34:49], v[132:135], v[148:151], v[34:49]
	ds_read_b128 v[112:115], v101 offset:28672
	v_mfma_f32_32x32x16_f16 v[66:81], v[136:139], v[144:147], v[66:81]
	ds_read_b128 v[128:131], v103 offset:30720
	v_mfma_f32_32x32x16_f16 v[18:33], v[136:139], v[148:151], v[18:33]
	ds_read_b128 v[116:119], v101 offset:30720
	v_mfma_f32_32x32x16_f16 v[50:65], v[140:143], v[144:147], v[50:65]
	ds_read_b128 v[120:123], v101 offset:32768
	v_mfma_f32_32x32x16_f16 v[2:17], v[140:143], v[148:151], v[2:17]
	s_waitcnt lgkmcnt(0)
	v_mfma_f32_32x32x16_f16 v[82:97], v[112:115], v[124:127], v[82:97]
	ds_read_b128 v[144:147], v104 offset:28672
	v_mfma_f32_32x32x16_f16 v[34:49], v[112:115], v[128:131], v[34:49]
	ds_read_b128 v[132:135], v102 offset:28672
	v_mfma_f32_32x32x16_f16 v[66:81], v[116:119], v[124:127], v[66:81]
	ds_read_b128 v[148:151], v104 offset:30720
	v_mfma_f32_32x32x16_f16 v[18:33], v[116:119], v[128:131], v[18:33]
	ds_read_b128 v[136:139], v102 offset:30720
	v_mfma_f32_32x32x16_f16 v[50:65], v[120:123], v[124:127], v[50:65]
	ds_read_b128 v[140:143], v102 offset:32768
	v_mfma_f32_32x32x16_f16 v[2:17], v[120:123], v[128:131], v[2:17]
	s_waitcnt lgkmcnt(0)
	s_barrier
	v_mfma_f32_32x32x16_f16 v[82:97], v[132:135], v[144:147], v[82:97]
	ds_read_b128 v[124:127], v107
	v_mfma_f32_32x32x16_f16 v[34:49], v[132:135], v[148:151], v[34:49]
	ds_read_b128 v[112:115], v105
	v_mfma_f32_32x32x16_f16 v[66:81], v[136:139], v[144:147], v[66:81]
	ds_read_b128 v[128:131], v107 offset:2048
	v_mfma_f32_32x32x16_f16 v[18:33], v[136:139], v[148:151], v[18:33]
	ds_read_b128 v[116:119], v105 offset:2048
	v_mfma_f32_32x32x16_f16 v[50:65], v[140:143], v[144:147], v[50:65]
	ds_read_b128 v[120:123], v105 offset:4096
	v_mfma_f32_32x32x16_f16 v[2:17], v[140:143], v[148:151], v[2:17]
	s_waitcnt lgkmcnt(0)
	v_mfma_f32_32x32x16_f16 v[82:97], v[112:115], v[124:127], v[82:97]
	ds_read_b128 v[144:147], v108
	v_mfma_f32_32x32x16_f16 v[34:49], v[112:115], v[128:131], v[34:49]
	ds_read_b128 v[132:135], v106
	v_mfma_f32_32x32x16_f16 v[66:81], v[116:119], v[124:127], v[66:81]
	ds_read_b128 v[148:151], v108 offset:2048
	v_mfma_f32_32x32x16_f16 v[18:33], v[116:119], v[128:131], v[18:33]
	ds_read_b128 v[136:139], v106 offset:2048
	v_mfma_f32_32x32x16_f16 v[50:65], v[120:123], v[124:127], v[50:65]
	ds_read_b128 v[140:143], v106 offset:4096
	v_mfma_f32_32x32x16_f16 v[2:17], v[120:123], v[128:131], v[2:17]
	s_waitcnt lgkmcnt(0)
	s_barrier
	v_mfma_f32_32x32x16_f16 v[82:97], v[132:135], v[144:147], v[82:97]
	ds_read_b128 v[124:127], v107 offset:28672
	v_mfma_f32_32x32x16_f16 v[34:49], v[132:135], v[148:151], v[34:49]
	ds_read_b128 v[112:115], v105 offset:28672
	v_mfma_f32_32x32x16_f16 v[66:81], v[136:139], v[144:147], v[66:81]
	ds_read_b128 v[128:131], v107 offset:30720
	v_mfma_f32_32x32x16_f16 v[18:33], v[136:139], v[148:151], v[18:33]
	ds_read_b128 v[116:119], v105 offset:30720
	v_mfma_f32_32x32x16_f16 v[50:65], v[140:143], v[144:147], v[50:65]
	ds_read_b128 v[120:123], v105 offset:32768
	v_mfma_f32_32x32x16_f16 v[2:17], v[140:143], v[148:151], v[2:17]
	s_waitcnt lgkmcnt(0)
	v_mfma_f32_32x32x16_f16 v[82:97], v[112:115], v[124:127], v[82:97]
	ds_read_b128 v[144:147], v108 offset:28672
	v_mfma_f32_32x32x16_f16 v[34:49], v[112:115], v[128:131], v[34:49]
	ds_read_b128 v[132:135], v106 offset:28672
	v_mfma_f32_32x32x16_f16 v[66:81], v[116:119], v[124:127], v[66:81]
	ds_read_b128 v[148:151], v108 offset:30720
	v_mfma_f32_32x32x16_f16 v[18:33], v[116:119], v[128:131], v[18:33]
	ds_read_b128 v[136:139], v106 offset:30720
	v_mfma_f32_32x32x16_f16 v[50:65], v[120:123], v[124:127], v[50:65]
	ds_read_b128 v[140:143], v106 offset:32768
	v_mfma_f32_32x32x16_f16 v[2:17], v[120:123], v[128:131], v[2:17]
	s_waitcnt lgkmcnt(0)
	v_mfma_f32_32x32x16_f16 v[82:97], v[132:135], v[144:147], v[82:97]
	v_mfma_f32_32x32x16_f16 v[34:49], v[132:135], v[148:151], v[34:49]
	v_mfma_f32_32x32x16_f16 v[66:81], v[136:139], v[144:147], v[66:81]
	v_mfma_f32_32x32x16_f16 v[18:33], v[136:139], v[148:151], v[18:33]
	v_mfma_f32_32x32x16_f16 v[50:65], v[140:143], v[144:147], v[50:65]
	v_mfma_f32_32x32x16_f16 v[2:17], v[140:143], v[148:151], v[2:17]
	s_branch .LBB1_35
.Lqkv_cv:
	s_barrier
	ds_read_b128 v[124:127], v103
	ds_read_b128 v[112:115], v101
	ds_read_b128 v[128:131], v103 offset:2048
	ds_read_b128 v[116:119], v101 offset:2048
	ds_read_b128 v[120:123], v101 offset:4096
	s_waitcnt lgkmcnt(0)
	v_mfma_f32_32x32x16_f16 v[82:97], v[124:127], v[112:115], v[82:97]
	ds_read_b128 v[144:147], v104
	v_mfma_f32_32x32x16_f16 v[34:49], v[128:131], v[112:115], v[34:49]
	ds_read_b128 v[132:135], v102
	v_mfma_f32_32x32x16_f16 v[66:81], v[124:127], v[116:119], v[66:81]
	ds_read_b128 v[148:151], v104 offset:2048
	v_mfma_f32_32x32x16_f16 v[18:33], v[128:131], v[116:119], v[18:33]
	ds_read_b128 v[136:139], v102 offset:2048
	v_mfma_f32_32x32x16_f16 v[50:65], v[124:127], v[120:123], v[50:65]
	ds_read_b128 v[140:143], v102 offset:4096
	v_mfma_f32_32x32x16_f16 v[2:17], v[128:131], v[120:123], v[2:17]
	s_waitcnt lgkmcnt(0)
	s_barrier
	v_mfma_f32_32x32x16_f16 v[82:97], v[144:147], v[132:135], v[82:97]
	ds_read_b128 v[124:127], v103 offset:28672
	v_mfma_f32_32x32x16_f16 v[34:49], v[148:151], v[132:135], v[34:49]
	ds_read_b128 v[112:115], v101 offset:28672
	v_mfma_f32_32x32x16_f16 v[66:81], v[144:147], v[136:139], v[66:81]
	ds_read_b128 v[128:131], v103 offset:30720
	v_mfma_f32_32x32x16_f16 v[18:33], v[148:151], v[136:139], v[18:33]
	ds_read_b128 v[116:119], v101 offset:30720
	v_mfma_f32_32x32x16_f16 v[50:65], v[144:147], v[140:143], v[50:65]
	ds_read_b128 v[120:123], v101 offset:32768
	v_mfma_f32_32x32x16_f16 v[2:17], v[148:151], v[140:143], v[2:17]
	s_waitcnt lgkmcnt(0)
	v_mfma_f32_32x32x16_f16 v[82:97], v[124:127], v[112:115], v[82:97]
	ds_read_b128 v[144:147], v104 offset:28672
	v_mfma_f32_32x32x16_f16 v[34:49], v[128:131], v[112:115], v[34:49]
	ds_read_b128 v[132:135], v102 offset:28672
	v_mfma_f32_32x32x16_f16 v[66:81], v[124:127], v[116:119], v[66:81]
	ds_read_b128 v[148:151], v104 offset:30720
	v_mfma_f32_32x32x16_f16 v[18:33], v[128:131], v[116:119], v[18:33]
	ds_read_b128 v[136:139], v102 offset:30720
	v_mfma_f32_32x32x16_f16 v[50:65], v[124:127], v[120:123], v[50:65]
	ds_read_b128 v[140:143], v102 offset:32768
	v_mfma_f32_32x32x16_f16 v[2:17], v[128:131], v[120:123], v[2:17]
	s_waitcnt lgkmcnt(0)
	s_barrier
	v_mfma_f32_32x32x16_f16 v[82:97], v[144:147], v[132:135], v[82:97]
	ds_read_b128 v[124:127], v107
	v_mfma_f32_32x32x16_f16 v[34:49], v[148:151], v[132:135], v[34:49]
	ds_read_b128 v[112:115], v105
	v_mfma_f32_32x32x16_f16 v[66:81], v[144:147], v[136:139], v[66:81]
	ds_read_b128 v[128:131], v107 offset:2048
	v_mfma_f32_32x32x16_f16 v[18:33], v[148:151], v[136:139], v[18:33]
	ds_read_b128 v[116:119], v105 offset:2048
	v_mfma_f32_32x32x16_f16 v[50:65], v[144:147], v[140:143], v[50:65]
	ds_read_b128 v[120:123], v105 offset:4096
	v_mfma_f32_32x32x16_f16 v[2:17], v[148:151], v[140:143], v[2:17]
	s_waitcnt lgkmcnt(0)
	v_mfma_f32_32x32x16_f16 v[82:97], v[124:127], v[112:115], v[82:97]
	ds_read_b128 v[144:147], v108
	v_mfma_f32_32x32x16_f16 v[34:49], v[128:131], v[112:115], v[34:49]
	ds_read_b128 v[132:135], v106
	v_mfma_f32_32x32x16_f16 v[66:81], v[124:127], v[116:119], v[66:81]
	ds_read_b128 v[148:151], v108 offset:2048
	v_mfma_f32_32x32x16_f16 v[18:33], v[128:131], v[116:119], v[18:33]
	ds_read_b128 v[136:139], v106 offset:2048
	v_mfma_f32_32x32x16_f16 v[50:65], v[124:127], v[120:123], v[50:65]
	ds_read_b128 v[140:143], v106 offset:4096
	v_mfma_f32_32x32x16_f16 v[2:17], v[128:131], v[120:123], v[2:17]
	s_waitcnt lgkmcnt(0)
	s_barrier
	v_mfma_f32_32x32x16_f16 v[82:97], v[144:147], v[132:135], v[82:97]
	ds_read_b128 v[124:127], v107 offset:28672
	v_mfma_f32_32x32x16_f16 v[34:49], v[148:151], v[132:135], v[34:49]
	ds_read_b128 v[112:115], v105 offset:28672
	v_mfma_f32_32x32x16_f16 v[66:81], v[144:147], v[136:139], v[66:81]
	ds_read_b128 v[128:131], v107 offset:30720
	v_mfma_f32_32x32x16_f16 v[18:33], v[148:151], v[136:139], v[18:33]
	ds_read_b128 v[116:119], v105 offset:30720
	v_mfma_f32_32x32x16_f16 v[50:65], v[144:147], v[140:143], v[50:65]
	ds_read_b128 v[120:123], v105 offset:32768
	v_mfma_f32_32x32x16_f16 v[2:17], v[148:151], v[140:143], v[2:17]
	s_waitcnt lgkmcnt(0)
	v_mfma_f32_32x32x16_f16 v[82:97], v[124:127], v[112:115], v[82:97]
	ds_read_b128 v[144:147], v108 offset:28672
	v_mfma_f32_32x32x16_f16 v[34:49], v[128:131], v[112:115], v[34:49]
	ds_read_b128 v[132:135], v106 offset:28672
	v_mfma_f32_32x32x16_f16 v[66:81], v[124:127], v[116:119], v[66:81]
	ds_read_b128 v[148:151], v108 offset:30720
	v_mfma_f32_32x32x16_f16 v[18:33], v[128:131], v[116:119], v[18:33]
	ds_read_b128 v[136:139], v106 offset:30720
	v_mfma_f32_32x32x16_f16 v[50:65], v[124:127], v[120:123], v[50:65]
	ds_read_b128 v[140:143], v106 offset:32768
	v_mfma_f32_32x32x16_f16 v[2:17], v[128:131], v[120:123], v[2:17]
	s_waitcnt lgkmcnt(0)
	s_barrier
	v_mfma_f32_32x32x16_f16 v[82:97], v[144:147], v[132:135], v[82:97]
	ds_read_b128 v[124:127], v154
	v_mfma_f32_32x32x16_f16 v[34:49], v[148:151], v[132:135], v[34:49]
	ds_read_b128 v[112:115], v152
	v_mfma_f32_32x32x16_f16 v[66:81], v[144:147], v[136:139], v[66:81]
	ds_read_b128 v[128:131], v154 offset:2048
	v_mfma_f32_32x32x16_f16 v[18:33], v[148:151], v[136:139], v[18:33]
	ds_read_b128 v[116:119], v152 offset:2048
	v_mfma_f32_32x32x16_f16 v[50:65], v[144:147], v[140:143], v[50:65]
	ds_read_b128 v[120:123], v152 offset:4096
	v_mfma_f32_32x32x16_f16 v[2:17], v[148:151], v[140:143], v[2:17]
	s_waitcnt lgkmcnt(0)
	v_mfma_f32_32x32x16_f16 v[82:97], v[124:127], v[112:115], v[82:97]
	ds_read_b128 v[144:147], v155
	v_mfma_f32_32x32x16_f16 v[34:49], v[128:131], v[112:115], v[34:49]
	ds_read_b128 v[132:135], v153
	v_mfma_f32_32x32x16_f16 v[66:81], v[124:127], v[116:119], v[66:81]
	ds_read_b128 v[148:151], v155 offset:2048
	v_mfma_f32_32x32x16_f16 v[18:33], v[128:131], v[116:119], v[18:33]
	ds_read_b128 v[136:139], v153 offset:2048
	v_mfma_f32_32x32x16_f16 v[50:65], v[124:127], v[120:123], v[50:65]
	ds_read_b128 v[140:143], v153 offset:4096
	v_mfma_f32_32x32x16_f16 v[2:17], v[128:131], v[120:123], v[2:17]
	s_waitcnt lgkmcnt(0)
	s_barrier
	v_mfma_f32_32x32x16_f16 v[82:97], v[144:147], v[132:135], v[82:97]
	ds_read_b128 v[124:127], v103
	v_mfma_f32_32x32x16_f16 v[34:49], v[148:151], v[132:135], v[34:49]
	ds_read_b128 v[112:115], v101
	v_mfma_f32_32x32x16_f16 v[66:81], v[144:147], v[136:139], v[66:81]
	ds_read_b128 v[128:131], v103 offset:2048
	v_mfma_f32_32x32x16_f16 v[18:33], v[148:151], v[136:139], v[18:33]
	ds_read_b128 v[116:119], v101 offset:2048
	v_mfma_f32_32x32x16_f16 v[50:65], v[144:147], v[140:143], v[50:65]
	ds_read_b128 v[120:123], v101 offset:4096
	v_mfma_f32_32x32x16_f16 v[2:17], v[148:151], v[140:143], v[2:17]
	s_waitcnt lgkmcnt(0)
	v_mfma_f32_32x32x16_f16 v[82:97], v[124:127], v[112:115], v[82:97]
	ds_read_b128 v[144:147], v104
	v_mfma_f32_32x32x16_f16 v[34:49], v[128:131], v[112:115], v[34:49]
	ds_read_b128 v[132:135], v102
	v_mfma_f32_32x32x16_f16 v[66:81], v[124:127], v[116:119], v[66:81]
	ds_read_b128 v[148:151], v104 offset:2048
	v_mfma_f32_32x32x16_f16 v[18:33], v[128:131], v[116:119], v[18:33]
	ds_read_b128 v[136:139], v102 offset:2048
	v_mfma_f32_32x32x16_f16 v[50:65], v[124:127], v[120:123], v[50:65]
	ds_read_b128 v[140:143], v102 offset:4096
	v_mfma_f32_32x32x16_f16 v[2:17], v[128:131], v[120:123], v[2:17]
	s_waitcnt lgkmcnt(0)
	s_barrier
	v_mfma_f32_32x32x16_f16 v[82:97], v[144:147], v[132:135], v[82:97]
	ds_read_b128 v[124:127], v103 offset:28672
	v_mfma_f32_32x32x16_f16 v[34:49], v[148:151], v[132:135], v[34:49]
	ds_read_b128 v[112:115], v101 offset:28672
	v_mfma_f32_32x32x16_f16 v[66:81], v[144:147], v[136:139], v[66:81]
	ds_read_b128 v[128:131], v103 offset:30720
	v_mfma_f32_32x32x16_f16 v[18:33], v[148:151], v[136:139], v[18:33]
	ds_read_b128 v[116:119], v101 offset:30720
	v_mfma_f32_32x32x16_f16 v[50:65], v[144:147], v[140:143], v[50:65]
	ds_read_b128 v[120:123], v101 offset:32768
	v_mfma_f32_32x32x16_f16 v[2:17], v[148:151], v[140:143], v[2:17]
	s_waitcnt lgkmcnt(0)
	v_mfma_f32_32x32x16_f16 v[82:97], v[124:127], v[112:115], v[82:97]
	ds_read_b128 v[144:147], v104 offset:28672
	v_mfma_f32_32x32x16_f16 v[34:49], v[128:131], v[112:115], v[34:49]
	ds_read_b128 v[132:135], v102 offset:28672
	v_mfma_f32_32x32x16_f16 v[66:81], v[124:127], v[116:119], v[66:81]
	ds_read_b128 v[148:151], v104 offset:30720
	v_mfma_f32_32x32x16_f16 v[18:33], v[128:131], v[116:119], v[18:33]
	ds_read_b128 v[136:139], v102 offset:30720
	v_mfma_f32_32x32x16_f16 v[50:65], v[124:127], v[120:123], v[50:65]
	ds_read_b128 v[140:143], v102 offset:32768
	v_mfma_f32_32x32x16_f16 v[2:17], v[128:131], v[120:123], v[2:17]
	s_waitcnt lgkmcnt(0)
	s_barrier
	v_mfma_f32_32x32x16_f16 v[82:97], v[144:147], v[132:135], v[82:97]
	ds_read_b128 v[124:127], v107
	v_mfma_f32_32x32x16_f16 v[34:49], v[148:151], v[132:135], v[34:49]
	ds_read_b128 v[112:115], v105
	v_mfma_f32_32x32x16_f16 v[66:81], v[144:147], v[136:139], v[66:81]
	ds_read_b128 v[128:131], v107 offset:2048
	v_mfma_f32_32x32x16_f16 v[18:33], v[148:151], v[136:139], v[18:33]
	ds_read_b128 v[116:119], v105 offset:2048
	v_mfma_f32_32x32x16_f16 v[50:65], v[144:147], v[140:143], v[50:65]
	ds_read_b128 v[120:123], v105 offset:4096
	v_mfma_f32_32x32x16_f16 v[2:17], v[148:151], v[140:143], v[2:17]
	s_waitcnt lgkmcnt(0)
	v_mfma_f32_32x32x16_f16 v[82:97], v[124:127], v[112:115], v[82:97]
	ds_read_b128 v[144:147], v108
	v_mfma_f32_32x32x16_f16 v[34:49], v[128:131], v[112:115], v[34:49]
	ds_read_b128 v[132:135], v106
	v_mfma_f32_32x32x16_f16 v[66:81], v[124:127], v[116:119], v[66:81]
	ds_read_b128 v[148:151], v108 offset:2048
	v_mfma_f32_32x32x16_f16 v[18:33], v[128:131], v[116:119], v[18:33]
	ds_read_b128 v[136:139], v106 offset:2048
	v_mfma_f32_32x32x16_f16 v[50:65], v[124:127], v[120:123], v[50:65]
	ds_read_b128 v[140:143], v106 offset:4096
	v_mfma_f32_32x32x16_f16 v[2:17], v[128:131], v[120:123], v[2:17]
	s_waitcnt lgkmcnt(0)
	s_barrier
	v_mfma_f32_32x32x16_f16 v[82:97], v[144:147], v[132:135], v[82:97]
	ds_read_b128 v[124:127], v107 offset:28672
	v_mfma_f32_32x32x16_f16 v[34:49], v[148:151], v[132:135], v[34:49]
	ds_read_b128 v[112:115], v105 offset:28672
	v_mfma_f32_32x32x16_f16 v[66:81], v[144:147], v[136:139], v[66:81]
	ds_read_b128 v[128:131], v107 offset:30720
	v_mfma_f32_32x32x16_f16 v[18:33], v[148:151], v[136:139], v[18:33]
	ds_read_b128 v[116:119], v105 offset:30720
	v_mfma_f32_32x32x16_f16 v[50:65], v[144:147], v[140:143], v[50:65]
	ds_read_b128 v[120:123], v105 offset:32768
	v_mfma_f32_32x32x16_f16 v[2:17], v[148:151], v[140:143], v[2:17]
	s_waitcnt lgkmcnt(0)
	v_mfma_f32_32x32x16_f16 v[82:97], v[124:127], v[112:115], v[82:97]
	ds_read_b128 v[144:147], v108 offset:28672
	v_mfma_f32_32x32x16_f16 v[34:49], v[128:131], v[112:115], v[34:49]
	ds_read_b128 v[132:135], v106 offset:28672
	v_mfma_f32_32x32x16_f16 v[66:81], v[124:127], v[116:119], v[66:81]
	ds_read_b128 v[148:151], v108 offset:30720
	v_mfma_f32_32x32x16_f16 v[18:33], v[128:131], v[116:119], v[18:33]
	ds_read_b128 v[136:139], v106 offset:30720
	v_mfma_f32_32x32x16_f16 v[50:65], v[124:127], v[120:123], v[50:65]
	ds_read_b128 v[140:143], v106 offset:32768
	v_mfma_f32_32x32x16_f16 v[2:17], v[128:131], v[120:123], v[2:17]
	s_waitcnt lgkmcnt(0)
	s_barrier
	v_mfma_f32_32x32x16_f16 v[82:97], v[144:147], v[132:135], v[82:97]
	ds_read_b128 v[124:127], v154
	v_mfma_f32_32x32x16_f16 v[34:49], v[148:151], v[132:135], v[34:49]
	ds_read_b128 v[112:115], v152
	v_mfma_f32_32x32x16_f16 v[66:81], v[144:147], v[136:139], v[66:81]
	ds_read_b128 v[128:131], v154 offset:2048
	v_mfma_f32_32x32x16_f16 v[18:33], v[148:151], v[136:139], v[18:33]
	ds_read_b128 v[116:119], v152 offset:2048
	v_mfma_f32_32x32x16_f16 v[50:65], v[144:147], v[140:143], v[50:65]
	ds_read_b128 v[120:123], v152 offset:4096
	v_mfma_f32_32x32x16_f16 v[2:17], v[148:151], v[140:143], v[2:17]
	s_waitcnt lgkmcnt(0)
	v_mfma_f32_32x32x16_f16 v[82:97], v[124:127], v[112:115], v[82:97]
	ds_read_b128 v[144:147], v155
	v_mfma_f32_32x32x16_f16 v[34:49], v[128:131], v[112:115], v[34:49]
	ds_read_b128 v[132:135], v153
	v_mfma_f32_32x32x16_f16 v[66:81], v[124:127], v[116:119], v[66:81]
	ds_read_b128 v[148:151], v155 offset:2048
	v_mfma_f32_32x32x16_f16 v[18:33], v[128:131], v[116:119], v[18:33]
	ds_read_b128 v[136:139], v153 offset:2048
	v_mfma_f32_32x32x16_f16 v[50:65], v[124:127], v[120:123], v[50:65]
	ds_read_b128 v[140:143], v153 offset:4096
	v_mfma_f32_32x32x16_f16 v[2:17], v[128:131], v[120:123], v[2:17]
	s_waitcnt lgkmcnt(0)
	s_barrier
	v_mfma_f32_32x32x16_f16 v[82:97], v[144:147], v[132:135], v[82:97]
	ds_read_b128 v[124:127], v103
	v_mfma_f32_32x32x16_f16 v[34:49], v[148:151], v[132:135], v[34:49]
	ds_read_b128 v[112:115], v101
	v_mfma_f32_32x32x16_f16 v[66:81], v[144:147], v[136:139], v[66:81]
	ds_read_b128 v[128:131], v103 offset:2048
	v_mfma_f32_32x32x16_f16 v[18:33], v[148:151], v[136:139], v[18:33]
	ds_read_b128 v[116:119], v101 offset:2048
	v_mfma_f32_32x32x16_f16 v[50:65], v[144:147], v[140:143], v[50:65]
	ds_read_b128 v[120:123], v101 offset:4096
	v_mfma_f32_32x32x16_f16 v[2:17], v[148:151], v[140:143], v[2:17]
	s_waitcnt lgkmcnt(0)
	v_mfma_f32_32x32x16_f16 v[82:97], v[124:127], v[112:115], v[82:97]
	ds_read_b128 v[144:147], v104
	v_mfma_f32_32x32x16_f16 v[34:49], v[128:131], v[112:115], v[34:49]
	ds_read_b128 v[132:135], v102
	v_mfma_f32_32x32x16_f16 v[66:81], v[124:127], v[116:119], v[66:81]
	ds_read_b128 v[148:151], v104 offset:2048
	v_mfma_f32_32x32x16_f16 v[18:33], v[128:131], v[116:119], v[18:33]
	ds_read_b128 v[136:139], v102 offset:2048
	v_mfma_f32_32x32x16_f16 v[50:65], v[124:127], v[120:123], v[50:65]
	ds_read_b128 v[140:143], v102 offset:4096
	v_mfma_f32_32x32x16_f16 v[2:17], v[128:131], v[120:123], v[2:17]
	s_waitcnt lgkmcnt(0)
	s_barrier
	v_mfma_f32_32x32x16_f16 v[82:97], v[144:147], v[132:135], v[82:97]
	ds_read_b128 v[124:127], v103 offset:28672
	v_mfma_f32_32x32x16_f16 v[34:49], v[148:151], v[132:135], v[34:49]
	ds_read_b128 v[112:115], v101 offset:28672
	v_mfma_f32_32x32x16_f16 v[66:81], v[144:147], v[136:139], v[66:81]
	ds_read_b128 v[128:131], v103 offset:30720
	v_mfma_f32_32x32x16_f16 v[18:33], v[148:151], v[136:139], v[18:33]
	ds_read_b128 v[116:119], v101 offset:30720
	v_mfma_f32_32x32x16_f16 v[50:65], v[144:147], v[140:143], v[50:65]
	ds_read_b128 v[120:123], v101 offset:32768
	v_mfma_f32_32x32x16_f16 v[2:17], v[148:151], v[140:143], v[2:17]
	s_waitcnt lgkmcnt(0)
	v_mfma_f32_32x32x16_f16 v[82:97], v[124:127], v[112:115], v[82:97]
	ds_read_b128 v[144:147], v104 offset:28672
	v_mfma_f32_32x32x16_f16 v[34:49], v[128:131], v[112:115], v[34:49]
	ds_read_b128 v[132:135], v102 offset:28672
	v_mfma_f32_32x32x16_f16 v[66:81], v[124:127], v[116:119], v[66:81]
	ds_read_b128 v[148:151], v104 offset:30720
	v_mfma_f32_32x32x16_f16 v[18:33], v[128:131], v[116:119], v[18:33]
	ds_read_b128 v[136:139], v102 offset:30720
	v_mfma_f32_32x32x16_f16 v[50:65], v[124:127], v[120:123], v[50:65]
	ds_read_b128 v[140:143], v102 offset:32768
	v_mfma_f32_32x32x16_f16 v[2:17], v[128:131], v[120:123], v[2:17]
	s_waitcnt lgkmcnt(0)
	s_barrier
	v_mfma_f32_32x32x16_f16 v[82:97], v[144:147], v[132:135], v[82:97]
	ds_read_b128 v[124:127], v107
	v_mfma_f32_32x32x16_f16 v[34:49], v[148:151], v[132:135], v[34:49]
	ds_read_b128 v[112:115], v105
	v_mfma_f32_32x32x16_f16 v[66:81], v[144:147], v[136:139], v[66:81]
	ds_read_b128 v[128:131], v107 offset:2048
	v_mfma_f32_32x32x16_f16 v[18:33], v[148:151], v[136:139], v[18:33]
	ds_read_b128 v[116:119], v105 offset:2048
	v_mfma_f32_32x32x16_f16 v[50:65], v[144:147], v[140:143], v[50:65]
	ds_read_b128 v[120:123], v105 offset:4096
	v_mfma_f32_32x32x16_f16 v[2:17], v[148:151], v[140:143], v[2:17]
	s_waitcnt lgkmcnt(0)
	v_mfma_f32_32x32x16_f16 v[82:97], v[124:127], v[112:115], v[82:97]
	ds_read_b128 v[144:147], v108
	v_mfma_f32_32x32x16_f16 v[34:49], v[128:131], v[112:115], v[34:49]
	ds_read_b128 v[132:135], v106
	v_mfma_f32_32x32x16_f16 v[66:81], v[124:127], v[116:119], v[66:81]
	ds_read_b128 v[148:151], v108 offset:2048
	v_mfma_f32_32x32x16_f16 v[18:33], v[128:131], v[116:119], v[18:33]
	ds_read_b128 v[136:139], v106 offset:2048
	v_mfma_f32_32x32x16_f16 v[50:65], v[124:127], v[120:123], v[50:65]
	ds_read_b128 v[140:143], v106 offset:4096
	v_mfma_f32_32x32x16_f16 v[2:17], v[128:131], v[120:123], v[2:17]
	s_waitcnt lgkmcnt(0)
	s_barrier
	v_mfma_f32_32x32x16_f16 v[82:97], v[144:147], v[132:135], v[82:97]
	ds_read_b128 v[124:127], v107 offset:28672
	v_mfma_f32_32x32x16_f16 v[34:49], v[148:151], v[132:135], v[34:49]
	ds_read_b128 v[112:115], v105 offset:28672
	v_mfma_f32_32x32x16_f16 v[66:81], v[144:147], v[136:139], v[66:81]
	ds_read_b128 v[128:131], v107 offset:30720
	v_mfma_f32_32x32x16_f16 v[18:33], v[148:151], v[136:139], v[18:33]
	ds_read_b128 v[116:119], v105 offset:30720
	v_mfma_f32_32x32x16_f16 v[50:65], v[144:147], v[140:143], v[50:65]
	ds_read_b128 v[120:123], v105 offset:32768
	v_mfma_f32_32x32x16_f16 v[2:17], v[148:151], v[140:143], v[2:17]
	s_waitcnt lgkmcnt(0)
	v_mfma_f32_32x32x16_f16 v[82:97], v[124:127], v[112:115], v[82:97]
	ds_read_b128 v[144:147], v108 offset:28672
	v_mfma_f32_32x32x16_f16 v[34:49], v[128:131], v[112:115], v[34:49]
	ds_read_b128 v[132:135], v106 offset:28672
	v_mfma_f32_32x32x16_f16 v[66:81], v[124:127], v[116:119], v[66:81]
	ds_read_b128 v[148:151], v108 offset:30720
	v_mfma_f32_32x32x16_f16 v[18:33], v[128:131], v[116:119], v[18:33]
	ds_read_b128 v[136:139], v106 offset:30720
	v_mfma_f32_32x32x16_f16 v[50:65], v[124:127], v[120:123], v[50:65]
	ds_read_b128 v[140:143], v106 offset:32768
	v_mfma_f32_32x32x16_f16 v[2:17], v[128:131], v[120:123], v[2:17]
	s_waitcnt lgkmcnt(0)
	s_barrier
	v_mfma_f32_32x32x16_f16 v[82:97], v[144:147], v[132:135], v[82:97]
	ds_read_b128 v[124:127], v154
	v_mfma_f32_32x32x16_f16 v[34:49], v[148:151], v[132:135], v[34:49]
	ds_read_b128 v[112:115], v152
	v_mfma_f32_32x32x16_f16 v[66:81], v[144:147], v[136:139], v[66:81]
	ds_read_b128 v[128:131], v154 offset:2048
	v_mfma_f32_32x32x16_f16 v[18:33], v[148:151], v[136:139], v[18:33]
	ds_read_b128 v[116:119], v152 offset:2048
	v_mfma_f32_32x32x16_f16 v[50:65], v[144:147], v[140:143], v[50:65]
	ds_read_b128 v[120:123], v152 offset:4096
	v_mfma_f32_32x32x16_f16 v[2:17], v[148:151], v[140:143], v[2:17]
	s_waitcnt lgkmcnt(0)
	v_mfma_f32_32x32x16_f16 v[82:97], v[124:127], v[112:115], v[82:97]
	ds_read_b128 v[144:147], v155
	v_mfma_f32_32x32x16_f16 v[34:49], v[128:131], v[112:115], v[34:49]
	ds_read_b128 v[132:135], v153
	v_mfma_f32_32x32x16_f16 v[66:81], v[124:127], v[116:119], v[66:81]
	ds_read_b128 v[148:151], v155 offset:2048
	v_mfma_f32_32x32x16_f16 v[18:33], v[128:131], v[116:119], v[18:33]
	ds_read_b128 v[136:139], v153 offset:2048
	v_mfma_f32_32x32x16_f16 v[50:65], v[124:127], v[120:123], v[50:65]
	ds_read_b128 v[140:143], v153 offset:4096
	v_mfma_f32_32x32x16_f16 v[2:17], v[128:131], v[120:123], v[2:17]
	s_waitcnt lgkmcnt(0)
	s_barrier
	v_mfma_f32_32x32x16_f16 v[82:97], v[144:147], v[132:135], v[82:97]
	ds_read_b128 v[124:127], v103
	v_mfma_f32_32x32x16_f16 v[34:49], v[148:151], v[132:135], v[34:49]
	ds_read_b128 v[112:115], v101
	v_mfma_f32_32x32x16_f16 v[66:81], v[144:147], v[136:139], v[66:81]
	ds_read_b128 v[128:131], v103 offset:2048
	v_mfma_f32_32x32x16_f16 v[18:33], v[148:151], v[136:139], v[18:33]
	ds_read_b128 v[116:119], v101 offset:2048
	v_mfma_f32_32x32x16_f16 v[50:65], v[144:147], v[140:143], v[50:65]
	ds_read_b128 v[120:123], v101 offset:4096
	v_mfma_f32_32x32x16_f16 v[2:17], v[148:151], v[140:143], v[2:17]
	s_waitcnt lgkmcnt(0)
	v_mfma_f32_32x32x16_f16 v[82:97], v[124:127], v[112:115], v[82:97]
	ds_read_b128 v[144:147], v104
	v_mfma_f32_32x32x16_f16 v[34:49], v[128:131], v[112:115], v[34:49]
	ds_read_b128 v[132:135], v102
	v_mfma_f32_32x32x16_f16 v[66:81], v[124:127], v[116:119], v[66:81]
	ds_read_b128 v[148:151], v104 offset:2048
	v_mfma_f32_32x32x16_f16 v[18:33], v[128:131], v[116:119], v[18:33]
	ds_read_b128 v[136:139], v102 offset:2048
	v_mfma_f32_32x32x16_f16 v[50:65], v[124:127], v[120:123], v[50:65]
	ds_read_b128 v[140:143], v102 offset:4096
	v_mfma_f32_32x32x16_f16 v[2:17], v[128:131], v[120:123], v[2:17]
	s_waitcnt lgkmcnt(0)
	s_barrier
	v_mfma_f32_32x32x16_f16 v[82:97], v[144:147], v[132:135], v[82:97]
	ds_read_b128 v[124:127], v103 offset:28672
	v_mfma_f32_32x32x16_f16 v[34:49], v[148:151], v[132:135], v[34:49]
	ds_read_b128 v[112:115], v101 offset:28672
	v_mfma_f32_32x32x16_f16 v[66:81], v[144:147], v[136:139], v[66:81]
	ds_read_b128 v[128:131], v103 offset:30720
	v_mfma_f32_32x32x16_f16 v[18:33], v[148:151], v[136:139], v[18:33]
	ds_read_b128 v[116:119], v101 offset:30720
	v_mfma_f32_32x32x16_f16 v[50:65], v[144:147], v[140:143], v[50:65]
	ds_read_b128 v[120:123], v101 offset:32768
	v_mfma_f32_32x32x16_f16 v[2:17], v[148:151], v[140:143], v[2:17]
	s_waitcnt lgkmcnt(0)
	v_mfma_f32_32x32x16_f16 v[82:97], v[124:127], v[112:115], v[82:97]
	ds_read_b128 v[144:147], v104 offset:28672
	v_mfma_f32_32x32x16_f16 v[34:49], v[128:131], v[112:115], v[34:49]
	ds_read_b128 v[132:135], v102 offset:28672
	v_mfma_f32_32x32x16_f16 v[66:81], v[124:127], v[116:119], v[66:81]
	ds_read_b128 v[148:151], v104 offset:30720
	v_mfma_f32_32x32x16_f16 v[18:33], v[128:131], v[116:119], v[18:33]
	ds_read_b128 v[136:139], v102 offset:30720
	v_mfma_f32_32x32x16_f16 v[50:65], v[124:127], v[120:123], v[50:65]
	ds_read_b128 v[140:143], v102 offset:32768
	v_mfma_f32_32x32x16_f16 v[2:17], v[128:131], v[120:123], v[2:17]
	s_waitcnt lgkmcnt(0)
	s_barrier
	v_mfma_f32_32x32x16_f16 v[82:97], v[144:147], v[132:135], v[82:97]
	ds_read_b128 v[124:127], v107
	v_mfma_f32_32x32x16_f16 v[34:49], v[148:151], v[132:135], v[34:49]
	ds_read_b128 v[112:115], v105
	v_mfma_f32_32x32x16_f16 v[66:81], v[144:147], v[136:139], v[66:81]
	ds_read_b128 v[128:131], v107 offset:2048
	v_mfma_f32_32x32x16_f16 v[18:33], v[148:151], v[136:139], v[18:33]
	ds_read_b128 v[116:119], v105 offset:2048
	v_mfma_f32_32x32x16_f16 v[50:65], v[144:147], v[140:143], v[50:65]
	ds_read_b128 v[120:123], v105 offset:4096
	v_mfma_f32_32x32x16_f16 v[2:17], v[148:151], v[140:143], v[2:17]
	s_waitcnt lgkmcnt(0)
	v_mfma_f32_32x32x16_f16 v[82:97], v[124:127], v[112:115], v[82:97]
	ds_read_b128 v[144:147], v108
	v_mfma_f32_32x32x16_f16 v[34:49], v[128:131], v[112:115], v[34:49]
	ds_read_b128 v[132:135], v106
	v_mfma_f32_32x32x16_f16 v[66:81], v[124:127], v[116:119], v[66:81]
	ds_read_b128 v[148:151], v108 offset:2048
	v_mfma_f32_32x32x16_f16 v[18:33], v[128:131], v[116:119], v[18:33]
	ds_read_b128 v[136:139], v106 offset:2048
	v_mfma_f32_32x32x16_f16 v[50:65], v[124:127], v[120:123], v[50:65]
	ds_read_b128 v[140:143], v106 offset:4096
	v_mfma_f32_32x32x16_f16 v[2:17], v[128:131], v[120:123], v[2:17]
	s_waitcnt lgkmcnt(0)
	s_barrier
	v_mfma_f32_32x32x16_f16 v[82:97], v[144:147], v[132:135], v[82:97]
	ds_read_b128 v[124:127], v107 offset:28672
	v_mfma_f32_32x32x16_f16 v[34:49], v[148:151], v[132:135], v[34:49]
	ds_read_b128 v[112:115], v105 offset:28672
	v_mfma_f32_32x32x16_f16 v[66:81], v[144:147], v[136:139], v[66:81]
	ds_read_b128 v[128:131], v107 offset:30720
	v_mfma_f32_32x32x16_f16 v[18:33], v[148:151], v[136:139], v[18:33]
	ds_read_b128 v[116:119], v105 offset:30720
	v_mfma_f32_32x32x16_f16 v[50:65], v[144:147], v[140:143], v[50:65]
	ds_read_b128 v[120:123], v105 offset:32768
	v_mfma_f32_32x32x16_f16 v[2:17], v[148:151], v[140:143], v[2:17]
	s_waitcnt lgkmcnt(0)
	v_mfma_f32_32x32x16_f16 v[82:97], v[124:127], v[112:115], v[82:97]
	ds_read_b128 v[144:147], v108 offset:28672
	v_mfma_f32_32x32x16_f16 v[34:49], v[128:131], v[112:115], v[34:49]
	ds_read_b128 v[132:135], v106 offset:28672
	v_mfma_f32_32x32x16_f16 v[66:81], v[124:127], v[116:119], v[66:81]
	ds_read_b128 v[148:151], v108 offset:30720
	v_mfma_f32_32x32x16_f16 v[18:33], v[128:131], v[116:119], v[18:33]
	ds_read_b128 v[136:139], v106 offset:30720
	v_mfma_f32_32x32x16_f16 v[50:65], v[124:127], v[120:123], v[50:65]
	ds_read_b128 v[140:143], v106 offset:32768
	v_mfma_f32_32x32x16_f16 v[2:17], v[128:131], v[120:123], v[2:17]
	s_waitcnt lgkmcnt(0)
	s_barrier
	v_mfma_f32_32x32x16_f16 v[82:97], v[144:147], v[132:135], v[82:97]
	ds_read_b128 v[124:127], v154
	v_mfma_f32_32x32x16_f16 v[34:49], v[148:151], v[132:135], v[34:49]
	ds_read_b128 v[112:115], v152
	v_mfma_f32_32x32x16_f16 v[66:81], v[144:147], v[136:139], v[66:81]
	ds_read_b128 v[128:131], v154 offset:2048
	v_mfma_f32_32x32x16_f16 v[18:33], v[148:151], v[136:139], v[18:33]
	ds_read_b128 v[116:119], v152 offset:2048
	v_mfma_f32_32x32x16_f16 v[50:65], v[144:147], v[140:143], v[50:65]
	ds_read_b128 v[120:123], v152 offset:4096
	v_mfma_f32_32x32x16_f16 v[2:17], v[148:151], v[140:143], v[2:17]
	s_waitcnt lgkmcnt(0)
	v_mfma_f32_32x32x16_f16 v[82:97], v[124:127], v[112:115], v[82:97]
	ds_read_b128 v[144:147], v155
	v_mfma_f32_32x32x16_f16 v[34:49], v[128:131], v[112:115], v[34:49]
	ds_read_b128 v[132:135], v153
	v_mfma_f32_32x32x16_f16 v[66:81], v[124:127], v[116:119], v[66:81]
	ds_read_b128 v[148:151], v155 offset:2048
	v_mfma_f32_32x32x16_f16 v[18:33], v[128:131], v[116:119], v[18:33]
	ds_read_b128 v[136:139], v153 offset:2048
	v_mfma_f32_32x32x16_f16 v[50:65], v[124:127], v[120:123], v[50:65]
	ds_read_b128 v[140:143], v153 offset:4096
	v_mfma_f32_32x32x16_f16 v[2:17], v[128:131], v[120:123], v[2:17]
	s_waitcnt lgkmcnt(0)
	s_barrier
	v_mfma_f32_32x32x16_f16 v[82:97], v[144:147], v[132:135], v[82:97]
	ds_read_b128 v[124:127], v103
	v_mfma_f32_32x32x16_f16 v[34:49], v[148:151], v[132:135], v[34:49]
	ds_read_b128 v[112:115], v101
	v_mfma_f32_32x32x16_f16 v[66:81], v[144:147], v[136:139], v[66:81]
	ds_read_b128 v[128:131], v103 offset:2048
	v_mfma_f32_32x32x16_f16 v[18:33], v[148:151], v[136:139], v[18:33]
	ds_read_b128 v[116:119], v101 offset:2048
	v_mfma_f32_32x32x16_f16 v[50:65], v[144:147], v[140:143], v[50:65]
	ds_read_b128 v[120:123], v101 offset:4096
	v_mfma_f32_32x32x16_f16 v[2:17], v[148:151], v[140:143], v[2:17]
	s_waitcnt lgkmcnt(0)
	v_mfma_f32_32x32x16_f16 v[82:97], v[124:127], v[112:115], v[82:97]
	ds_read_b128 v[144:147], v104
	v_mfma_f32_32x32x16_f16 v[34:49], v[128:131], v[112:115], v[34:49]
	ds_read_b128 v[132:135], v102
	v_mfma_f32_32x32x16_f16 v[66:81], v[124:127], v[116:119], v[66:81]
	ds_read_b128 v[148:151], v104 offset:2048
	v_mfma_f32_32x32x16_f16 v[18:33], v[128:131], v[116:119], v[18:33]
	ds_read_b128 v[136:139], v102 offset:2048
	v_mfma_f32_32x32x16_f16 v[50:65], v[124:127], v[120:123], v[50:65]
	ds_read_b128 v[140:143], v102 offset:4096
	v_mfma_f32_32x32x16_f16 v[2:17], v[128:131], v[120:123], v[2:17]
	s_waitcnt lgkmcnt(0)
	s_barrier
	v_mfma_f32_32x32x16_f16 v[82:97], v[144:147], v[132:135], v[82:97]
	ds_read_b128 v[124:127], v103 offset:28672
	v_mfma_f32_32x32x16_f16 v[34:49], v[148:151], v[132:135], v[34:49]
	ds_read_b128 v[112:115], v101 offset:28672
	v_mfma_f32_32x32x16_f16 v[66:81], v[144:147], v[136:139], v[66:81]
	ds_read_b128 v[128:131], v103 offset:30720
	v_mfma_f32_32x32x16_f16 v[18:33], v[148:151], v[136:139], v[18:33]
	ds_read_b128 v[116:119], v101 offset:30720
	v_mfma_f32_32x32x16_f16 v[50:65], v[144:147], v[140:143], v[50:65]
	ds_read_b128 v[120:123], v101 offset:32768
	v_mfma_f32_32x32x16_f16 v[2:17], v[148:151], v[140:143], v[2:17]
	s_waitcnt lgkmcnt(0)
	v_mfma_f32_32x32x16_f16 v[82:97], v[124:127], v[112:115], v[82:97]
	ds_read_b128 v[144:147], v104 offset:28672
	v_mfma_f32_32x32x16_f16 v[34:49], v[128:131], v[112:115], v[34:49]
	ds_read_b128 v[132:135], v102 offset:28672
	v_mfma_f32_32x32x16_f16 v[66:81], v[124:127], v[116:119], v[66:81]
	ds_read_b128 v[148:151], v104 offset:30720
	v_mfma_f32_32x32x16_f16 v[18:33], v[128:131], v[116:119], v[18:33]
	ds_read_b128 v[136:139], v102 offset:30720
	v_mfma_f32_32x32x16_f16 v[50:65], v[124:127], v[120:123], v[50:65]
	ds_read_b128 v[140:143], v102 offset:32768
	v_mfma_f32_32x32x16_f16 v[2:17], v[128:131], v[120:123], v[2:17]
	s_waitcnt lgkmcnt(0)
	s_barrier
	v_mfma_f32_32x32x16_f16 v[82:97], v[144:147], v[132:135], v[82:97]
	ds_read_b128 v[124:127], v107
	v_mfma_f32_32x32x16_f16 v[34:49], v[148:151], v[132:135], v[34:49]
	ds_read_b128 v[112:115], v105
	v_mfma_f32_32x32x16_f16 v[66:81], v[144:147], v[136:139], v[66:81]
	ds_read_b128 v[128:131], v107 offset:2048
	v_mfma_f32_32x32x16_f16 v[18:33], v[148:151], v[136:139], v[18:33]
	ds_read_b128 v[116:119], v105 offset:2048
	v_mfma_f32_32x32x16_f16 v[50:65], v[144:147], v[140:143], v[50:65]
	ds_read_b128 v[120:123], v105 offset:4096
	v_mfma_f32_32x32x16_f16 v[2:17], v[148:151], v[140:143], v[2:17]
	s_waitcnt lgkmcnt(0)
	v_mfma_f32_32x32x16_f16 v[82:97], v[124:127], v[112:115], v[82:97]
	ds_read_b128 v[144:147], v108
	v_mfma_f32_32x32x16_f16 v[34:49], v[128:131], v[112:115], v[34:49]
	ds_read_b128 v[132:135], v106
	v_mfma_f32_32x32x16_f16 v[66:81], v[124:127], v[116:119], v[66:81]
	ds_read_b128 v[148:151], v108 offset:2048
	v_mfma_f32_32x32x16_f16 v[18:33], v[128:131], v[116:119], v[18:33]
	ds_read_b128 v[136:139], v106 offset:2048
	v_mfma_f32_32x32x16_f16 v[50:65], v[124:127], v[120:123], v[50:65]
	ds_read_b128 v[140:143], v106 offset:4096
	v_mfma_f32_32x32x16_f16 v[2:17], v[128:131], v[120:123], v[2:17]
	s_waitcnt lgkmcnt(0)
	s_barrier
	v_mfma_f32_32x32x16_f16 v[82:97], v[144:147], v[132:135], v[82:97]
	ds_read_b128 v[124:127], v107 offset:28672
	v_mfma_f32_32x32x16_f16 v[34:49], v[148:151], v[132:135], v[34:49]
	ds_read_b128 v[112:115], v105 offset:28672
	v_mfma_f32_32x32x16_f16 v[66:81], v[144:147], v[136:139], v[66:81]
	ds_read_b128 v[128:131], v107 offset:30720
	v_mfma_f32_32x32x16_f16 v[18:33], v[148:151], v[136:139], v[18:33]
	ds_read_b128 v[116:119], v105 offset:30720
	v_mfma_f32_32x32x16_f16 v[50:65], v[144:147], v[140:143], v[50:65]
	ds_read_b128 v[120:123], v105 offset:32768
	v_mfma_f32_32x32x16_f16 v[2:17], v[148:151], v[140:143], v[2:17]
	s_waitcnt lgkmcnt(0)
	v_mfma_f32_32x32x16_f16 v[82:97], v[124:127], v[112:115], v[82:97]
	ds_read_b128 v[144:147], v108 offset:28672
	v_mfma_f32_32x32x16_f16 v[34:49], v[128:131], v[112:115], v[34:49]
	ds_read_b128 v[132:135], v106 offset:28672
	v_mfma_f32_32x32x16_f16 v[66:81], v[124:127], v[116:119], v[66:81]
	ds_read_b128 v[148:151], v108 offset:30720
	v_mfma_f32_32x32x16_f16 v[18:33], v[128:131], v[116:119], v[18:33]
	ds_read_b128 v[136:139], v106 offset:30720
	v_mfma_f32_32x32x16_f16 v[50:65], v[124:127], v[120:123], v[50:65]
	ds_read_b128 v[140:143], v106 offset:32768
	v_mfma_f32_32x32x16_f16 v[2:17], v[128:131], v[120:123], v[2:17]
	s_waitcnt lgkmcnt(0)
	v_mfma_f32_32x32x16_f16 v[82:97], v[144:147], v[132:135], v[82:97]
	v_mfma_f32_32x32x16_f16 v[34:49], v[148:151], v[132:135], v[34:49]
	v_mfma_f32_32x32x16_f16 v[66:81], v[144:147], v[136:139], v[66:81]
	v_mfma_f32_32x32x16_f16 v[18:33], v[148:151], v[136:139], v[18:33]
	v_mfma_f32_32x32x16_f16 v[50:65], v[144:147], v[140:143], v[50:65]
	v_mfma_f32_32x32x16_f16 v[2:17], v[148:151], v[140:143], v[2:17]

	.amdhsa_kernel _Z15qkv_proj_kernelPKDF16_S0_PKfS2_S2_PDF16_S3_S3_
		.amdhsa_group_segment_fixed_size 30720
		.amdhsa_private_segment_fixed_size 0
		.amdhsa_kernarg_size 64
		.amdhsa_user_sgpr_count 2
		.amdhsa_user_sgpr_dispatch_ptr 0
		.amdhsa_user_sgpr_queue_ptr 0
		.amdhsa_user_sgpr_kernarg_segment_ptr 1
		.amdhsa_user_sgpr_dispatch_id 0
		.amdhsa_user_sgpr_kernarg_preload_length 0
		.amdhsa_user_sgpr_kernarg_preload_offset 0
		.amdhsa_user_sgpr_private_segment_size 0
		.amdhsa_uses_dynamic_stack 0
		.amdhsa_enable_private_segment 0
		.amdhsa_system_sgpr_workgroup_id_x 1
		.amdhsa_system_sgpr_workgroup_id_y 0
		.amdhsa_system_sgpr_workgroup_id_z 0
		.amdhsa_system_sgpr_workgroup_info 0
		.amdhsa_system_vgpr_workitem_id 0
		.amdhsa_next_free_vgpr 156
		.amdhsa_next_free_sgpr 41
		.amdhsa_accum_offset 156
		.amdhsa_reserve_vcc 1
		.amdhsa_float_round_mode_32 0
		.amdhsa_float_round_mode_16_64 0
		.amdhsa_float_denorm_mode_32 3
		.amdhsa_float_denorm_mode_16_64 3
		.amdhsa_dx10_clamp 1
		.amdhsa_ieee_mode 1
		.amdhsa_fp16_overflow 0
		.amdhsa_tg_split 0
		.amdhsa_exception_fp_ieee_invalid_op 0
		.amdhsa_exception_fp_denorm_src 0
		.amdhsa_exception_fp_ieee_div_zero 0
		.amdhsa_exception_fp_ieee_overflow 0
		.amdhsa_exception_fp_ieee_underflow 0
		.amdhsa_exception_fp_ieee_inexact 0
		.amdhsa_exception_int_div_zero 0
	.end_amdhsa_kernel

.LBB2_3:
	s_load_dwordx4 s[4:7], s[0:1], 0x10
	v_and_b32_e32 v51, 31, v1
	v_lshrrev_b32_e32 v50, 5, v1
	v_bfe_u32 v52, v1, 1, 3
	s_lshl_b32 s2, s13, 5
	v_or_b32_e32 v53, s2, v51
	v_lshlrev_b32_e32 v53, 7, v53
	v_add_u32_e32 v53, 0x800, v53
	v_lshlrev_b32_e32 v54, 7, v51
	v_add_u32_e32 v54, 0x4800, v54
	v_xor_b32_e32 v55, v50, v52
	v_lshlrev_b32_e32 v104, 4, v55
	v_add_u32_e32 v56, v53, v104
	v_add_u32_e32 v60, v54, v104
	v_add_u32_e32 v64, 0xe000, v56
	v_add_u32_e32 v68, 0xe000, v60
	v_add_u32_e32 v136, 0x1c000, v56
	v_add_u32_e32 v140, 0x1c000, v60
	v_xor_b32_e32 v104, 2, v55
	v_lshlrev_b32_e32 v104, 4, v104
	v_add_u32_e32 v57, v53, v104
	v_add_u32_e32 v61, v54, v104
	v_add_u32_e32 v65, 0xe000, v57
	v_add_u32_e32 v69, 0xe000, v61
	v_add_u32_e32 v137, 0x1c000, v57
	v_add_u32_e32 v141, 0x1c000, v61
	v_xor_b32_e32 v104, 4, v55
	v_lshlrev_b32_e32 v104, 4, v104
	v_add_u32_e32 v58, v53, v104
	v_add_u32_e32 v62, v54, v104
	v_add_u32_e32 v66, 0xe000, v58
	v_add_u32_e32 v70, 0xe000, v62
	v_add_u32_e32 v138, 0x1c000, v58
	v_add_u32_e32 v142, 0x1c000, v62
	v_xor_b32_e32 v104, 6, v55
	v_lshlrev_b32_e32 v104, 4, v104
	v_add_u32_e32 v59, v53, v104
	v_add_u32_e32 v63, v54, v104
	v_add_u32_e32 v67, 0xe000, v59
	v_add_u32_e32 v71, 0xe000, v63
	v_add_u32_e32 v139, 0x1c000, v59
	v_add_u32_e32 v143, 0x1c000, v63
	v_mov_b32_e32 v2, 0
	v_mov_b32_e32 v3, 0
	v_mov_b32_e32 v4, 0
	v_mov_b32_e32 v5, 0
	v_mov_b32_e32 v6, 0
	v_mov_b32_e32 v7, 0
	v_mov_b32_e32 v8, 0
	v_mov_b32_e32 v9, 0
	v_mov_b32_e32 v10, 0
	v_mov_b32_e32 v11, 0
	v_mov_b32_e32 v12, 0
	v_mov_b32_e32 v13, 0
	v_mov_b32_e32 v14, 0
	v_mov_b32_e32 v15, 0
	v_mov_b32_e32 v16, 0
	v_mov_b32_e32 v17, 0
	v_mov_b32_e32 v18, 0
	v_mov_b32_e32 v19, 0
	v_mov_b32_e32 v20, 0
	v_mov_b32_e32 v21, 0
	v_mov_b32_e32 v22, 0
	v_mov_b32_e32 v23, 0
	v_mov_b32_e32 v24, 0
	v_mov_b32_e32 v25, 0
	v_mov_b32_e32 v26, 0
	v_mov_b32_e32 v27, 0
	v_mov_b32_e32 v28, 0
	v_mov_b32_e32 v29, 0
	v_mov_b32_e32 v30, 0
	v_mov_b32_e32 v31, 0
	v_mov_b32_e32 v32, 0
	v_mov_b32_e32 v33, 0
	v_mov_b32_e32 v34, 0
	v_mov_b32_e32 v35, 0
	v_mov_b32_e32 v36, 0
	v_mov_b32_e32 v37, 0
	v_mov_b32_e32 v38, 0
	v_mov_b32_e32 v39, 0
	v_mov_b32_e32 v40, 0
	v_mov_b32_e32 v41, 0
	v_mov_b32_e32 v42, 0
	v_mov_b32_e32 v43, 0
	v_mov_b32_e32 v44, 0
	v_mov_b32_e32 v45, 0
	v_mov_b32_e32 v46, 0
	v_mov_b32_e32 v47, 0
	v_mov_b32_e32 v48, 0
	v_mov_b32_e32 v49, 0
	s_barrier
	ds_read_b128 v[72:75], v56
	ds_read_b128 v[76:79], v60
	ds_read_b128 v[80:83], v60 offset:4096
	ds_read_b128 v[84:87], v60 offset:8192
	ds_read_b128 v[88:91], v57
	ds_read_b128 v[92:95], v61
	ds_read_b128 v[96:99], v61 offset:4096
	ds_read_b128 v[100:103], v61 offset:8192
	s_waitcnt lgkmcnt(0)
	v_mfma_f32_32x32x16_f16 v[34:49], v[72:75], v[76:79], v[34:49]
	ds_read_b128 v[104:107], v58
	ds_read_b128 v[108:111], v62
	v_mfma_f32_32x32x16_f16 v[18:33], v[72:75], v[80:83], v[18:33]
	ds_read_b128 v[112:115], v62 offset:4096
	ds_read_b128 v[116:119], v62 offset:8192
	v_mfma_f32_32x32x16_f16 v[2:17], v[72:75], v[84:87], v[2:17]
	ds_read_b128 v[120:123], v59
	v_mfma_f32_32x32x16_f16 v[34:49], v[88:91], v[92:95], v[34:49]
	ds_read_b128 v[124:127], v63
	v_mfma_f32_32x32x16_f16 v[18:33], v[88:91], v[96:99], v[18:33]
	ds_read_b128 v[128:131], v63 offset:4096
	v_mfma_f32_32x32x16_f16 v[2:17], v[88:91], v[100:103], v[2:17]
	ds_read_b128 v[132:135], v63 offset:8192
	s_waitcnt lgkmcnt(0)
	s_barrier
	v_mfma_f32_32x32x16_f16 v[34:49], v[104:107], v[108:111], v[34:49]
	ds_read_b128 v[72:75], v56 offset:28672
	ds_read_b128 v[76:79], v60 offset:28672
	v_mfma_f32_32x32x16_f16 v[18:33], v[104:107], v[112:115], v[18:33]
	ds_read_b128 v[80:83], v60 offset:32768
	ds_read_b128 v[84:87], v60 offset:36864
	v_mfma_f32_32x32x16_f16 v[2:17], v[104:107], v[116:119], v[2:17]
	ds_read_b128 v[88:91], v57 offset:28672
	v_mfma_f32_32x32x16_f16 v[34:49], v[120:123], v[124:127], v[34:49]
	ds_read_b128 v[92:95], v61 offset:28672
	v_mfma_f32_32x32x16_f16 v[18:33], v[120:123], v[128:131], v[18:33]
	ds_read_b128 v[96:99], v61 offset:32768
	v_mfma_f32_32x32x16_f16 v[2:17], v[120:123], v[132:135], v[2:17]
	ds_read_b128 v[100:103], v61 offset:36864
	s_waitcnt lgkmcnt(0)
	v_mfma_f32_32x32x16_f16 v[34:49], v[72:75], v[76:79], v[34:49]
	ds_read_b128 v[104:107], v58 offset:28672
	ds_read_b128 v[108:111], v62 offset:28672
	v_mfma_f32_32x32x16_f16 v[18:33], v[72:75], v[80:83], v[18:33]
	ds_read_b128 v[112:115], v62 offset:32768
	ds_read_b128 v[116:119], v62 offset:36864
	v_mfma_f32_32x32x16_f16 v[2:17], v[72:75], v[84:87], v[2:17]
	ds_read_b128 v[120:123], v59 offset:28672
	v_mfma_f32_32x32x16_f16 v[34:49], v[88:91], v[92:95], v[34:49]
	ds_read_b128 v[124:127], v63 offset:28672
	v_mfma_f32_32x32x16_f16 v[18:33], v[88:91], v[96:99], v[18:33]
	ds_read_b128 v[128:131], v63 offset:32768
	v_mfma_f32_32x32x16_f16 v[2:17], v[88:91], v[100:103], v[2:17]
	ds_read_b128 v[132:135], v63 offset:36864
	s_waitcnt lgkmcnt(0)
	s_barrier
	v_mfma_f32_32x32x16_f16 v[34:49], v[104:107], v[108:111], v[34:49]
	ds_read_b128 v[72:75], v64
	ds_read_b128 v[76:79], v68
	v_mfma_f32_32x32x16_f16 v[18:33], v[104:107], v[112:115], v[18:33]
	ds_read_b128 v[80:83], v68 offset:4096
	ds_read_b128 v[84:87], v68 offset:8192
	v_mfma_f32_32x32x16_f16 v[2:17], v[104:107], v[116:119], v[2:17]
	ds_read_b128 v[88:91], v65
	v_mfma_f32_32x32x16_f16 v[34:49], v[120:123], v[124:127], v[34:49]
	ds_read_b128 v[92:95], v69
	v_mfma_f32_32x32x16_f16 v[18:33], v[120:123], v[128:131], v[18:33]
	ds_read_b128 v[96:99], v69 offset:4096
	v_mfma_f32_32x32x16_f16 v[2:17], v[120:123], v[132:135], v[2:17]
	ds_read_b128 v[100:103], v69 offset:8192
	s_waitcnt lgkmcnt(0)
	v_mfma_f32_32x32x16_f16 v[34:49], v[72:75], v[76:79], v[34:49]
	ds_read_b128 v[104:107], v66
	ds_read_b128 v[108:111], v70
	v_mfma_f32_32x32x16_f16 v[18:33], v[72:75], v[80:83], v[18:33]
	ds_read_b128 v[112:115], v70 offset:4096
	ds_read_b128 v[116:119], v70 offset:8192
	v_mfma_f32_32x32x16_f16 v[2:17], v[72:75], v[84:87], v[2:17]
	ds_read_b128 v[120:123], v67
	v_mfma_f32_32x32x16_f16 v[34:49], v[88:91], v[92:95], v[34:49]
	ds_read_b128 v[124:127], v71
	v_mfma_f32_32x32x16_f16 v[18:33], v[88:91], v[96:99], v[18:33]
	ds_read_b128 v[128:131], v71 offset:4096
	v_mfma_f32_32x32x16_f16 v[2:17], v[88:91], v[100:103], v[2:17]
	ds_read_b128 v[132:135], v71 offset:8192
	s_waitcnt lgkmcnt(0)
	s_barrier
	v_mfma_f32_32x32x16_f16 v[34:49], v[104:107], v[108:111], v[34:49]
	ds_read_b128 v[72:75], v64 offset:28672
	ds_read_b128 v[76:79], v68 offset:28672
	v_mfma_f32_32x32x16_f16 v[18:33], v[104:107], v[112:115], v[18:33]
	ds_read_b128 v[80:83], v68 offset:32768
	ds_read_b128 v[84:87], v68 offset:36864
	v_mfma_f32_32x32x16_f16 v[2:17], v[104:107], v[116:119], v[2:17]
	ds_read_b128 v[88:91], v65 offset:28672
	v_mfma_f32_32x32x16_f16 v[34:49], v[120:123], v[124:127], v[34:49]
	ds_read_b128 v[92:95], v69 offset:28672
	v_mfma_f32_32x32x16_f16 v[18:33], v[120:123], v[128:131], v[18:33]
	ds_read_b128 v[96:99], v69 offset:32768
	v_mfma_f32_32x32x16_f16 v[2:17], v[120:123], v[132:135], v[2:17]
	ds_read_b128 v[100:103], v69 offset:36864
	s_waitcnt lgkmcnt(0)
	v_mfma_f32_32x32x16_f16 v[34:49], v[72:75], v[76:79], v[34:49]
	ds_read_b128 v[104:107], v66 offset:28672
	ds_read_b128 v[108:111], v70 offset:28672
	v_mfma_f32_32x32x16_f16 v[18:33], v[72:75], v[80:83], v[18:33]
	ds_read_b128 v[112:115], v70 offset:32768
	ds_read_b128 v[116:119], v70 offset:36864
	v_mfma_f32_32x32x16_f16 v[2:17], v[72:75], v[84:87], v[2:17]
	ds_read_b128 v[120:123], v67 offset:28672
	v_mfma_f32_32x32x16_f16 v[34:49], v[88:91], v[92:95], v[34:49]
	ds_read_b128 v[124:127], v71 offset:28672
	v_mfma_f32_32x32x16_f16 v[18:33], v[88:91], v[96:99], v[18:33]
	ds_read_b128 v[128:131], v71 offset:32768
	v_mfma_f32_32x32x16_f16 v[2:17], v[88:91], v[100:103], v[2:17]
	ds_read_b128 v[132:135], v71 offset:36864
	s_waitcnt lgkmcnt(0)
	s_barrier
	v_mfma_f32_32x32x16_f16 v[34:49], v[104:107], v[108:111], v[34:49]
	ds_read_b128 v[72:75], v136
	ds_read_b128 v[76:79], v140
	v_mfma_f32_32x32x16_f16 v[18:33], v[104:107], v[112:115], v[18:33]
	ds_read_b128 v[80:83], v140 offset:4096
	ds_read_b128 v[84:87], v140 offset:8192
	v_mfma_f32_32x32x16_f16 v[2:17], v[104:107], v[116:119], v[2:17]
	ds_read_b128 v[88:91], v137
	v_mfma_f32_32x32x16_f16 v[34:49], v[120:123], v[124:127], v[34:49]
	ds_read_b128 v[92:95], v141
	v_mfma_f32_32x32x16_f16 v[18:33], v[120:123], v[128:131], v[18:33]
	ds_read_b128 v[96:99], v141 offset:4096
	v_mfma_f32_32x32x16_f16 v[2:17], v[120:123], v[132:135], v[2:17]
	ds_read_b128 v[100:103], v141 offset:8192
	s_waitcnt lgkmcnt(0)
	v_mfma_f32_32x32x16_f16 v[34:49], v[72:75], v[76:79], v[34:49]
	ds_read_b128 v[104:107], v138
	ds_read_b128 v[108:111], v142
	v_mfma_f32_32x32x16_f16 v[18:33], v[72:75], v[80:83], v[18:33]
	ds_read_b128 v[112:115], v142 offset:4096
	ds_read_b128 v[116:119], v142 offset:8192
	v_mfma_f32_32x32x16_f16 v[2:17], v[72:75], v[84:87], v[2:17]
	ds_read_b128 v[120:123], v139
	v_mfma_f32_32x32x16_f16 v[34:49], v[88:91], v[92:95], v[34:49]
	ds_read_b128 v[124:127], v143
	v_mfma_f32_32x32x16_f16 v[18:33], v[88:91], v[96:99], v[18:33]
	ds_read_b128 v[128:131], v143 offset:4096
	v_mfma_f32_32x32x16_f16 v[2:17], v[88:91], v[100:103], v[2:17]
	ds_read_b128 v[132:135], v143 offset:8192
	s_waitcnt lgkmcnt(0)
	s_barrier
	v_mfma_f32_32x32x16_f16 v[34:49], v[104:107], v[108:111], v[34:49]
	ds_read_b128 v[72:75], v56
	ds_read_b128 v[76:79], v60
	v_mfma_f32_32x32x16_f16 v[18:33], v[104:107], v[112:115], v[18:33]
	ds_read_b128 v[80:83], v60 offset:4096
	ds_read_b128 v[84:87], v60 offset:8192
	v_mfma_f32_32x32x16_f16 v[2:17], v[104:107], v[116:119], v[2:17]
	ds_read_b128 v[88:91], v57
	v_mfma_f32_32x32x16_f16 v[34:49], v[120:123], v[124:127], v[34:49]
	ds_read_b128 v[92:95], v61
	v_mfma_f32_32x32x16_f16 v[18:33], v[120:123], v[128:131], v[18:33]
	ds_read_b128 v[96:99], v61 offset:4096
	v_mfma_f32_32x32x16_f16 v[2:17], v[120:123], v[132:135], v[2:17]
	ds_read_b128 v[100:103], v61 offset:8192
	s_waitcnt lgkmcnt(0)
	v_mfma_f32_32x32x16_f16 v[34:49], v[72:75], v[76:79], v[34:49]
	ds_read_b128 v[104:107], v58
	ds_read_b128 v[108:111], v62
	v_mfma_f32_32x32x16_f16 v[18:33], v[72:75], v[80:83], v[18:33]
	ds_read_b128 v[112:115], v62 offset:4096
	ds_read_b128 v[116:119], v62 offset:8192
	v_mfma_f32_32x32x16_f16 v[2:17], v[72:75], v[84:87], v[2:17]
	ds_read_b128 v[120:123], v59
	v_mfma_f32_32x32x16_f16 v[34:49], v[88:91], v[92:95], v[34:49]
	ds_read_b128 v[124:127], v63
	v_mfma_f32_32x32x16_f16 v[18:33], v[88:91], v[96:99], v[18:33]
	ds_read_b128 v[128:131], v63 offset:4096
	v_mfma_f32_32x32x16_f16 v[2:17], v[88:91], v[100:103], v[2:17]
	ds_read_b128 v[132:135], v63 offset:8192
	s_waitcnt lgkmcnt(0)
	s_barrier
	v_mfma_f32_32x32x16_f16 v[34:49], v[104:107], v[108:111], v[34:49]
	ds_read_b128 v[72:75], v56 offset:28672
	ds_read_b128 v[76:79], v60 offset:28672
	v_mfma_f32_32x32x16_f16 v[18:33], v[104:107], v[112:115], v[18:33]
	ds_read_b128 v[80:83], v60 offset:32768
	ds_read_b128 v[84:87], v60 offset:36864
	v_mfma_f32_32x32x16_f16 v[2:17], v[104:107], v[116:119], v[2:17]
	ds_read_b128 v[88:91], v57 offset:28672
	v_mfma_f32_32x32x16_f16 v[34:49], v[120:123], v[124:127], v[34:49]
	ds_read_b128 v[92:95], v61 offset:28672
	v_mfma_f32_32x32x16_f16 v[18:33], v[120:123], v[128:131], v[18:33]
	ds_read_b128 v[96:99], v61 offset:32768
	v_mfma_f32_32x32x16_f16 v[2:17], v[120:123], v[132:135], v[2:17]
	ds_read_b128 v[100:103], v61 offset:36864
	s_waitcnt lgkmcnt(0)
	v_mfma_f32_32x32x16_f16 v[34:49], v[72:75], v[76:79], v[34:49]
	ds_read_b128 v[104:107], v58 offset:28672
	ds_read_b128 v[108:111], v62 offset:28672
	v_mfma_f32_32x32x16_f16 v[18:33], v[72:75], v[80:83], v[18:33]
	ds_read_b128 v[112:115], v62 offset:32768
	ds_read_b128 v[116:119], v62 offset:36864
	v_mfma_f32_32x32x16_f16 v[2:17], v[72:75], v[84:87], v[2:17]
	ds_read_b128 v[120:123], v59 offset:28672
	v_mfma_f32_32x32x16_f16 v[34:49], v[88:91], v[92:95], v[34:49]
	ds_read_b128 v[124:127], v63 offset:28672
	v_mfma_f32_32x32x16_f16 v[18:33], v[88:91], v[96:99], v[18:33]
	ds_read_b128 v[128:131], v63 offset:32768
	v_mfma_f32_32x32x16_f16 v[2:17], v[88:91], v[100:103], v[2:17]
	ds_read_b128 v[132:135], v63 offset:36864
	s_waitcnt lgkmcnt(0)
	s_barrier
	v_mfma_f32_32x32x16_f16 v[34:49], v[104:107], v[108:111], v[34:49]
	ds_read_b128 v[72:75], v64
	ds_read_b128 v[76:79], v68
	v_mfma_f32_32x32x16_f16 v[18:33], v[104:107], v[112:115], v[18:33]
	ds_read_b128 v[80:83], v68 offset:4096
	ds_read_b128 v[84:87], v68 offset:8192
	v_mfma_f32_32x32x16_f16 v[2:17], v[104:107], v[116:119], v[2:17]
	ds_read_b128 v[88:91], v65
	v_mfma_f32_32x32x16_f16 v[34:49], v[120:123], v[124:127], v[34:49]
	ds_read_b128 v[92:95], v69
	v_mfma_f32_32x32x16_f16 v[18:33], v[120:123], v[128:131], v[18:33]
	ds_read_b128 v[96:99], v69 offset:4096
	v_mfma_f32_32x32x16_f16 v[2:17], v[120:123], v[132:135], v[2:17]
	ds_read_b128 v[100:103], v69 offset:8192
	s_waitcnt lgkmcnt(0)
	v_mfma_f32_32x32x16_f16 v[34:49], v[72:75], v[76:79], v[34:49]
	ds_read_b128 v[104:107], v66
	ds_read_b128 v[108:111], v70
	v_mfma_f32_32x32x16_f16 v[18:33], v[72:75], v[80:83], v[18:33]
	ds_read_b128 v[112:115], v70 offset:4096
	ds_read_b128 v[116:119], v70 offset:8192
	v_mfma_f32_32x32x16_f16 v[2:17], v[72:75], v[84:87], v[2:17]
	ds_read_b128 v[120:123], v67
	v_mfma_f32_32x32x16_f16 v[34:49], v[88:91], v[92:95], v[34:49]
	ds_read_b128 v[124:127], v71
	v_mfma_f32_32x32x16_f16 v[18:33], v[88:91], v[96:99], v[18:33]
	ds_read_b128 v[128:131], v71 offset:4096
	v_mfma_f32_32x32x16_f16 v[2:17], v[88:91], v[100:103], v[2:17]
	ds_read_b128 v[132:135], v71 offset:8192
	s_waitcnt lgkmcnt(0)
	s_barrier
	v_mfma_f32_32x32x16_f16 v[34:49], v[104:107], v[108:111], v[34:49]
	ds_read_b128 v[72:75], v64 offset:28672
	ds_read_b128 v[76:79], v68 offset:28672
	v_mfma_f32_32x32x16_f16 v[18:33], v[104:107], v[112:115], v[18:33]
	ds_read_b128 v[80:83], v68 offset:32768
	ds_read_b128 v[84:87], v68 offset:36864
	v_mfma_f32_32x32x16_f16 v[2:17], v[104:107], v[116:119], v[2:17]
	ds_read_b128 v[88:91], v65 offset:28672
	v_mfma_f32_32x32x16_f16 v[34:49], v[120:123], v[124:127], v[34:49]
	ds_read_b128 v[92:95], v69 offset:28672
	v_mfma_f32_32x32x16_f16 v[18:33], v[120:123], v[128:131], v[18:33]
	ds_read_b128 v[96:99], v69 offset:32768
	v_mfma_f32_32x32x16_f16 v[2:17], v[120:123], v[132:135], v[2:17]
	ds_read_b128 v[100:103], v69 offset:36864
	s_waitcnt lgkmcnt(0)
	v_mfma_f32_32x32x16_f16 v[34:49], v[72:75], v[76:79], v[34:49]
	ds_read_b128 v[104:107], v66 offset:28672
	ds_read_b128 v[108:111], v70 offset:28672
	v_mfma_f32_32x32x16_f16 v[18:33], v[72:75], v[80:83], v[18:33]
	ds_read_b128 v[112:115], v70 offset:32768
	ds_read_b128 v[116:119], v70 offset:36864
	v_mfma_f32_32x32x16_f16 v[2:17], v[72:75], v[84:87], v[2:17]
	ds_read_b128 v[120:123], v67 offset:28672
	v_mfma_f32_32x32x16_f16 v[34:49], v[88:91], v[92:95], v[34:49]
	ds_read_b128 v[124:127], v71 offset:28672
	v_mfma_f32_32x32x16_f16 v[18:33], v[88:91], v[96:99], v[18:33]
	ds_read_b128 v[128:131], v71 offset:32768
	v_mfma_f32_32x32x16_f16 v[2:17], v[88:91], v[100:103], v[2:17]
	ds_read_b128 v[132:135], v71 offset:36864
	s_waitcnt lgkmcnt(0)
	s_barrier
	v_mfma_f32_32x32x16_f16 v[34:49], v[104:107], v[108:111], v[34:49]
	ds_read_b128 v[72:75], v136
	ds_read_b128 v[76:79], v140
	v_mfma_f32_32x32x16_f16 v[18:33], v[104:107], v[112:115], v[18:33]
	ds_read_b128 v[80:83], v140 offset:4096
	ds_read_b128 v[84:87], v140 offset:8192
	v_mfma_f32_32x32x16_f16 v[2:17], v[104:107], v[116:119], v[2:17]
	ds_read_b128 v[88:91], v137
	v_mfma_f32_32x32x16_f16 v[34:49], v[120:123], v[124:127], v[34:49]
	ds_read_b128 v[92:95], v141
	v_mfma_f32_32x32x16_f16 v[18:33], v[120:123], v[128:131], v[18:33]
	ds_read_b128 v[96:99], v141 offset:4096
	v_mfma_f32_32x32x16_f16 v[2:17], v[120:123], v[132:135], v[2:17]
	ds_read_b128 v[100:103], v141 offset:8192
	s_waitcnt lgkmcnt(0)
	v_mfma_f32_32x32x16_f16 v[34:49], v[72:75], v[76:79], v[34:49]
	ds_read_b128 v[104:107], v138
	ds_read_b128 v[108:111], v142
	v_mfma_f32_32x32x16_f16 v[18:33], v[72:75], v[80:83], v[18:33]
	ds_read_b128 v[112:115], v142 offset:4096
	ds_read_b128 v[116:119], v142 offset:8192
	v_mfma_f32_32x32x16_f16 v[2:17], v[72:75], v[84:87], v[2:17]
	ds_read_b128 v[120:123], v139
	v_mfma_f32_32x32x16_f16 v[34:49], v[88:91], v[92:95], v[34:49]
	ds_read_b128 v[124:127], v143
	v_mfma_f32_32x32x16_f16 v[18:33], v[88:91], v[96:99], v[18:33]
	ds_read_b128 v[128:131], v143 offset:4096
	v_mfma_f32_32x32x16_f16 v[2:17], v[88:91], v[100:103], v[2:17]
	ds_read_b128 v[132:135], v143 offset:8192
	s_waitcnt lgkmcnt(0)
	s_barrier
	v_mfma_f32_32x32x16_f16 v[34:49], v[104:107], v[108:111], v[34:49]
	ds_read_b128 v[72:75], v56
	ds_read_b128 v[76:79], v60
	v_mfma_f32_32x32x16_f16 v[18:33], v[104:107], v[112:115], v[18:33]
	ds_read_b128 v[80:83], v60 offset:4096
	ds_read_b128 v[84:87], v60 offset:8192
	v_mfma_f32_32x32x16_f16 v[2:17], v[104:107], v[116:119], v[2:17]
	ds_read_b128 v[88:91], v57
	v_mfma_f32_32x32x16_f16 v[34:49], v[120:123], v[124:127], v[34:49]
	ds_read_b128 v[92:95], v61
	v_mfma_f32_32x32x16_f16 v[18:33], v[120:123], v[128:131], v[18:33]
	ds_read_b128 v[96:99], v61 offset:4096
	v_mfma_f32_32x32x16_f16 v[2:17], v[120:123], v[132:135], v[2:17]
	ds_read_b128 v[100:103], v61 offset:8192
	s_waitcnt lgkmcnt(0)
	v_mfma_f32_32x32x16_f16 v[34:49], v[72:75], v[76:79], v[34:49]
	ds_read_b128 v[104:107], v58
	ds_read_b128 v[108:111], v62
	v_mfma_f32_32x32x16_f16 v[18:33], v[72:75], v[80:83], v[18:33]
	ds_read_b128 v[112:115], v62 offset:4096
	ds_read_b128 v[116:119], v62 offset:8192
	v_mfma_f32_32x32x16_f16 v[2:17], v[72:75], v[84:87], v[2:17]
	ds_read_b128 v[120:123], v59
	v_mfma_f32_32x32x16_f16 v[34:49], v[88:91], v[92:95], v[34:49]
	ds_read_b128 v[124:127], v63
	v_mfma_f32_32x32x16_f16 v[18:33], v[88:91], v[96:99], v[18:33]
	ds_read_b128 v[128:131], v63 offset:4096
	v_mfma_f32_32x32x16_f16 v[2:17], v[88:91], v[100:103], v[2:17]
	ds_read_b128 v[132:135], v63 offset:8192
	s_waitcnt lgkmcnt(0)
	s_barrier
	v_mfma_f32_32x32x16_f16 v[34:49], v[104:107], v[108:111], v[34:49]
	ds_read_b128 v[72:75], v56 offset:28672
	ds_read_b128 v[76:79], v60 offset:28672
	v_mfma_f32_32x32x16_f16 v[18:33], v[104:107], v[112:115], v[18:33]
	ds_read_b128 v[80:83], v60 offset:32768
	ds_read_b128 v[84:87], v60 offset:36864
	v_mfma_f32_32x32x16_f16 v[2:17], v[104:107], v[116:119], v[2:17]
	ds_read_b128 v[88:91], v57 offset:28672
	v_mfma_f32_32x32x16_f16 v[34:49], v[120:123], v[124:127], v[34:49]
	ds_read_b128 v[92:95], v61 offset:28672
	v_mfma_f32_32x32x16_f16 v[18:33], v[120:123], v[128:131], v[18:33]
	ds_read_b128 v[96:99], v61 offset:32768
	v_mfma_f32_32x32x16_f16 v[2:17], v[120:123], v[132:135], v[2:17]
	ds_read_b128 v[100:103], v61 offset:36864
	s_waitcnt lgkmcnt(0)
	v_mfma_f32_32x32x16_f16 v[34:49], v[72:75], v[76:79], v[34:49]
	ds_read_b128 v[104:107], v58 offset:28672
	ds_read_b128 v[108:111], v62 offset:28672
	v_mfma_f32_32x32x16_f16 v[18:33], v[72:75], v[80:83], v[18:33]
	ds_read_b128 v[112:115], v62 offset:32768
	ds_read_b128 v[116:119], v62 offset:36864
	v_mfma_f32_32x32x16_f16 v[2:17], v[72:75], v[84:87], v[2:17]
	ds_read_b128 v[120:123], v59 offset:28672
	v_mfma_f32_32x32x16_f16 v[34:49], v[88:91], v[92:95], v[34:49]
	ds_read_b128 v[124:127], v63 offset:28672
	v_mfma_f32_32x32x16_f16 v[18:33], v[88:91], v[96:99], v[18:33]
	ds_read_b128 v[128:131], v63 offset:32768
	v_mfma_f32_32x32x16_f16 v[2:17], v[88:91], v[100:103], v[2:17]
	ds_read_b128 v[132:135], v63 offset:36864
	s_waitcnt lgkmcnt(0)
	v_mfma_f32_32x32x16_f16 v[34:49], v[104:107], v[108:111], v[34:49]
	v_mfma_f32_32x32x16_f16 v[18:33], v[104:107], v[112:115], v[18:33]
	v_mfma_f32_32x32x16_f16 v[2:17], v[104:107], v[116:119], v[2:17]
	v_mfma_f32_32x32x16_f16 v[34:49], v[120:123], v[124:127], v[34:49]
	v_mfma_f32_32x32x16_f16 v[18:33], v[120:123], v[128:131], v[18:33]
	v_mfma_f32_32x32x16_f16 v[2:17], v[120:123], v[132:135], v[2:17]
	v_add_u32_e32 v51, s9, v51
	v_lshlrev_b32_e32 v104, 2, v51
	global_load_dword v105, v104, s[4:5]
	global_load_dword v106, v104, s[4:5] offset:128
	global_load_dword v107, v104, s[4:5] offset:256
	s_add_i32 s2, s2, s8
	v_lshl_add_u32 v108, v50, 2, s2
	v_mul_u32_u24_e32 v108, 0xc00, v108
	v_add_u32_e32 v108, v108, v104
	s_waitcnt vmcnt(0)
	s_nop 15
	v_add_f32_e32 v110, v105, v34
	v_add_f32_e32 v111, v106, v18
	v_add_f32_e32 v112, v107, v2
	global_store_dword v108, v110, s[6:7] nt
	global_store_dword v108, v111, s[6:7] offset:128 nt
	global_store_dword v108, v112, s[6:7] offset:256 nt
	v_add_u32_e32 v109, 0xc00, v108
	v_add_f32_e32 v110, v105, v35
	v_add_f32_e32 v111, v106, v19
	v_add_f32_e32 v112, v107, v3
	global_store_dword v109, v110, s[6:7] nt
	global_store_dword v109, v111, s[6:7] offset:128 nt
	global_store_dword v109, v112, s[6:7] offset:256 nt
	v_add_u32_e32 v109, 0x1800, v108
	v_add_f32_e32 v110, v105, v36
	v_add_f32_e32 v111, v106, v20
	v_add_f32_e32 v112, v107, v4
	global_store_dword v109, v110, s[6:7] nt
	global_store_dword v109, v111, s[6:7] offset:128 nt
	global_store_dword v109, v112, s[6:7] offset:256 nt
	v_add_u32_e32 v109, 0x2400, v108
	v_add_f32_e32 v110, v105, v37
	v_add_f32_e32 v111, v106, v21
	v_add_f32_e32 v112, v107, v5
	global_store_dword v109, v110, s[6:7] nt
	global_store_dword v109, v111, s[6:7] offset:128 nt
	global_store_dword v109, v112, s[6:7] offset:256 nt
	v_add_u32_e32 v109, 0x6000, v108
	v_add_f32_e32 v110, v105, v38
	v_add_f32_e32 v111, v106, v22
	v_add_f32_e32 v112, v107, v6
	global_store_dword v109, v110, s[6:7] nt
	global_store_dword v109, v111, s[6:7] offset:128 nt
	global_store_dword v109, v112, s[6:7] offset:256 nt
	v_add_u32_e32 v109, 0x6c00, v108
	v_add_f32_e32 v110, v105, v39
	v_add_f32_e32 v111, v106, v23
	v_add_f32_e32 v112, v107, v7
	global_store_dword v109, v110, s[6:7] nt
	global_store_dword v109, v111, s[6:7] offset:128 nt
	global_store_dword v109, v112, s[6:7] offset:256 nt
	v_add_u32_e32 v109, 0x7800, v108
	v_add_f32_e32 v110, v105, v40
	v_add_f32_e32 v111, v106, v24
	v_add_f32_e32 v112, v107, v8
	global_store_dword v109, v110, s[6:7] nt
	global_store_dword v109, v111, s[6:7] offset:128 nt
	global_store_dword v109, v112, s[6:7] offset:256 nt
	v_add_u32_e32 v109, 0x8400, v108
	v_add_f32_e32 v110, v105, v41
	v_add_f32_e32 v111, v106, v25
	v_add_f32_e32 v112, v107, v9
	global_store_dword v109, v110, s[6:7] nt
	global_store_dword v109, v111, s[6:7] offset:128 nt
	global_store_dword v109, v112, s[6:7] offset:256 nt
	v_add_u32_e32 v109, 0xc000, v108
	v_add_f32_e32 v110, v105, v42
	v_add_f32_e32 v111, v106, v26
	v_add_f32_e32 v112, v107, v10
	global_store_dword v109, v110, s[6:7] nt
	global_store_dword v109, v111, s[6:7] offset:128 nt
	global_store_dword v109, v112, s[6:7] offset:256 nt
	v_add_u32_e32 v109, 0xcc00, v108
	v_add_f32_e32 v110, v105, v43
	v_add_f32_e32 v111, v106, v27
	v_add_f32_e32 v112, v107, v11
	global_store_dword v109, v110, s[6:7] nt
	global_store_dword v109, v111, s[6:7] offset:128 nt
	global_store_dword v109, v112, s[6:7] offset:256 nt
	v_add_u32_e32 v109, 0xd800, v108
	v_add_f32_e32 v110, v105, v44
	v_add_f32_e32 v111, v106, v28
	v_add_f32_e32 v112, v107, v12
	global_store_dword v109, v110, s[6:7] nt
	global_store_dword v109, v111, s[6:7] offset:128 nt
	global_store_dword v109, v112, s[6:7] offset:256 nt
	v_add_u32_e32 v109, 0xe400, v108
	v_add_f32_e32 v110, v105, v45
	v_add_f32_e32 v111, v106, v29
	v_add_f32_e32 v112, v107, v13
	global_store_dword v109, v110, s[6:7] nt
	global_store_dword v109, v111, s[6:7] offset:128 nt
	global_store_dword v109, v112, s[6:7] offset:256 nt
	v_add_u32_e32 v109, 0x12000, v108
	v_add_f32_e32 v110, v105, v46
	v_add_f32_e32 v111, v106, v30
	v_add_f32_e32 v112, v107, v14
	global_store_dword v109, v110, s[6:7] nt
	global_store_dword v109, v111, s[6:7] offset:128 nt
	global_store_dword v109, v112, s[6:7] offset:256 nt
	v_add_u32_e32 v109, 0x12c00, v108
	v_add_f32_e32 v110, v105, v47
	v_add_f32_e32 v111, v106, v31
	v_add_f32_e32 v112, v107, v15
	global_store_dword v109, v110, s[6:7] nt
	global_store_dword v109, v111, s[6:7] offset:128 nt
	global_store_dword v109, v112, s[6:7] offset:256 nt
	v_add_u32_e32 v109, 0x13800, v108
	v_add_f32_e32 v110, v105, v48
	v_add_f32_e32 v111, v106, v32
	v_add_f32_e32 v112, v107, v16
	global_store_dword v109, v110, s[6:7] nt
	global_store_dword v109, v111, s[6:7] offset:128 nt
	global_store_dword v109, v112, s[6:7] offset:256 nt
	v_add_u32_e32 v109, 0x14400, v108
	v_add_f32_e32 v110, v105, v49
	v_add_f32_e32 v111, v106, v33
	v_add_f32_e32 v112, v107, v17
	global_store_dword v109, v110, s[6:7] nt
	global_store_dword v109, v111, s[6:7] offset:128 nt
	global_store_dword v109, v112, s[6:7] offset:256 nt
	s_endpgm
.LBB2_4:
	s_load_dwordx4 s[4:7], s[0:1], 0x0
	s_add_i32 s13, s13, -4
	v_lshrrev_b32_e32 v1, 3, v1
	v_and_b32_e32 v30, 7, v0
	s_mul_i32 s10, s8, 0x600
	s_mul_i32 s11, s9, 0x600
	s_waitcnt lgkmcnt(0)
	s_add_u32 s4, s4, s10
	s_addc_u32 s5, s5, 0
	s_add_u32 s6, s6, s11
	s_addc_u32 s7, s7, 0
	s_cmp_eq_u32 s13, 1
	s_cselect_b32 s14, s6, s4
	s_cselect_b32 s15, s7, s5
	s_cselect_b32 s16, -16, 0
	s_mul_i32 s17, s13, 112
	v_add_u32_e32 v31, s17, v1
	v_bfe_u32 v32, v31, 1, 3
	v_xor_b32_e32 v32, v32, v30
	v_mul_u32_u24_e32 v2, 0x600, v31
	v_lshl_add_u32 v2, v32, 4, v2
	v_mov_b32_e32 v3, 0
	v_lshl_add_u64 v[2:3], v[2:3], 0, s[4:5]
	v_add_u32_e32 v31, s17, v1
	v_add_u32_e32 v31, 8, v31
	v_bfe_u32 v32, v31, 1, 3
	v_xor_b32_e32 v32, v32, v30
	v_mul_u32_u24_e32 v4, 0x600, v31
	v_lshl_add_u32 v4, v32, 4, v4
	v_mov_b32_e32 v5, 0
	v_lshl_add_u64 v[4:5], v[4:5], 0, s[4:5]
	v_add_u32_e32 v31, s16, v1
	v_add_u32_e32 v31, 16, v31
	v_bfe_u32 v32, v31, 1, 3
	v_xor_b32_e32 v32, v32, v30
	v_mul_u32_u24_e32 v6, 0x600, v31
	v_lshl_add_u32 v6, v32, 4, v6
	v_mov_b32_e32 v7, 0
	v_lshl_add_u64 v[6:7], v[6:7], 0, s[14:15]
	v_add_u32_e32 v31, s16, v1
	v_add_u32_e32 v31, 24, v31
	v_bfe_u32 v32, v31, 1, 3
	v_xor_b32_e32 v32, v32, v30
	v_mul_u32_u24_e32 v8, 0x600, v31
	v_lshl_add_u32 v8, v32, 4, v8
	v_mov_b32_e32 v9, 0
	v_lshl_add_u64 v[8:9], v[8:9], 0, s[14:15]
	v_add_u32_e32 v31, s16, v1
	v_add_u32_e32 v31, 32, v31
	v_bfe_u32 v32, v31, 1, 3
	v_xor_b32_e32 v32, v32, v30
	v_mul_u32_u24_e32 v10, 0x600, v31
	v_lshl_add_u32 v10, v32, 4, v10
	v_mov_b32_e32 v11, 0
	v_lshl_add_u64 v[10:11], v[10:11], 0, s[14:15]
	v_add_u32_e32 v31, s16, v1
	v_add_u32_e32 v31, 40, v31
	v_bfe_u32 v32, v31, 1, 3
	v_xor_b32_e32 v32, v32, v30
	v_mul_u32_u24_e32 v12, 0x600, v31
	v_lshl_add_u32 v12, v32, 4, v12
	v_mov_b32_e32 v13, 0
	v_lshl_add_u64 v[12:13], v[12:13], 0, s[14:15]
	v_add_u32_e32 v31, s16, v1
	v_add_u32_e32 v31, 48, v31
	v_bfe_u32 v32, v31, 1, 3
	v_xor_b32_e32 v32, v32, v30
	v_mul_u32_u24_e32 v14, 0x600, v31
	v_lshl_add_u32 v14, v32, 4, v14
	v_mov_b32_e32 v15, 0
	v_lshl_add_u64 v[14:15], v[14:15], 0, s[14:15]
	v_add_u32_e32 v31, s16, v1
	v_add_u32_e32 v31, 56, v31
	v_bfe_u32 v32, v31, 1, 3
	v_xor_b32_e32 v32, v32, v30
	v_mul_u32_u24_e32 v16, 0x600, v31
	v_lshl_add_u32 v16, v32, 4, v16
	v_mov_b32_e32 v17, 0
	v_lshl_add_u64 v[16:17], v[16:17], 0, s[14:15]
	v_add_u32_e32 v31, s16, v1
	v_add_u32_e32 v31, 64, v31
	v_bfe_u32 v32, v31, 1, 3
	v_xor_b32_e32 v32, v32, v30
	v_mul_u32_u24_e32 v18, 0x600, v31
	v_lshl_add_u32 v18, v32, 4, v18
	v_mov_b32_e32 v19, 0
	v_lshl_add_u64 v[18:19], v[18:19], 0, s[14:15]
	v_add_u32_e32 v31, s16, v1
	v_add_u32_e32 v31, 72, v31
	v_bfe_u32 v32, v31, 1, 3
	v_xor_b32_e32 v32, v32, v30
	v_mul_u32_u24_e32 v20, 0x600, v31
	v_lshl_add_u32 v20, v32, 4, v20
	v_mov_b32_e32 v21, 0
	v_lshl_add_u64 v[20:21], v[20:21], 0, s[14:15]
	v_add_u32_e32 v31, s16, v1
	v_add_u32_e32 v31, 80, v31
	v_bfe_u32 v32, v31, 1, 3
	v_xor_b32_e32 v32, v32, v30
	v_mul_u32_u24_e32 v22, 0x600, v31
	v_lshl_add_u32 v22, v32, 4, v22
	v_mov_b32_e32 v23, 0
	v_lshl_add_u64 v[22:23], v[22:23], 0, s[14:15]
	v_add_u32_e32 v31, s16, v1
	v_add_u32_e32 v31, 88, v31
	v_bfe_u32 v32, v31, 1, 3
	v_xor_b32_e32 v32, v32, v30
	v_mul_u32_u24_e32 v24, 0x600, v31
	v_lshl_add_u32 v24, v32, 4, v24
	v_mov_b32_e32 v25, 0
	v_lshl_add_u64 v[24:25], v[24:25], 0, s[14:15]
	v_add_u32_e32 v31, s16, v1
	v_add_u32_e32 v31, 96, v31
	v_bfe_u32 v32, v31, 1, 3
	v_xor_b32_e32 v32, v32, v30
	v_mul_u32_u24_e32 v26, 0x600, v31
	v_lshl_add_u32 v26, v32, 4, v26
	v_mov_b32_e32 v27, 0
	v_lshl_add_u64 v[26:27], v[26:27], 0, s[14:15]
	v_add_u32_e32 v31, s16, v1
	v_add_u32_e32 v31, 104, v31
	v_bfe_u32 v32, v31, 1, 3
	v_xor_b32_e32 v32, v32, v30
	v_mul_u32_u24_e32 v28, 0x600, v31
	v_lshl_add_u32 v28, v32, 4, v28
	v_mov_b32_e32 v29, 0
	v_lshl_add_u64 v[28:29], v[28:29], 0, s[14:15]
	s_mul_i32 s18, s13, 0x3800
	s_add_i32 m0, s18, 2048
	s_nop 0
	global_load_lds_dwordx4 v[2:3], off
	s_add_i32 m0, s18, 3072
	s_nop 0
	global_load_lds_dwordx4 v[4:5], off
	s_add_i32 m0, s18, 4096
	s_nop 0
	global_load_lds_dwordx4 v[6:7], off
	s_add_i32 m0, s18, 5120
	s_nop 0
	global_load_lds_dwordx4 v[8:9], off
	s_add_i32 m0, s18, 6144
	s_nop 0
	global_load_lds_dwordx4 v[10:11], off
	s_add_i32 m0, s18, 7168
	s_nop 0
	global_load_lds_dwordx4 v[12:13], off
	s_add_i32 m0, s18, 8192
	s_nop 0
	global_load_lds_dwordx4 v[14:15], off
	s_add_i32 m0, s18, 9216
	s_nop 0
	global_load_lds_dwordx4 v[16:17], off
	s_add_i32 m0, s18, 10240
	s_nop 0
	global_load_lds_dwordx4 v[18:19], off
	s_add_i32 m0, s18, 11264
	s_nop 0
	global_load_lds_dwordx4 v[20:21], off
	s_add_i32 m0, s18, 12288
	s_nop 0
	global_load_lds_dwordx4 v[22:23], off
	s_add_i32 m0, s18, 13312
	s_nop 0
	global_load_lds_dwordx4 v[24:25], off
	s_add_i32 m0, s18, 14336
	s_nop 0
	global_load_lds_dwordx4 v[26:27], off
	s_add_i32 m0, s18, 15360
	s_nop 0
	global_load_lds_dwordx4 v[28:29], off
	s_add_i32 m0, s18, 30592
	s_nop 0
	global_load_lds_dwordx4 v[2:3], off offset:128
	s_add_i32 m0, s18, 31616
	s_nop 0
	global_load_lds_dwordx4 v[4:5], off offset:128
	s_add_i32 m0, s18, 32640
	s_nop 0
	global_load_lds_dwordx4 v[6:7], off offset:128
	s_add_i32 m0, s18, 33664
	s_nop 0
	global_load_lds_dwordx4 v[8:9], off offset:128
	s_add_i32 m0, s18, 34688
	s_nop 0
	global_load_lds_dwordx4 v[10:11], off offset:128
	s_add_i32 m0, s18, 35712
	s_nop 0
	global_load_lds_dwordx4 v[12:13], off offset:128
	s_add_i32 m0, s18, 36736
	s_nop 0
	global_load_lds_dwordx4 v[14:15], off offset:128
	s_add_i32 m0, s18, 37760
	s_nop 0
	global_load_lds_dwordx4 v[16:17], off offset:128
	s_add_i32 m0, s18, 38784
	s_nop 0
	global_load_lds_dwordx4 v[18:19], off offset:128
	s_add_i32 m0, s18, 39808
	s_nop 0
	global_load_lds_dwordx4 v[20:21], off offset:128
	s_add_i32 m0, s18, 40832
	s_nop 0
	global_load_lds_dwordx4 v[22:23], off offset:128
	s_add_i32 m0, s18, 41856
	s_nop 0
	global_load_lds_dwordx4 v[24:25], off offset:128
	s_add_i32 m0, s18, 42880
	s_nop 0
	global_load_lds_dwordx4 v[26:27], off offset:128
	s_add_i32 m0, s18, 43904
	s_nop 0
	global_load_lds_dwordx4 v[28:29], off offset:128
	s_add_i32 m0, s18, 59136
	s_nop 0
	global_load_lds_dwordx4 v[2:3], off offset:256
	s_add_i32 m0, s18, 60160
	s_nop 0
	global_load_lds_dwordx4 v[4:5], off offset:256
	s_add_i32 m0, s18, 61184
	s_nop 0
	global_load_lds_dwordx4 v[6:7], off offset:256
	s_add_i32 m0, s18, 62208
	s_nop 0
	global_load_lds_dwordx4 v[8:9], off offset:256
	s_add_i32 m0, s18, 63232
	s_nop 0
	global_load_lds_dwordx4 v[10:11], off offset:256
	s_add_i32 m0, s18, 64256
	s_nop 0
	global_load_lds_dwordx4 v[12:13], off offset:256
	s_add_i32 m0, s18, 65280
	s_nop 0
	global_load_lds_dwordx4 v[14:15], off offset:256
	s_add_i32 m0, s18, 66304
	s_nop 0
	global_load_lds_dwordx4 v[16:17], off offset:256
	s_add_i32 m0, s18, 67328
	s_nop 0
	global_load_lds_dwordx4 v[18:19], off offset:256
	s_add_i32 m0, s18, 68352
	s_nop 0
	global_load_lds_dwordx4 v[20:21], off offset:256
	s_add_i32 m0, s18, 69376
	s_nop 0
	global_load_lds_dwordx4 v[22:23], off offset:256
	s_add_i32 m0, s18, 70400
	s_nop 0
	global_load_lds_dwordx4 v[24:25], off offset:256
	s_add_i32 m0, s18, 71424
	s_nop 0
	global_load_lds_dwordx4 v[26:27], off offset:256
	s_add_i32 m0, s18, 72448
	s_nop 0
	global_load_lds_dwordx4 v[28:29], off offset:256
	s_add_i32 m0, s18, 87680
	s_nop 0
	global_load_lds_dwordx4 v[2:3], off offset:384
	s_add_i32 m0, s18, 88704
	s_nop 0
	global_load_lds_dwordx4 v[4:5], off offset:384
	s_add_i32 m0, s18, 89728
	s_nop 0
	global_load_lds_dwordx4 v[6:7], off offset:384
	s_add_i32 m0, s18, 90752
	s_nop 0
	global_load_lds_dwordx4 v[8:9], off offset:384
	s_add_i32 m0, s18, 91776
	s_nop 0
	global_load_lds_dwordx4 v[10:11], off offset:384
	s_add_i32 m0, s18, 92800
	s_nop 0
	global_load_lds_dwordx4 v[12:13], off offset:384
	s_add_i32 m0, s18, 93824
	s_nop 0
	global_load_lds_dwordx4 v[14:15], off offset:384
	s_add_i32 m0, s18, 94848
	s_nop 0
	global_load_lds_dwordx4 v[16:17], off offset:384
	s_add_i32 m0, s18, 95872
	s_nop 0
	global_load_lds_dwordx4 v[18:19], off offset:384
	s_add_i32 m0, s18, 96896
	s_nop 0
	global_load_lds_dwordx4 v[20:21], off offset:384
	s_add_i32 m0, s18, 97920
	s_nop 0
	global_load_lds_dwordx4 v[22:23], off offset:384
	s_add_i32 m0, s18, 98944
	s_nop 0
	global_load_lds_dwordx4 v[24:25], off offset:384
	s_add_i32 m0, s18, 99968
	s_nop 0
	global_load_lds_dwordx4 v[26:27], off offset:384
	s_add_i32 m0, s18, 100992
	s_nop 0
	global_load_lds_dwordx4 v[28:29], off offset:384
	s_waitcnt vmcnt(42)
	s_barrier
	s_add_i32 m0, s18, 116224
	s_nop 0
	global_load_lds_dwordx4 v[2:3], off offset:512
	s_add_i32 m0, s18, 117248
	s_nop 0
	global_load_lds_dwordx4 v[4:5], off offset:512
	s_add_i32 m0, s18, 118272
	s_nop 0
	global_load_lds_dwordx4 v[6:7], off offset:512
	s_add_i32 m0, s18, 119296
	s_nop 0
	global_load_lds_dwordx4 v[8:9], off offset:512
	s_add_i32 m0, s18, 120320
	s_nop 0
	global_load_lds_dwordx4 v[10:11], off offset:512
	s_add_i32 m0, s18, 121344
	s_nop 0
	global_load_lds_dwordx4 v[12:13], off offset:512
	s_add_i32 m0, s18, 122368
	s_nop 0
	global_load_lds_dwordx4 v[14:15], off offset:512
	s_add_i32 m0, s18, 123392
	s_nop 0
	global_load_lds_dwordx4 v[16:17], off offset:512
	s_add_i32 m0, s18, 124416
	s_nop 0
	global_load_lds_dwordx4 v[18:19], off offset:512
	s_add_i32 m0, s18, 125440
	s_nop 0
	global_load_lds_dwordx4 v[20:21], off offset:512
	s_add_i32 m0, s18, 126464
	s_nop 0
	global_load_lds_dwordx4 v[22:23], off offset:512
	s_add_i32 m0, s18, 127488
	s_nop 0
	global_load_lds_dwordx4 v[24:25], off offset:512
	s_add_i32 m0, s18, 128512
	s_nop 0
	global_load_lds_dwordx4 v[26:27], off offset:512
	s_add_i32 m0, s18, 129536
	s_nop 0
	global_load_lds_dwordx4 v[28:29], off offset:512
	s_waitcnt vmcnt(42)
	s_barrier
	s_add_i32 m0, s18, 1408
	s_nop 0
	global_load_lds_dwordx4 v[2:3], off offset:640
	s_add_i32 m0, s18, 2432
	s_nop 0
	global_load_lds_dwordx4 v[4:5], off offset:640
	s_add_i32 m0, s18, 3456
	s_nop 0
	global_load_lds_dwordx4 v[6:7], off offset:640
	s_add_i32 m0, s18, 4480
	s_nop 0
	global_load_lds_dwordx4 v[8:9], off offset:640
	s_add_i32 m0, s18, 5504
	s_nop 0
	global_load_lds_dwordx4 v[10:11], off offset:640
	s_add_i32 m0, s18, 6528
	s_nop 0
	global_load_lds_dwordx4 v[12:13], off offset:640
	s_add_i32 m0, s18, 7552
	s_nop 0
	global_load_lds_dwordx4 v[14:15], off offset:640
	s_add_i32 m0, s18, 8576
	s_nop 0
	global_load_lds_dwordx4 v[16:17], off offset:640
	s_add_i32 m0, s18, 9600
	s_nop 0
	global_load_lds_dwordx4 v[18:19], off offset:640
	s_add_i32 m0, s18, 10624
	s_nop 0
	global_load_lds_dwordx4 v[20:21], off offset:640
	s_add_i32 m0, s18, 11648
	s_nop 0
	global_load_lds_dwordx4 v[22:23], off offset:640
	s_add_i32 m0, s18, 12672
	s_nop 0
	global_load_lds_dwordx4 v[24:25], off offset:640
	s_add_i32 m0, s18, 13696
	s_nop 0
	global_load_lds_dwordx4 v[26:27], off offset:640
	s_add_i32 m0, s18, 14720
	s_nop 0
	global_load_lds_dwordx4 v[28:29], off offset:640
	s_waitcnt vmcnt(42)
	s_barrier
	s_add_i32 m0, s18, 29952
	s_nop 0
	global_load_lds_dwordx4 v[2:3], off offset:768
	s_add_i32 m0, s18, 30976
	s_nop 0
	global_load_lds_dwordx4 v[4:5], off offset:768
	s_add_i32 m0, s18, 32000
	s_nop 0
	global_load_lds_dwordx4 v[6:7], off offset:768
	s_add_i32 m0, s18, 33024
	s_nop 0
	global_load_lds_dwordx4 v[8:9], off offset:768
	s_add_i32 m0, s18, 34048
	s_nop 0
	global_load_lds_dwordx4 v[10:11], off offset:768
	s_add_i32 m0, s18, 35072
	s_nop 0
	global_load_lds_dwordx4 v[12:13], off offset:768
	s_add_i32 m0, s18, 36096
	s_nop 0
	global_load_lds_dwordx4 v[14:15], off offset:768
	s_add_i32 m0, s18, 37120
	s_nop 0
	global_load_lds_dwordx4 v[16:17], off offset:768
	s_add_i32 m0, s18, 38144
	s_nop 0
	global_load_lds_dwordx4 v[18:19], off offset:768
	s_add_i32 m0, s18, 39168
	s_nop 0
	global_load_lds_dwordx4 v[20:21], off offset:768
	s_add_i32 m0, s18, 40192
	s_nop 0
	global_load_lds_dwordx4 v[22:23], off offset:768
	s_add_i32 m0, s18, 41216
	s_nop 0
	global_load_lds_dwordx4 v[24:25], off offset:768
	s_add_i32 m0, s18, 42240
	s_nop 0
	global_load_lds_dwordx4 v[26:27], off offset:768
	s_add_i32 m0, s18, 43264
	s_nop 0
	global_load_lds_dwordx4 v[28:29], off offset:768
	s_waitcnt vmcnt(42)
	s_barrier
	s_add_i32 m0, s18, 58496
	s_nop 0
	global_load_lds_dwordx4 v[2:3], off offset:896
	s_add_i32 m0, s18, 59520
	s_nop 0
	global_load_lds_dwordx4 v[4:5], off offset:896
	s_add_i32 m0, s18, 60544
	s_nop 0
	global_load_lds_dwordx4 v[6:7], off offset:896
	s_add_i32 m0, s18, 61568
	s_nop 0
	global_load_lds_dwordx4 v[8:9], off offset:896
	s_add_i32 m0, s18, 62592
	s_nop 0
	global_load_lds_dwordx4 v[10:11], off offset:896
	s_add_i32 m0, s18, 63616
	s_nop 0
	global_load_lds_dwordx4 v[12:13], off offset:896
	s_add_i32 m0, s18, 64640
	s_nop 0
	global_load_lds_dwordx4 v[14:15], off offset:896
	s_add_i32 m0, s18, 65664
	s_nop 0
	global_load_lds_dwordx4 v[16:17], off offset:896
	s_add_i32 m0, s18, 66688
	s_nop 0
	global_load_lds_dwordx4 v[18:19], off offset:896
	s_add_i32 m0, s18, 67712
	s_nop 0
	global_load_lds_dwordx4 v[20:21], off offset:896
	s_add_i32 m0, s18, 68736
	s_nop 0
	global_load_lds_dwordx4 v[22:23], off offset:896
	s_add_i32 m0, s18, 69760
	s_nop 0
	global_load_lds_dwordx4 v[24:25], off offset:896
	s_add_i32 m0, s18, 70784
	s_nop 0
	global_load_lds_dwordx4 v[26:27], off offset:896
	s_add_i32 m0, s18, 71808
	s_nop 0
	global_load_lds_dwordx4 v[28:29], off offset:896
	s_waitcnt vmcnt(42)
	s_barrier
	s_add_i32 m0, s18, 87040
	s_nop 0
	global_load_lds_dwordx4 v[2:3], off offset:1024
	s_add_i32 m0, s18, 88064
	s_nop 0
	global_load_lds_dwordx4 v[4:5], off offset:1024
	s_add_i32 m0, s18, 89088
	s_nop 0
	global_load_lds_dwordx4 v[6:7], off offset:1024
	s_add_i32 m0, s18, 90112
	s_nop 0
	global_load_lds_dwordx4 v[8:9], off offset:1024
	s_add_i32 m0, s18, 91136
	s_nop 0
	global_load_lds_dwordx4 v[10:11], off offset:1024
	s_add_i32 m0, s18, 92160
	s_nop 0
	global_load_lds_dwordx4 v[12:13], off offset:1024
	s_add_i32 m0, s18, 93184
	s_nop 0
	global_load_lds_dwordx4 v[14:15], off offset:1024
	s_add_i32 m0, s18, 94208
	s_nop 0
	global_load_lds_dwordx4 v[16:17], off offset:1024
	s_add_i32 m0, s18, 95232
	s_nop 0
	global_load_lds_dwordx4 v[18:19], off offset:1024
	s_add_i32 m0, s18, 96256
	s_nop 0
	global_load_lds_dwordx4 v[20:21], off offset:1024
	s_add_i32 m0, s18, 97280
	s_nop 0
	global_load_lds_dwordx4 v[22:23], off offset:1024
	s_add_i32 m0, s18, 98304
	s_nop 0
	global_load_lds_dwordx4 v[24:25], off offset:1024
	s_add_i32 m0, s18, 99328
	s_nop 0
	global_load_lds_dwordx4 v[26:27], off offset:1024
	s_add_i32 m0, s18, 100352
	s_nop 0
	global_load_lds_dwordx4 v[28:29], off offset:1024
	s_waitcnt vmcnt(42)
	s_barrier
	s_add_i32 m0, s18, 115584
	s_nop 0
	global_load_lds_dwordx4 v[2:3], off offset:1152
	s_add_i32 m0, s18, 116608
	s_nop 0
	global_load_lds_dwordx4 v[4:5], off offset:1152
	s_add_i32 m0, s18, 117632
	s_nop 0
	global_load_lds_dwordx4 v[6:7], off offset:1152
	s_add_i32 m0, s18, 118656
	s_nop 0
	global_load_lds_dwordx4 v[8:9], off offset:1152
	s_add_i32 m0, s18, 119680
	s_nop 0
	global_load_lds_dwordx4 v[10:11], off offset:1152
	s_add_i32 m0, s18, 120704
	s_nop 0
	global_load_lds_dwordx4 v[12:13], off offset:1152
	s_add_i32 m0, s18, 121728
	s_nop 0
	global_load_lds_dwordx4 v[14:15], off offset:1152
	s_add_i32 m0, s18, 122752
	s_nop 0
	global_load_lds_dwordx4 v[16:17], off offset:1152
	s_add_i32 m0, s18, 123776
	s_nop 0
	global_load_lds_dwordx4 v[18:19], off offset:1152
	s_add_i32 m0, s18, 124800
	s_nop 0
	global_load_lds_dwordx4 v[20:21], off offset:1152
	s_add_i32 m0, s18, 125824
	s_nop 0
	global_load_lds_dwordx4 v[22:23], off offset:1152
	s_add_i32 m0, s18, 126848
	s_nop 0
	global_load_lds_dwordx4 v[24:25], off offset:1152
	s_add_i32 m0, s18, 127872
	s_nop 0
	global_load_lds_dwordx4 v[26:27], off offset:1152
	s_add_i32 m0, s18, 128896
	s_nop 0
	global_load_lds_dwordx4 v[28:29], off offset:1152
	s_waitcnt vmcnt(42)
	s_barrier
	s_add_i32 m0, s18, 768
	s_nop 0
	global_load_lds_dwordx4 v[2:3], off offset:1280
	s_add_i32 m0, s18, 1792
	s_nop 0
	global_load_lds_dwordx4 v[4:5], off offset:1280
	s_add_i32 m0, s18, 2816
	s_nop 0
	global_load_lds_dwordx4 v[6:7], off offset:1280
	s_add_i32 m0, s18, 3840
	s_nop 0
	global_load_lds_dwordx4 v[8:9], off offset:1280
	s_add_i32 m0, s18, 4864
	s_nop 0
	global_load_lds_dwordx4 v[10:11], off offset:1280
	s_add_i32 m0, s18, 5888
	s_nop 0
	global_load_lds_dwordx4 v[12:13], off offset:1280
	s_add_i32 m0, s18, 6912
	s_nop 0
	global_load_lds_dwordx4 v[14:15], off offset:1280
	s_add_i32 m0, s18, 7936
	s_nop 0
	global_load_lds_dwordx4 v[16:17], off offset:1280
	s_add_i32 m0, s18, 8960
	s_nop 0
	global_load_lds_dwordx4 v[18:19], off offset:1280
	s_add_i32 m0, s18, 9984
	s_nop 0
	global_load_lds_dwordx4 v[20:21], off offset:1280
	s_add_i32 m0, s18, 11008
	s_nop 0
	global_load_lds_dwordx4 v[22:23], off offset:1280
	s_add_i32 m0, s18, 12032
	s_nop 0
	global_load_lds_dwordx4 v[24:25], off offset:1280
	s_add_i32 m0, s18, 13056
	s_nop 0
	global_load_lds_dwordx4 v[26:27], off offset:1280
	s_add_i32 m0, s18, 14080
	s_nop 0
	global_load_lds_dwordx4 v[28:29], off offset:1280
	s_waitcnt vmcnt(42)
	s_barrier
	s_add_i32 m0, s18, 29312
	s_nop 0
	global_load_lds_dwordx4 v[2:3], off offset:1408
	s_add_i32 m0, s18, 30336
	s_nop 0
	global_load_lds_dwordx4 v[4:5], off offset:1408
	s_add_i32 m0, s18, 31360
	s_nop 0
	global_load_lds_dwordx4 v[6:7], off offset:1408
	s_add_i32 m0, s18, 32384
	s_nop 0
	global_load_lds_dwordx4 v[8:9], off offset:1408
	s_add_i32 m0, s18, 33408
	s_nop 0
	global_load_lds_dwordx4 v[10:11], off offset:1408
	s_add_i32 m0, s18, 34432
	s_nop 0
	global_load_lds_dwordx4 v[12:13], off offset:1408
	s_add_i32 m0, s18, 35456
	s_nop 0
	global_load_lds_dwordx4 v[14:15], off offset:1408
	s_add_i32 m0, s18, 36480
	s_nop 0
	global_load_lds_dwordx4 v[16:17], off offset:1408
	s_add_i32 m0, s18, 37504
	s_nop 0
	global_load_lds_dwordx4 v[18:19], off offset:1408
	s_add_i32 m0, s18, 38528
	s_nop 0
	global_load_lds_dwordx4 v[20:21], off offset:1408
	s_add_i32 m0, s18, 39552
	s_nop 0
	global_load_lds_dwordx4 v[22:23], off offset:1408
	s_add_i32 m0, s18, 40576
	s_nop 0
	global_load_lds_dwordx4 v[24:25], off offset:1408
	s_add_i32 m0, s18, 41600
	s_nop 0
	global_load_lds_dwordx4 v[26:27], off offset:1408
	s_add_i32 m0, s18, 42624
	s_nop 0
	global_load_lds_dwordx4 v[28:29], off offset:1408
	s_waitcnt vmcnt(42)
	s_barrier
	s_waitcnt vmcnt(28)
	s_barrier
	s_waitcnt vmcnt(14)
	s_barrier
	s_waitcnt vmcnt(0)
	s_barrier
	s_endpgm

	.amdhsa_kernel _Z15out_proj_kernelPKDF16_S0_PKfPf
		.amdhsa_group_segment_fixed_size 30720
		.amdhsa_private_segment_fixed_size 0
		.amdhsa_kernarg_size 32
		.amdhsa_user_sgpr_count 2
		.amdhsa_user_sgpr_dispatch_ptr 0
		.amdhsa_user_sgpr_queue_ptr 0
		.amdhsa_user_sgpr_kernarg_segment_ptr 1
		.amdhsa_user_sgpr_dispatch_id 0
		.amdhsa_user_sgpr_kernarg_preload_length 0
		.amdhsa_user_sgpr_kernarg_preload_offset 0
		.amdhsa_user_sgpr_private_segment_size 0
		.amdhsa_uses_dynamic_stack 0
		.amdhsa_enable_private_segment 0
		.amdhsa_system_sgpr_workgroup_id_x 1
		.amdhsa_system_sgpr_workgroup_id_y 0
		.amdhsa_system_sgpr_workgroup_id_z 0
		.amdhsa_system_sgpr_workgroup_info 0
		.amdhsa_system_vgpr_workitem_id 0
		.amdhsa_next_free_vgpr 144
		.amdhsa_next_free_sgpr 61
		.amdhsa_accum_offset 144
		.amdhsa_reserve_vcc 1
		.amdhsa_float_round_mode_32 0
		.amdhsa_float_round_mode_16_64 0
		.amdhsa_float_denorm_mode_32 3
		.amdhsa_float_denorm_mode_16_64 3
		.amdhsa_dx10_clamp 1
		.amdhsa_ieee_mode 1
		.amdhsa_fp16_overflow 0
		.amdhsa_tg_split 0
		.amdhsa_exception_fp_ieee_invalid_op 0
		.amdhsa_exception_fp_denorm_src 0
		.amdhsa_exception_fp_ieee_div_zero 0
		.amdhsa_exception_fp_ieee_overflow 0
		.amdhsa_exception_fp_ieee_underflow 0
		.amdhsa_exception_fp_ieee_inexact 0
		.amdhsa_exception_int_div_zero 0
	.end_amdhsa_kernel

_Z11attn_kernelPKDF16_S0_S0_PDF16_P15HIP_vector_typeIfLj2EE:
	s_mov_b32 s28, s2
	s_mov_b64 s[30:31], s[0:1]
	v_readfirstlane_b32 s3, v0
	s_ashr_i32 s12, s2, 5
	s_lshr_b32 s21, s3, 6
	s_and_b32 s3, s2, 7
	s_and_b32 s12, s12, -8
	s_load_dwordx8 s[4:11], s[0:1], 0x0
	s_or_b32 s12, s12, s3
	s_bfe_u32 s20, s2, 0x10003
	s_lshl_b32 s2, s2, 3
	s_and_b32 s2, s2, 0x780
	s_lshl_b32 s3, s21, 5
	s_ashr_i32 s13, s12, 31
	s_add_i32 s2, s3, s2
	s_lshl_b64 s[16:17], s[12:13], 11
	s_lshl_b32 s3, s20, 10
	s_or_b32 s14, s16, s3
	s_mov_b32 s15, s17
	s_lshl_b64 s[18:19], s[14:15], 7
	s_lshl_b64 s[14:15], s[12:13], 18
	s_waitcnt lgkmcnt(0)
	s_add_u32 s3, s8, s14
	s_addc_u32 s22, s9, s15
	s_add_u32 s16, s16, s2
	v_and_b32_e32 v98, 31, v0
	s_addc_u32 s17, s17, 0
	v_or_b32_e32 v2, s16, v98
	v_mov_b32_e32 v3, s17
	v_bfe_u32 v54, v0, 5, 1
	v_lshlrev_b64 v[2:3], 7, v[2:3]
	v_mov_b32_e32 v51, 0
	v_lshl_add_u64 v[2:3], s[4:5], 0, v[2:3]
	v_lshlrev_b32_e32 v50, 4, v54
	v_lshl_add_u64 v[2:3], v[2:3], 0, v[50:51]
	s_add_u32 s18, s6, s18
	v_bfe_u32 v1, v0, 3, 3
	global_load_dwordx4 v[94:97], v[2:3], off nt
	global_load_dwordx4 v[90:93], v[2:3], off offset:32 nt
	global_load_dwordx4 v[86:89], v[2:3], off offset:64 nt
	global_load_dwordx4 v[82:85], v[2:3], off offset:96 nt
	s_addc_u32 s19, s7, s19
	s_lshl_b32 s24, s20, 11
	v_lshl_or_b32 v2, s21, 4, v1
	v_and_b32_e32 v99, 63, v0
	s_add_u32 s4, s3, s24
	v_or_b32_e32 v3, 8, v2
	v_lshlrev_b32_e32 v4, 4, v0
	s_movk_i32 s3, 0x70
	v_bitop3_b32 v53, v99, s3, v4 bitop3:0x48
	v_lshrrev_b32_e32 v4, 1, v3
	v_xor_b32_e32 v4, v4, v0
	s_addc_u32 s5, s22, 0
	v_lshlrev_b32_e32 v4, 4, v4
	s_lshl_b32 s22, s21, 11
	v_and_b32_e32 v52, 0x70, v4
	v_lshl_or_b32 v55, v2, 7, v53
	s_mov_b32 m0, s22
	v_lshl_or_b32 v64, v3, 7, v52
	global_load_lds_dwordx4 v55, s[18:19]
	s_or_b32 m0, s22, 0x400
	v_lshl_or_b32 v50, v2, 12, v53
	global_load_lds_dwordx4 v64, s[18:19]
	s_add_i32 m0, s22, 0x2000
	v_lshl_or_b32 v2, v3, 12, v52
	global_load_lds_dwordx4 v50, s[4:5]
	s_add_i32 m0, s22, 0x2400
	v_mov_b32_e32 v3, v51
	global_load_lds_dwordx4 v2, s[4:5]
	s_add_i32 m0, s22, 0x4000
	v_lshl_add_u64 v[60:61], s[4:5], 0, v[50:51]
	v_lshl_add_u64 v[62:63], s[4:5], 0, v[2:3]
	s_add_u32 s4, s18, 0x2000
	s_addc_u32 s5, s19, 0
	global_load_lds_dwordx4 v55, s[4:5]
	s_add_i32 m0, s22, 0x4400
	s_load_dwordx2 s[0:1], s[0:1], 0x20
	global_load_lds_dwordx4 v64, s[4:5]
	s_mov_b64 s[4:5], 0x80
	v_lshl_add_u64 v[2:3], v[60:61], 0, s[4:5]
	s_add_i32 m0, s22, 0x6000
	v_lshrrev_b32_e32 v4, 1, v0
	global_load_lds_dwordx4 v[2:3], off
	v_lshl_add_u64 v[2:3], v[62:63], 0, s[4:5]
	s_add_i32 m0, s22, 0x6400
	v_and_b32_e32 v5, 4, v4
	global_load_lds_dwordx4 v[2:3], off
	v_lshlrev_b32_e32 v3, 1, v0
	v_and_b32_e32 v2, 19, v0
	v_and_b32_e32 v3, 8, v3
	v_or3_b32 v2, v3, v2, v5
	s_waitcnt vmcnt(4)
	v_lshlrev_b32_e32 v115, 7, v2
	v_lshrrev_b32_e32 v3, 1, v2
	v_bfe_u32 v46, v2, 1, 3
	v_bitop3_b32 v2, v54, v4, 7 bitop3:0x78
	s_mov_b32 s3, 0
	v_lshlrev_b32_e32 v108, 3, v54
	s_mov_b32 s23, 1
	s_mov_b64 s[16:17], 0x2000
	v_lshlrev_b32_e32 v109, 7, v98
	v_lshlrev_b32_e32 v110, 4, v2
	s_movk_i32 s25, 0x400
	v_bfe_u32 v50, v0, 1, 3
	s_barrier
	v_bitop3_b32 v2, v54, v3, 7 bitop3:0x78
	v_lshlrev_b32_e32 v116, 4, v2
	v_or_b32_e32 v6, v115, v116
	ds_read_b128 v[2:5], v6
	ds_read_b128 v[18:21], v6 offset:4096
	v_bitop3_b32 v6, v54, v46, 2 bitop3:0x36
	v_lshlrev_b32_e32 v117, 4, v6
	v_or_b32_e32 v6, v115, v117
	ds_read_b128 v[34:37], v6
	ds_read_b128 v[38:41], v6 offset:4096
	s_waitcnt vmcnt(0) lgkmcnt(0)
	v_mfma_f32_32x32x16_f16 v[2:17], v[2:5], v[94:97], 0
	v_bitop3_b32 v42, v54, v46, 4 bitop3:0x36
	v_bitop3_b32 v46, v54, v46, 6 bitop3:0x36
	v_lshlrev_b32_e32 v118, 4, v42
	v_lshlrev_b32_e32 v119, 4, v46
	v_or_b32_e32 v42, v115, v118
	v_or_b32_e32 v56, v115, v119
	v_mfma_f32_32x32x16_f16 v[18:33], v[18:21], v[94:97], 0
	v_mfma_f32_32x32x16_f16 v[2:17], v[34:37], v[90:93], v[2:17]
	ds_read_b128 v[34:37], v42
	ds_read_b128 v[42:45], v42 offset:4096
	ds_read_b128 v[46:49], v56
	ds_read_b128 v[56:59], v56 offset:4096
	v_mfma_f32_32x32x16_f16 v[18:33], v[38:41], v[90:93], v[18:33]
	s_waitcnt lgkmcnt(3)
	v_mfma_f32_32x32x16_f16 v[2:17], v[34:37], v[86:89], v[2:17]
	s_waitcnt lgkmcnt(2)
	v_mfma_f32_32x32x16_f16 v[18:33], v[42:45], v[86:89], v[18:33]
	s_waitcnt lgkmcnt(1)
	v_mfma_f32_32x32x16_f16 v[2:17], v[46:49], v[82:85], v[2:17]
	s_waitcnt lgkmcnt(0)
	v_mfma_f32_32x32x16_f16 v[18:33], v[56:59], v[82:85], v[18:33]
	s_add_i32 m0, s22, 0x8000
	s_add_u32 s18, s18, 0x4000
	s_addc_u32 s19, s19, 0
	global_load_lds_dwordx4 v55, s[18:19]
	s_add_i32 m0, s22, 0x8400
	s_nop 0
	global_load_lds_dwordx4 v64, s[18:19]
	s_mov_b64 s[18:19], 0x100
	v_lshl_add_u64 v[34:35], v[60:61], 0, s[18:19]
	s_add_i32 m0, s22, 0xa000
	s_nop 0
	global_load_lds_dwordx4 v[34:35], off
	v_lshl_add_u64 v[34:35], v[62:63], 0, s[18:19]
	s_add_i32 m0, s22, 0xa400
	s_mov_b32 s18, 0x8000
	global_load_lds_dwordx4 v[34:35], off
	v_max3_f32 v34, v2, v3, v4
	v_max3_f32 v34, v34, v5, v6
	v_max3_f32 v34, v34, v7, v8
	v_max3_f32 v34, v34, v9, v10
	v_max3_f32 v34, v34, v11, v12
	v_max3_f32 v34, v34, v13, v14
	v_max3_f32 v34, v34, v15, v16
	v_max_f32 v34, v34, v17
	v_max3_f32 v35, v18, v19, v20
	v_max3_f32 v35, v35, v21, v22
	v_max3_f32 v35, v35, v23, v24
	v_max3_f32 v35, v35, v25, v26
	v_max3_f32 v35, v35, v27, v28
	v_max3_f32 v35, v35, v29, v30
	v_max3_f32 v35, v35, v31, v32
	v_max_f32 v35, v35, v33
	s_nop 0
	v_max3_f32 v34, v34, v35, v35
	s_nop 0
	v_mov_b32_e32 v35, v34
	s_nop 1
	v_permlane32_swap_b32_e32 v34, v35
	v_max3_f32 v47, v34, v35, v35
	s_nop 0
	v_sub_f32_e32 v10, v10, v47
	v_exp_f32_e32 v126, v10
	v_bitop3_b32 v10, v54, v50, 2 bitop3:0x36
	v_sub_f32_e32 v6, v6, v47
	v_lshlrev_b32_e32 v112, 4, v10
	v_sub_f32_e32 v2, v2, v47
	v_sub_f32_e32 v3, v3, v47
	v_sub_f32_e32 v4, v4, v47
	v_sub_f32_e32 v5, v5, v47
	v_sub_f32_e32 v7, v7, v47
	v_sub_f32_e32 v8, v8, v47
	v_sub_f32_e32 v9, v9, v47
	v_exp_f32_e32 v106, v6
	v_or_b32_e32 v6, v109, v110
	v_or_b32_e32 v10, v109, v112
	v_sub_f32_e32 v19, v19, v47
	v_sub_f32_e32 v20, v20, v47
	v_sub_f32_e32 v21, v21, v47
	v_sub_f32_e32 v22, v22, v47
	v_exp_f32_e32 v80, v2
	v_exp_f32_e32 v100, v3
	v_exp_f32_e32 v102, v4
	v_exp_f32_e32 v104, v5
	v_exp_f32_e32 v120, v7
	v_exp_f32_e32 v122, v8
	v_exp_f32_e32 v124, v9
	ds_read_b128 v[2:5], v6 offset:8192
	ds_read_b128 v[6:9], v6 offset:12288
	ds_read_b128 v[56:59], v10 offset:8192
	ds_read_b128 v[60:63], v10 offset:12288
	v_exp_f32_e32 v101, v19
	v_exp_f32_e32 v103, v20
	v_exp_f32_e32 v105, v21
	v_exp_f32_e32 v107, v22
	v_sub_f32_e32 v34, 0, v47
	v_mov_b32_e32 v35, v34
	v_mov_b32_e32 v36, v34
	v_mov_b32_e32 v37, v34
	v_mov_b32_e32 v38, v34
	v_mov_b32_e32 v39, v34
	v_mov_b32_e32 v40, v34
	v_mov_b32_e32 v41, v34
	v_mov_b32_e32 v42, v34
	v_mov_b32_e32 v43, v34
	v_mov_b32_e32 v44, v34
	v_mov_b32_e32 v45, v34
	v_mov_b32_e32 v46, v34
	v_sub_f32_e32 v18, v18, v47
	v_sub_f32_e32 v23, v23, v47
	v_sub_f32_e32 v24, v24, v47
	v_sub_f32_e32 v25, v25, v47
	v_sub_f32_e32 v26, v26, v47
	v_sub_f32_e32 v27, v27, v47
	v_sub_f32_e32 v28, v28, v47
	v_sub_f32_e32 v29, v29, v47
	v_sub_f32_e32 v30, v30, v47
	v_sub_f32_e32 v31, v31, v47
	v_sub_f32_e32 v32, v32, v47
	v_sub_f32_e32 v33, v33, v47
	v_sub_f32_e32 v11, v11, v47
	v_sub_f32_e32 v12, v12, v47
	v_sub_f32_e32 v13, v13, v47
	v_sub_f32_e32 v14, v14, v47
	v_sub_f32_e32 v15, v15, v47
	v_sub_f32_e32 v16, v16, v47
	v_sub_f32_e32 v17, v17, v47
	v_mov_b32_e32 v47, v34
	v_mov_b32_e32 v48, v34
	v_mov_b32_e32 v49, v34
	v_exp_f32_e32 v128, v11
	v_exp_f32_e32 v130, v12
	v_exp_f32_e32 v132, v13
	v_exp_f32_e32 v134, v14
	v_exp_f32_e32 v136, v15
	v_exp_f32_e32 v138, v16
	v_exp_f32_e32 v140, v17
	v_exp_f32_e32 v81, v18
	v_exp_f32_e32 v121, v23
	v_exp_f32_e32 v123, v24
	v_exp_f32_e32 v125, v25
	v_exp_f32_e32 v127, v26
	v_exp_f32_e32 v129, v27
	v_exp_f32_e32 v131, v28
	v_exp_f32_e32 v133, v29
	v_exp_f32_e32 v135, v30
	v_exp_f32_e32 v137, v31
	v_exp_f32_e32 v139, v32
	v_exp_f32_e32 v141, v33
	v_cvt_pk_f16_f32 v13, v122, v124
	v_cvt_pk_f16_f32 v12, v106, v120
	v_cvt_pk_f16_f32 v11, v102, v104
	v_cvt_pk_f16_f32 v10, v80, v100
	v_cvt_pk_f16_f32 v67, v138, v140
	v_cvt_pk_f16_f32 v66, v134, v136
	s_waitcnt lgkmcnt(0)
	v_mfma_f32_32x32x16_f16 v[18:33], v[2:5], v[10:13], 0
	v_cvt_pk_f16_f32 v65, v130, v132
	v_cvt_pk_f16_f32 v64, v126, v128
	v_bitop3_b32 v55, v54, v50, 4 bitop3:0x36
	v_bitop3_b32 v50, v54, v50, 6 bitop3:0x36
	v_lshlrev_b32_e32 v111, 4, v55
	v_lshlrev_b32_e32 v113, 4, v50
	v_or_b32_e32 v55, v109, v111
	v_mfma_f32_32x32x16_f16 v[2:17], v[6:9], v[10:13], 0
	v_or_b32_e32 v50, v109, v113
	v_mfma_f32_32x32x16_f16 v[18:33], v[56:59], v[64:67], v[18:33]
	ds_read_b128 v[56:59], v55 offset:8192
	ds_read_b128 v[68:71], v55 offset:12288
	ds_read_b128 v[72:75], v50 offset:8192
	ds_read_b128 v[76:79], v50 offset:12288
	v_mfma_f32_32x32x16_f16 v[2:17], v[60:63], v[64:67], v[2:17]
	v_add_f32_e64 v54, v80, 0
	v_add_f32_e64 v55, v81, 0
	v_cvt_pk_f16_f32 v63, v123, v125
	v_add_f32_e64 v54, v54, v100
	v_add_f32_e64 v55, v55, v101
	v_cvt_pk_f16_f32 v62, v107, v121
	v_add_f32_e32 v54, v54, v102
	v_add_f32_e32 v55, v55, v103
	v_cvt_pk_f16_f32 v61, v103, v105
	v_add_f32_e32 v54, v54, v104
	v_add_f32_e32 v55, v55, v105
	v_cvt_pk_f16_f32 v60, v81, v101
	v_add_f32_e32 v54, v54, v106
	v_add_f32_e32 v55, v55, v107
	v_cvt_pk_f16_f32 v67, v139, v141
	v_add_f32_e32 v54, v54, v120
	v_add_f32_e32 v55, v55, v121
	s_waitcnt lgkmcnt(0)
	v_mfma_f32_32x32x16_f16 v[18:33], v[56:59], v[60:63], v[18:33]
	v_add_f32_e64 v54, v54, v122
	v_add_f32_e64 v55, v55, v123
	v_cvt_pk_f16_f32 v66, v135, v137
	v_add_f32_e64 v54, v54, v124
	v_add_f32_e64 v55, v55, v125
	v_cvt_pk_f16_f32 v65, v131, v133
	v_add_f32_e32 v54, v54, v126
	v_add_f32_e32 v55, v55, v127
	v_cvt_pk_f16_f32 v64, v127, v129
	v_add_f32_e32 v54, v54, v128
	v_add_f32_e32 v55, v55, v129
	v_mfma_f32_32x32x16_f16 v[2:17], v[68:71], v[60:63], v[2:17]
	v_add_f32_e64 v54, v54, v130
	v_add_f32_e64 v55, v55, v131
	s_add_u32 s8, s8, s24
	v_add_f32_e64 v54, v54, v132
	v_add_f32_e64 v55, v55, v133
	s_addc_u32 s9, s9, 0
	v_add_f32_e32 v54, v54, v134
	v_add_f32_e32 v55, v55, v135
	s_mov_b64 s[26:27], 0x180
	v_add_f32_e32 v54, v54, v136
	v_add_f32_e32 v55, v55, v137
	v_mfma_f32_32x32x16_f16 v[18:33], v[72:75], v[64:67], v[18:33]
	v_add_f32_e64 v54, v54, v138
	v_add_f32_e64 v55, v55, v139
	v_add_f32_e64 v54, v54, v140
	v_add_f32_e64 v55, v55, v141
	v_add_f32_e32 v50, v54, v55
	v_add_f32_e32 v114, 0, v50
	v_lshlrev_b32_e32 v50, 12, v1
	v_lshl_or_b32 v56, s21, 16, v50
	v_mfma_f32_32x32x16_f16 v[2:17], v[76:79], v[64:67], v[2:17]
	v_or_b32_e32 v50, v56, v53
	v_lshl_add_u64 v[54:55], s[8:9], 0, v[50:51]
	v_or3_b32 v50, v56, v52, s18
	v_lshl_add_u64 v[100:101], v[54:55], 0, s[26:27]
	v_lshl_add_u64 v[54:55], s[8:9], 0, v[50:51]
	s_lshl_b32 s8, s20, 17
	v_lshl_or_b32 v56, v1, 7, s22
	s_add_u32 s6, s6, s8
	v_or_b32_e32 v50, v56, v53
	s_addc_u32 s7, s7, 0
	v_lshl_add_u64 v[102:103], v[54:55], 0, s[26:27]
	v_lshl_add_u64 v[54:55], s[6:7], 0, v[50:51]
	v_or3_b32 v50, v56, v52, s25
	s_mov_b64 s[8:9], 0x6000
	v_lshl_add_u64 v[50:51], s[6:7], 0, v[50:51]
	v_lshl_add_u64 v[104:105], v[54:55], 0, s[8:9]
	v_lshl_add_u64 v[106:107], v[50:51], 0, s[8:9]
	s_mov_b32 s8, 0x41000000
	s_mov_b32 s9, 1
	s_load_dwordx4 s[32:35], s[30:31], 0x8
	s_and_b32 s29, s28, 7
	s_lshr_b32 s40, s28, 3
	s_lshr_b32 s41, s40, 5
	s_lshl_b32 s41, s41, 3
	s_or_b32 s29, s41, s29
	s_and_b32 s40, s40, 1
	s_lshl_b32 s29, s29, 18
	s_lshl_b32 s41, s40, 17
	s_lshl_b32 s42, s40, 11
	s_add_i32 s41, s41, s29
	s_add_i32 s41, s41, 0x6000
	s_add_i32 s42, s42, s29
	s_add_i32 s42, s42, 0x180
	v_and_b32_e32 v145, 63, v0
	v_lshrrev_b32_e32 v146, 3, v145
	v_lshl_add_u32 v146, s21, 4, v146
	v_and_b32_e32 v145, 7, v145
	v_bfe_u32 v147, v146, 1, 3
	v_xor_b32_e32 v148, v145, v147
	v_xor_b32_e32 v147, 4, v148
	v_lshlrev_b32_e32 v148, 4, v148
	v_lshlrev_b32_e32 v147, 4, v147
	v_lshl_add_u32 v145, v146, 7, v148
	v_lshl_add_u32 v149, v146, 7, v147
	v_add_u32_e32 v149, 0x400, v149
	v_lshl_add_u32 v148, v146, 12, v148
	v_lshl_add_u32 v147, v146, 12, v147
	v_add_u32_e32 v147, 0x8000, v147
	s_waitcnt lgkmcnt(0)
	s_add_u32 s36, s32, s41
	s_addc_u32 s37, s33, 0
	s_add_u32 s38, s34, s42
	s_addc_u32 s39, s35, 0
.LBB3_1:
	s_waitcnt vmcnt(4)
	s_lshl_b32 s18, s23, 14
	s_barrier
	v_or_b32_e32 v132, s18, v115
	v_add_u32_e32 v54, v132, v116
	ds_read_b128 v[50:53], v54
	ds_read_b128 v[120:123], v54 offset:4096
	v_add_u32_e32 v54, v132, v117
	ds_read_b128 v[124:127], v54
	ds_read_b128 v[128:131], v54 offset:4096
	s_waitcnt lgkmcnt(0)
	s_setprio 1
	v_mfma_f32_32x32x16_f16 v[66:81], v[50:53], v[94:97], v[34:49]
	v_add_u32_e32 v136, v132, v119
	v_mfma_f32_32x32x16_f16 v[50:65], v[120:123], v[94:97], v[34:49]
	v_mfma_f32_32x32x16_f16 v[66:81], v[124:127], v[90:93], v[66:81]
	v_add_u32_e32 v124, v132, v118
	ds_read_b128 v[120:123], v124
	ds_read_b128 v[124:127], v124 offset:4096
	ds_read_b128 v[132:135], v136
	ds_read_b128 v[136:139], v136 offset:4096
	v_mfma_f32_32x32x16_f16 v[50:65], v[128:131], v[90:93], v[50:65]
	s_waitcnt lgkmcnt(0)
	v_mfma_f32_32x32x16_f16 v[66:81], v[120:123], v[86:89], v[66:81]
	v_mfma_f32_32x32x16_f16 v[50:65], v[124:127], v[86:89], v[50:65]
	v_mfma_f32_32x32x16_f16 v[66:81], v[132:135], v[82:85], v[66:81]
	v_mfma_f32_32x32x16_f16 v[50:65], v[136:139], v[82:85], v[50:65]
	s_setprio 0
	s_cmp_gt_u32 s9, 13
	s_mov_b64 s[6:7], -1
	s_cbranch_scc0 .LBB3_3
	s_sleep 1
	s_mov_b64 s[6:7], 0
.LBB3_3:
	s_andn2_b64 vcc, exec, s[6:7]
	s_cbranch_vccnz .LBB3_5
	s_add_i32 s6, s18, 0xffffc000
	s_cmp_lg_u32 s23, 0
	s_cselect_b32 s6, s6, 0x8000
	s_add_i32 s6, s22, s6
	s_mov_b32 m0, s6
	s_nop 0
	global_load_lds_dwordx4 v145, s[36:37]
	s_add_i32 m0, s6, 0x400
	s_nop 0
	global_load_lds_dwordx4 v149, s[36:37]
	s_add_i32 m0, s6, 0x2000
	s_nop 0
	global_load_lds_dwordx4 v148, s[38:39]
	s_add_i32 m0, s6, 0x2400
	s_nop 0
	global_load_lds_dwordx4 v147, s[38:39]
	s_add_u32 s36, s36, 0x2000
	s_addc_u32 s37, s37, 0
	s_add_u32 s38, s38, 0x80
	s_addc_u32 s39, s39, 0

.LBB3_6:
	v_exp_f32_e32 v140, v50
	v_exp_f32_e32 v141, v51
	v_exp_f32_e32 v142, v52
	v_exp_f32_e32 v136, v66
	v_exp_f32_e32 v143, v53
	v_exp_f32_e32 v137, v67
	v_add_f32_e32 v50, 0, v140
	v_exp_f32_e32 v138, v68
	v_add_f32_e32 v50, v50, v141
	v_exp_f32_e32 v139, v69
	v_add_f32_e32 v50, v50, v142
	v_exp_f32_e32 v120, v70
	v_add_f32_e32 v51, v50, v143
	v_exp_f32_e32 v121, v54
	v_add_f32_e32 v50, 0, v136
	v_exp_f32_e32 v122, v71
	v_exp_f32_e32 v123, v55
	v_add_f32_e32 v50, v50, v137
	v_exp_f32_e32 v124, v72
	v_exp_f32_e32 v125, v56
	v_add_f32_e32 v50, v50, v138
	v_exp_f32_e32 v126, v73
	v_exp_f32_e32 v127, v57
	v_add_f32_e32 v50, v50, v139
	v_exp_f32_e32 v74, v74
	v_exp_f32_e32 v128, v75
	v_exp_f32_e32 v75, v58
	v_add_f32_e32 v50, v50, v120
	v_add_f32_e32 v51, v51, v121
	v_exp_f32_e32 v129, v59
	v_add_f32_e32 v50, v50, v122
	v_add_f32_e32 v51, v51, v123
	v_exp_f32_e32 v76, v76
	v_exp_f32_e32 v130, v77
	v_exp_f32_e32 v77, v60
	v_add_f32_e32 v50, v50, v124
	v_add_f32_e32 v51, v51, v125
	v_exp_f32_e32 v131, v61
	v_add_f32_e32 v50, v50, v126
	v_add_f32_e32 v51, v51, v127
	v_exp_f32_e32 v78, v78
	v_exp_f32_e32 v132, v79
	v_exp_f32_e32 v79, v62
	v_add_f32_e32 v50, v50, v74
	v_add_f32_e32 v51, v51, v75
	v_exp_f32_e32 v133, v63
	v_add_f32_e32 v50, v50, v128
	v_add_f32_e32 v51, v51, v129
	v_add_u32_e32 v70, s18, v109
	v_add_f32_e32 v50, v50, v76
	v_add_f32_e32 v51, v51, v77
	v_exp_f32_e32 v80, v80
	v_exp_f32_e32 v134, v81
	v_exp_f32_e32 v81, v64
	v_add_f32_e32 v50, v50, v130
	v_add_f32_e32 v51, v51, v131
	v_add_u32_e32 v54, v70, v110
	v_add_u32_e32 v62, v70, v112
	v_exp_f32_e32 v135, v65
	v_add_f32_e32 v66, v50, v78
	v_add_f32_e32 v67, v51, v79
	ds_read_b128 v[50:53], v54 offset:8192
	ds_read_b128 v[54:57], v54 offset:12288
	ds_read_b128 v[58:61], v62 offset:8192
	ds_read_b128 v[62:65], v62 offset:12288
	s_add_i32 s9, s9, 1
	s_add_i32 s6, s23, 1
	v_add_f32_e32 v66, v66, v132
	v_add_f32_e32 v67, v67, v133
	s_cmp_lg_u32 s23, 2
	v_add_f32_e32 v66, v66, v80
	v_add_f32_e32 v67, v67, v81
	s_cselect_b32 s23, s6, 0
	v_add_f32_e32 v66, v66, v134
	v_add_f32_e32 v67, v67, v135
	s_nop 0
	v_add_f32_e32 v144, v66, v67
	v_cvt_pk_f16_f32 v69, v124, v126
	v_cvt_pk_f16_f32 v68, v120, v122
	v_cvt_pk_f16_f32 v67, v138, v139
	v_cvt_pk_f16_f32 v66, v136, v137
	s_waitcnt lgkmcnt(0)
	s_nop 0
	s_setprio 1
	v_mfma_f32_32x32x16_f16 v[18:33], v[50:53], v[66:69], v[18:33]
	v_cvt_pk_f16_f32 v53, v80, v134
	v_cvt_pk_f16_f32 v52, v78, v132
	v_cvt_pk_f16_f32 v51, v76, v130
	v_cvt_pk_f16_f32 v50, v74, v128
	v_mfma_f32_32x32x16_f16 v[2:17], v[54:57], v[66:69], v[2:17]
	s_nop 0
	v_mfma_f32_32x32x16_f16 v[18:33], v[58:61], v[50:53], v[18:33]
	v_add_u32_e32 v58, v70, v111
	v_add_u32_e32 v70, v70, v113
	ds_read_b128 v[54:57], v58 offset:8192
	ds_read_b128 v[58:61], v58 offset:12288
	ds_read_b128 v[66:69], v70 offset:8192
	ds_read_b128 v[70:73], v70 offset:12288
	v_mfma_f32_32x32x16_f16 v[2:17], v[62:65], v[50:53], v[2:17]
	v_cvt_pk_f16_f32 v53, v125, v127
	v_cvt_pk_f16_f32 v52, v121, v123
	v_cvt_pk_f16_f32 v51, v142, v143
	v_cvt_pk_f16_f32 v50, v140, v141
	v_add_f32_e32 v114, v114, v144
	s_waitcnt lgkmcnt(0)
	v_mfma_f32_32x32x16_f16 v[18:33], v[54:57], v[50:53], v[18:33]
	s_cmp_eq_u32 s9, 15
	v_mfma_f32_32x32x16_f16 v[2:17], v[58:61], v[50:53], v[2:17]
	v_cvt_pk_f16_f32 v53, v81, v135
	v_cvt_pk_f16_f32 v52, v79, v133
	v_cvt_pk_f16_f32 v51, v77, v131
	v_cvt_pk_f16_f32 v50, v75, v129
	s_nop 1
	v_mfma_f32_32x32x16_f16 v[18:33], v[66:69], v[50:53], v[18:33]
	v_mfma_f32_32x32x16_f16 v[2:17], v[70:73], v[50:53], v[2:17]
	s_setprio 0
	s_cbranch_scc0 .LBB3_1
	s_branch .LBB3_8

.LBB3_9:
	s_nop 1
	v_exp_f32_e32 v93, v50
	v_exp_f32_e32 v94, v51
	v_exp_f32_e32 v95, v52
	v_exp_f32_e32 v35, v66
	v_exp_f32_e32 v96, v53
	v_exp_f32_e32 v90, v67
	v_add_f32_e32 v36, 0, v93
	v_exp_f32_e32 v91, v68
	v_add_f32_e32 v36, v36, v94
	v_exp_f32_e32 v92, v69
	v_add_f32_e32 v36, v36, v95
	v_exp_f32_e32 v66, v70
	v_add_f32_e32 v37, v36, v96
	v_exp_f32_e32 v67, v54
	v_add_f32_e32 v36, 0, v35
	v_exp_f32_e32 v68, v71
	v_exp_f32_e32 v69, v55
	v_add_f32_e32 v36, v36, v90
	v_exp_f32_e32 v70, v72
	v_exp_f32_e32 v71, v56
	v_add_f32_e32 v36, v36, v91
	v_exp_f32_e32 v72, v73
	v_exp_f32_e32 v73, v57
	v_add_f32_e32 v36, v36, v92
	v_exp_f32_e32 v74, v74
	v_exp_f32_e32 v82, v75
	v_exp_f32_e32 v75, v58
	v_add_f32_e32 v36, v36, v66
	v_add_f32_e32 v37, v37, v67
	v_exp_f32_e32 v83, v59
	v_add_f32_e32 v36, v36, v68
	v_add_f32_e32 v37, v37, v69
	v_exp_f32_e32 v76, v76
	v_exp_f32_e32 v84, v77
	v_exp_f32_e32 v77, v60
	v_add_f32_e32 v36, v36, v70
	v_add_f32_e32 v37, v37, v71
	v_exp_f32_e32 v85, v61
	v_add_f32_e32 v36, v36, v72
	v_add_f32_e32 v37, v37, v73
	v_exp_f32_e32 v78, v78
	v_exp_f32_e32 v86, v79
	v_exp_f32_e32 v79, v62
	v_add_f32_e32 v36, v36, v74
	v_add_f32_e32 v37, v37, v75
	v_exp_f32_e32 v87, v63
	v_add_f32_e32 v36, v36, v82
	v_add_f32_e32 v37, v37, v83
	v_add_u32_e32 v56, s4, v109
	v_add_f32_e32 v36, v36, v76
	v_add_f32_e32 v37, v37, v77
	v_exp_f32_e32 v80, v80
	v_exp_f32_e32 v88, v81
	v_exp_f32_e32 v81, v64
	v_add_f32_e32 v36, v36, v84
	v_add_f32_e32 v37, v37, v85
	v_add_u32_e32 v40, v56, v110
	v_add_u32_e32 v48, v56, v112
	v_exp_f32_e32 v89, v65
	v_add_f32_e32 v52, v36, v78
	v_add_f32_e32 v53, v37, v79
	ds_read_b128 v[36:39], v40 offset:8192
	ds_read_b128 v[40:43], v40 offset:12288
	ds_read_b128 v[44:47], v48 offset:8192
	ds_read_b128 v[48:51], v48 offset:12288
	v_add_f32_e32 v52, v52, v86
	v_add_f32_e32 v53, v53, v87
	s_nop 0
	v_add_f32_e32 v52, v52, v80
	v_add_f32_e32 v53, v53, v81
	s_nop 0
	v_add_f32_e32 v52, v52, v88
	v_add_f32_e32 v53, v53, v89
	s_nop 0
	v_add_f32_e32 v60, v52, v53
	v_cvt_pk_f16_f32 v55, v70, v72
	v_cvt_pk_f16_f32 v54, v66, v68
	v_cvt_pk_f16_f32 v53, v91, v92
	v_cvt_pk_f16_f32 v52, v35, v90
	v_add_u32_e32 v35, v56, v111
	s_waitcnt lgkmcnt(0)
	v_mfma_f32_32x32x16_f16 v[18:33], v[36:39], v[52:55], v[18:33]
	v_cvt_pk_f16_f32 v39, v80, v88
	v_cvt_pk_f16_f32 v38, v78, v86
	v_cvt_pk_f16_f32 v37, v76, v84
	v_cvt_pk_f16_f32 v36, v74, v82
	v_mfma_f32_32x32x16_f16 v[2:17], v[40:43], v[52:55], v[2:17]
	s_nop 0
	v_mfma_f32_32x32x16_f16 v[18:33], v[44:47], v[36:39], v[18:33]
	ds_read_b128 v[40:43], v35 offset:8192
	ds_read_b128 v[44:47], v35 offset:12288
	v_add_u32_e32 v35, v56, v113
	ds_read_b128 v[52:55], v35 offset:8192
	ds_read_b128 v[56:59], v35 offset:12288
	v_mfma_f32_32x32x16_f16 v[2:17], v[48:51], v[36:39], v[2:17]
	v_cvt_pk_f16_f32 v39, v71, v73
	v_cvt_pk_f16_f32 v38, v67, v69
	v_cvt_pk_f16_f32 v37, v95, v96
	v_cvt_pk_f16_f32 v36, v93, v94
	v_add_f32_e32 v35, v114, v60
	v_cmp_gt_u32_e32 vcc, 32, v99
	s_waitcnt lgkmcnt(0)
	v_mfma_f32_32x32x16_f16 v[18:33], v[40:43], v[36:39], v[18:33]
	v_mov_b32_e32 v40, v35
	s_nop 1
	v_permlane32_swap_b32_e32 v35, v40
	v_add_f32_e32 v35, v35, v40
	v_mfma_f32_32x32x16_f16 v[2:17], v[44:47], v[36:39], v[2:17]
	v_cvt_pk_f16_f32 v39, v81, v89
	v_cvt_pk_f16_f32 v38, v79, v87
	v_cvt_pk_f16_f32 v37, v77, v85
	v_cvt_pk_f16_f32 v36, v75, v83
	s_nop 1
	v_mfma_f32_32x32x16_f16 v[18:33], v[52:55], v[36:39], v[18:33]
	v_mfma_f32_32x32x16_f16 v[2:17], v[56:59], v[36:39], v[2:17]
	s_and_saveexec_b64 s[4:5], vcc
	s_cbranch_execz .LBB3_11
	s_mul_i32 s6, s20, 24
	s_add_u32 s6, s6, s12
	s_addc_u32 s7, 0, s13
	s_lshl_b64 s[6:7], s[6:7], 14
	s_add_u32 s6, s0, s6
	s_addc_u32 s7, s1, s7
	s_lshl_b64 s[0:1], s[2:3], 3
	s_add_u32 s0, s6, s0
	v_xor_b32_e32 v34, 0x80000000, v34
	s_addc_u32 s1, s7, s1
	v_lshlrev_b32_e32 v36, 3, v98
	global_store_dwordx2 v36, v[34:35], s[0:1]

	.amdhsa_kernel _Z11attn_kernelPKDF16_S0_S0_PDF16_P15HIP_vector_typeIfLj2EE
		.amdhsa_group_segment_fixed_size 49152
		.amdhsa_private_segment_fixed_size 0
		.amdhsa_kernarg_size 40
		.amdhsa_user_sgpr_count 2
		.amdhsa_user_sgpr_dispatch_ptr 0
		.amdhsa_user_sgpr_queue_ptr 0
		.amdhsa_user_sgpr_kernarg_segment_ptr 1
		.amdhsa_user_sgpr_dispatch_id 0
		.amdhsa_user_sgpr_kernarg_preload_length 0
		.amdhsa_user_sgpr_kernarg_preload_offset 0
		.amdhsa_user_sgpr_private_segment_size 0
		.amdhsa_uses_dynamic_stack 0
		.amdhsa_enable_private_segment 0
		.amdhsa_system_sgpr_workgroup_id_x 1
		.amdhsa_system_sgpr_workgroup_id_y 0
		.amdhsa_system_sgpr_workgroup_id_z 0
		.amdhsa_system_sgpr_workgroup_info 0
		.amdhsa_system_vgpr_workitem_id 0
		.amdhsa_next_free_vgpr 150
		.amdhsa_next_free_sgpr 96
		.amdhsa_accum_offset 152
		.amdhsa_reserve_vcc 1
		.amdhsa_float_round_mode_32 0
		.amdhsa_float_round_mode_16_64 0
		.amdhsa_float_denorm_mode_32 3
		.amdhsa_float_denorm_mode_16_64 3
		.amdhsa_dx10_clamp 1
		.amdhsa_ieee_mode 1
		.amdhsa_fp16_overflow 0
		.amdhsa_tg_split 0
		.amdhsa_exception_fp_ieee_invalid_op 0
		.amdhsa_exception_fp_denorm_src 0
		.amdhsa_exception_fp_ieee_div_zero 0
		.amdhsa_exception_fp_ieee_overflow 0
		.amdhsa_exception_fp_ieee_underflow 0
		.amdhsa_exception_fp_ieee_inexact 0
		.amdhsa_exception_int_div_zero 0
	.end_amdhsa_kernel

amdhsa.kernels:
  - .agpr_count:     0
    .args:
      - .actual_access:  read_only
        .address_space:  global
        .offset:         0
        .size:           8
        .value_kind:     global_buffer
      - .actual_access:  read_only
        .address_space:  global
        .offset:         8
        .size:           8
        .value_kind:     global_buffer
      - .actual_access:  read_only
        .address_space:  global
        .offset:         16
        .size:           8
        .value_kind:     global_buffer
      - .actual_access:  read_only
        .address_space:  global
        .offset:         24
        .size:           8
        .value_kind:     global_buffer
      - .actual_access:  read_only
        .address_space:  global
        .offset:         32
        .size:           8
        .value_kind:     global_buffer
      - .actual_access:  read_only
        .address_space:  global
        .offset:         40
        .size:           8
        .value_kind:     global_buffer
      - .actual_access:  read_only
        .address_space:  global
        .offset:         48
        .size:           8
        .value_kind:     global_buffer
      - .actual_access:  write_only
        .address_space:  global
        .offset:         56
        .size:           8
        .value_kind:     global_buffer
      - .actual_access:  write_only
        .address_space:  global
        .offset:         64
        .size:           8
        .value_kind:     global_buffer
    .group_segment_fixed_size: 0
    .kernarg_segment_align: 8
    .kernarg_segment_size: 72
    .language:       OpenCL C
    .language_version:
      - 2
      - 0
    .max_flat_workgroup_size: 256
    .name:           _Z11prep_kernelPKfS0_S0_S0_S0_S0_S0_PDF16_S1_
    .private_segment_fixed_size: 0
    .sgpr_count:     21
    .sgpr_spill_count: 0
    .symbol:         _Z11prep_kernelPKfS0_S0_S0_S0_S0_S0_PDF16_S1_.kd
    .uniform_work_group_size: 1
    .uses_dynamic_stack: false
    .vgpr_count:     10
    .vgpr_spill_count: 0
    .wavefront_size: 64
  - .agpr_count:     0
    .args:
      - .address_space:  global
        .offset:         0
        .size:           8
        .value_kind:     global_buffer
      - .address_space:  global
        .offset:         8
        .size:           8
        .value_kind:     global_buffer
      - .actual_access:  read_only
        .address_space:  global
        .offset:         16
        .size:           8
        .value_kind:     global_buffer
      - .actual_access:  read_only
        .address_space:  global
        .offset:         24
        .size:           8
        .value_kind:     global_buffer
      - .actual_access:  read_only
        .address_space:  global
        .offset:         32
        .size:           8
        .value_kind:     global_buffer
      - .actual_access:  write_only
        .address_space:  global
        .offset:         40
        .size:           8
        .value_kind:     global_buffer
      - .actual_access:  write_only
        .address_space:  global
        .offset:         48
        .size:           8
        .value_kind:     global_buffer
      - .actual_access:  write_only
        .address_space:  global
        .offset:         56
        .size:           8
        .value_kind:     global_buffer
    .group_segment_fixed_size: 30720
    .kernarg_segment_align: 8
    .kernarg_segment_size: 64
    .language:       OpenCL C
    .language_version:
      - 2
      - 0
    .max_flat_workgroup_size: 768
    .name:           _Z15qkv_proj_kernelPKDF16_S0_PKfS2_S2_PDF16_S3_S3_
    .private_segment_fixed_size: 0
    .sgpr_count:     47
    .sgpr_spill_count: 0
    .symbol:         _Z15qkv_proj_kernelPKDF16_S0_PKfS2_S2_PDF16_S3_S3_.kd
    .uniform_work_group_size: 1
    .uses_dynamic_stack: false
    .vgpr_count:     156
    .vgpr_spill_count: 0
    .wavefront_size: 64
  - .agpr_count:     0
    .args:
      - .address_space:  global
        .offset:         0
        .size:           8
        .value_kind:     global_buffer
      - .address_space:  global
        .offset:         8
        .size:           8
        .value_kind:     global_buffer
      - .actual_access:  read_only
        .address_space:  global
        .offset:         16
        .size:           8
        .value_kind:     global_buffer
      - .actual_access:  write_only
        .address_space:  global
        .offset:         24
        .size:           8
        .value_kind:     global_buffer
    .group_segment_fixed_size: 30720
    .kernarg_segment_align: 8
    .kernarg_segment_size: 32
    .language:       OpenCL C
    .language_version:
      - 2
      - 0
    .max_flat_workgroup_size: 384
    .name:           _Z15out_proj_kernelPKDF16_S0_PKfPf
    .private_segment_fixed_size: 0
    .sgpr_count:     67
    .sgpr_spill_count: 0
    .symbol:         _Z15out_proj_kernelPKDF16_S0_PKfPf.kd
    .uniform_work_group_size: 1
    .uses_dynamic_stack: false
    .vgpr_count:     144
    .vgpr_spill_count: 0
    .wavefront_size: 64
  - .agpr_count:     0
    .args:
      - .actual_access:  read_only
        .address_space:  global
        .offset:         0
        .size:           8
        .value_kind:     global_buffer
      - .address_space:  global
        .offset:         8
        .size:           8
        .value_kind:     global_buffer
      - .address_space:  global
        .offset:         16
        .size:           8
        .value_kind:     global_buffer
      - .actual_access:  write_only
        .address_space:  global
        .offset:         24
        .size:           8
        .value_kind:     global_buffer
      - .actual_access:  write_only
        .address_space:  global
        .offset:         32
        .size:           8
        .value_kind:     global_buffer
    .group_segment_fixed_size: 49152
    .kernarg_segment_align: 8
    .kernarg_segment_size: 40
    .language:       OpenCL C
    .language_version:
      - 2
      - 0
    .max_flat_workgroup_size: 256
    .name:           _Z11attn_kernelPKDF16_S0_S0_PDF16_P15HIP_vector_typeIfLj2EE
    .private_segment_fixed_size: 0
    .sgpr_count:     34
    .sgpr_spill_count: 0
    .symbol:         _Z11attn_kernelPKDF16_S0_S0_PDF16_P15HIP_vector_typeIfLj2EE.kd
    .uniform_work_group_size: 1
    .uses_dynamic_stack: false
    .vgpr_count:     150
    .vgpr_spill_count: 0
    .wavefront_size: 64
  - .agpr_count:     0
    .args:
      - .actual_access:  read_only
        .address_space:  global
        .offset:         0
        .size:           8
        .value_kind:     global_buffer
      - .actual_access:  read_only
        .address_space:  global
        .offset:         8
        .size:           8
        .value_kind:     global_buffer
      - .actual_access:  write_only
        .address_space:  global
        .offset:         16
        .size:           8
        .value_kind:     global_buffer
    .group_segment_fixed_size: 0
    .kernarg_segment_align: 8
    .kernarg_segment_size: 24
    .language:       OpenCL C
    .language_version:
      - 2
      - 0
    .max_flat_workgroup_size: 256
    .name:           _Z14combine_kernelPKDF16_PK15HIP_vector_typeIfLj2EEPDF16_
    .private_segment_fixed_size: 0
    .sgpr_count:     16
    .sgpr_spill_count: 0
    .symbol:         _Z14combine_kernelPKDF16_PK15HIP_vector_typeIfLj2EEPDF16_.kd
    .uniform_work_group_size: 1
    .uses_dynamic_stack: false
    .vgpr_count:     44
    .vgpr_spill_count: 0
    .wavefront_size: 64
